# GEMM epilogues (SwiGLU, QKV, rotary, gate): the eight per-row scale reads of a unit batched at the epilogue start instead of one LDS round trip per 16-row block
# speedup vs baseline: 1.0059x; 1.0059x over previous
; __device__ __forceinline__ unsigned cvt_pk_bf16(float lo, float hi) { unsigned r; asm volatile("v_cvt_pk_bf16_f32 %0, %1, %2" : "=v"(r) : "v"(lo), "v"(hi)); return r; }
;     __device__ __forceinline__ void operator()(const f32x4 (&acc)[2][2][4][2], const Unit& u, int wr, int wc, int fr, int fq) const {
;     ...
;             for (int q = 0; q < 8; ++q) { const int j = wc * 32 + 8 * fq + q; invf[q] = __builtin_amdgcn_exp2f(-(float)j * (13.287712379549449f / 127.0f)) * 0.15915494309189535f; }
; #pragma unroll
;             for (int ai = 0; ai < 2; ++ai)
; #pragma unroll
;                 for (int m = 0; m < 4; ++m) { const int row = row0 + ai * HALF + m * 16; const float pos = (float)(row & 2047), r = tab[u.idx * 256 + (row & 255)] * osc;
;                     bf16_t* rowp = O + (size_t)row * ldc + col0;
;                     float o1[8], o2[8];
; #pragma unroll
;                     for (int n = 0; n < 2; ++n)
; #pragma unroll
;                         for (int e = 0; e < 4; ++e) { const int q = n * 4 + e; float t = pos * invf[q]; t = __builtin_amdgcn_fractf(t);
;                             const float sn = __builtin_amdgcn_sinf(t), cs = __builtin_amdgcn_cosf(t);
;                             const float a = acc[ai][0][m][n][e], b = acc[ai][1][m][n][e];
;                             o1[q] = (a * cs - b * sn) * r; o2[q] = (a * sn + b * cs) * r; }
;                     u32x4 w; w.x = cvt_pk_bf16(o1[0], o1[1]); w.y = cvt_pk_bf16(o1[2], o1[3]); w.z = cvt_pk_bf16(o1[4], o1[5]); w.w = cvt_pk_bf16(o1[6], o1[7]);
;                     *(u32x4*)rowp = w;
;                     w.x = cvt_pk_bf16(o2[0], o2[1]); w.y = cvt_pk_bf16(o2[2], o2[3]); w.z = cvt_pk_bf16(o2[4], o2[5]); w.w = cvt_pk_bf16(o2[6], o2[7]);
;                     *(u32x4*)(rowp + HALF) = w; }
.LBB0_104:
	s_cmp_gt_i32 s0, 3
	s_cselect_b64 vcc, -1, 0
	v_mov_b32_e32 v144, 0x3d800000
	v_lshl_add_u32 v146, s52, 8, v148
	v_cndmask_b32_e32 v145, 1.0, v144, vcc
	v_and_b32_e32 v144, 0x7cf, v146
	v_lshl_or_b32 v162, s0, 8, v150
	v_cvt_f32_u32_e32 v161, v144
	s_lshl_b32 s0, s1, 10
	s_add_i32 s0, s0, 0
	s_add_i32 s0, s0, 0x20000
	v_lshl_add_u32 v144, v159, 2, s0
	ds_read_b32 v198, v144 offset:64
	ds_read_b32 v199, v144 offset:128
	ds_read_b32 v200, v144 offset:192
	ds_read_b32 v201, v144 offset:512
	ds_read_b32 v202, v144 offset:576
	ds_read_b32 v203, v144 offset:640
	ds_read_b32 v204, v144 offset:704
	ds_read_b32 v165, v144
	v_mul_f32_e32 v144, v151, v161
	v_fract_f32_e32 v144, v144
	v_mov_b32_e32 v171, v124
	v_mul_f32_e32 v124, v152, v161
	v_sin_f32_e32 v169, v144
	v_cos_f32_e32 v168, v144
	v_fract_f32_e32 v124, v124
	v_sin_f32_e32 v177, v124
	v_cos_f32_e32 v176, v124
	v_mov_b32_e32 v170, v128
	v_mov_b32_e32 v174, v169
	v_mov_b32_e32 v175, v168
	v_pk_mul_f32 v[172:173], v[168:169], v[170:171]
	v_pk_mul_f32 v[168:169], v[174:175], v[170:171]
	v_mov_b32_e32 v124, v129
	v_mov_b32_e32 v170, v177
	v_mov_b32_e32 v171, v176
	v_pk_mul_f32 v[128:129], v[176:177], v[124:125]
	v_mul_f32_e32 v144, v153, v161
	v_pk_mul_f32 v[124:125], v[170:171], v[124:125]
	v_mov_b32_e32 v171, v126
	v_mul_f32_e32 v126, v154, v161
	v_fract_f32_e32 v144, v144
	v_fract_f32_e32 v126, v126
	v_sin_f32_e32 v175, v144
	v_cos_f32_e32 v174, v144
	v_sin_f32_e32 v181, v126
	v_cos_f32_e32 v180, v126
	v_mov_b32_e32 v170, v130
	v_pk_mul_f32 v[176:177], v[174:175], v[170:171]
	v_mov_b32_e32 v178, v175
	v_mov_b32_e32 v179, v174
	v_mov_b32_e32 v126, v131
	v_mov_b32_e32 v174, v181
	v_mov_b32_e32 v175, v180
	v_pk_mul_f32 v[130:131], v[180:181], v[126:127]
	v_mul_f32_e32 v144, v155, v161
	v_pk_mul_f32 v[126:127], v[174:175], v[126:127]
	v_mov_b32_e32 v175, v116
	v_mul_f32_e32 v116, v156, v161
	v_fract_f32_e32 v144, v144
	v_fract_f32_e32 v116, v116
	v_pk_mul_f32 v[170:171], v[178:179], v[170:171]
	v_sin_f32_e32 v179, v144
	v_cos_f32_e32 v178, v144
	v_sin_f32_e32 v185, v116
	v_cos_f32_e32 v184, v116
	v_ashrrev_i32_e32 v147, 31, v146
	v_mul_f32_e32 v144, v157, v161
	v_lshlrev_b64 v[166:167], 12, v[146:147]
	v_mov_b32_e32 v174, v120
	v_fract_f32_e32 v147, v144
	v_pk_mul_f32 v[180:181], v[178:179], v[174:175]
	v_mov_b32_e32 v182, v179
	v_mov_b32_e32 v183, v178
	v_mov_b32_e32 v116, v121
	v_mov_b32_e32 v178, v185
	v_mov_b32_e32 v179, v184
	v_cos_f32_e32 v144, v147
	v_pk_mul_f32 v[120:121], v[184:185], v[116:117]
	v_pk_mul_f32 v[116:117], v[178:179], v[116:117]
	v_sin_f32_e32 v178, v147
	v_mov_b32_e32 v164, v122
	s_waitcnt lgkmcnt(0)
	v_pk_mul_f32 v[164:165], v[144:145], v[164:165]
	v_add_f32_e32 v116, v116, v117
	v_sub_f32_e32 v128, v128, v129
	v_add_f32_e32 v129, v170, v171
	v_mul_f32_e32 v170, v116, v165
	v_fma_f32 v116, -v178, v118, v164
	v_mov_b32_e32 v117, v118
	v_mul_f32_e32 v118, v158, v161
	v_sub_f32_e32 v120, v120, v121
	v_fract_f32_e32 v118, v118
	v_add_f32_e32 v168, v168, v169
	v_mul_f32_e32 v169, v120, v165
	v_sin_f32_e32 v121, v118
	v_cos_f32_e32 v120, v118
	v_mul_f32_e32 v164, v116, v165
	v_mov_b32_e32 v179, v144
	v_mov_b32_e32 v116, v122
	v_pk_mul_f32 v[116:117], v[178:179], v[116:117]
	v_mov_b32_e32 v118, v123
	v_add_f32_e32 v116, v116, v117
	v_mul_f32_e32 v144, v116, v165
	v_pk_mul_f32 v[116:117], v[120:121], v[118:119]
	v_pk_mul_f32 v[174:175], v[182:183], v[174:175]
	v_sub_f32_e32 v116, v116, v117
	v_mul_f32_e32 v161, v116, v165
	v_mov_b32_e32 v116, v121
	v_mov_b32_e32 v117, v120
	v_pk_mul_f32 v[116:117], v[116:117], v[118:119]
	v_ashrrev_i32_e32 v163, 31, v162
	v_sub_f32_e32 v147, v172, v173
	v_add_f32_e32 v124, v124, v125
	v_sub_f32_e32 v125, v176, v177
	v_sub_f32_e32 v130, v130, v131
	v_add_f32_e32 v126, v126, v127
	v_sub_f32_e32 v127, v180, v181
	v_add_f32_e32 v131, v174, v175
	v_add_f32_e32 v116, v116, v117
	v_lshl_add_u64 v[166:167], s[8:9], 0, v[166:167]
	v_mul_f32_e32 v147, v147, v165
	v_mul_f32_e32 v168, v168, v165
	v_mul_f32_e32 v128, v128, v165
	v_mul_f32_e32 v124, v124, v165
	v_mul_f32_e32 v125, v125, v165
	v_mul_f32_e32 v129, v129, v165
	v_mul_f32_e32 v130, v130, v165
	v_mul_f32_e32 v126, v126, v165
	v_mul_f32_e32 v127, v127, v165
	v_mul_f32_e32 v131, v131, v165
	v_mul_f32_e32 v165, v116, v165
	v_lshlrev_b64 v[116:117], 1, v[162:163]
	v_lshl_add_u64 v[122:123], v[166:167], 0, v[116:117]
	v_cvt_pk_bf16_f32 v118, v147, v128
	v_cvt_pk_bf16_f32 v119, v125, v130
	v_cvt_pk_bf16_f32 v120, v127, v169
	v_cvt_pk_bf16_f32 v121, v164, v161
	global_store_dwordx4 v[122:123], v[118:121], off
	s_movk_i32 s1, 0x7df
	v_mov_b32_e32 v125, v108
	v_cvt_pk_bf16_f32 v118, v168, v124
	v_cvt_pk_bf16_f32 v119, v129, v126
	v_cvt_pk_bf16_f32 v120, v131, v170
	v_cvt_pk_bf16_f32 v121, v144, v165
	global_store_dwordx4 v[122:123], v[118:121], off offset:256
	v_mov_b32_e32 v124, v112
	s_movk_i32 s71, 0xdf
	v_bitop3_b32 v119, v146, s1, 16 bitop3:0xc8
	v_cvt_f32_u32_e32 v147, v119
	v_bitop3_b32 v119, v146, s71, 16 bitop3:0xc8
	v_lshl_add_u32 v119, v119, 2, s0
	v_mov_b32_e32 v121, v198
	v_mul_f32_e32 v120, v151, v147
	v_fract_f32_e32 v120, v120
	v_mul_f32_e32 v108, v152, v147
	v_sin_f32_e32 v123, v120
	v_cos_f32_e32 v122, v120
	v_fract_f32_e32 v108, v108
	v_sin_f32_e32 v131, v108
	v_cos_f32_e32 v130, v108
	v_mov_b32_e32 v128, v123
	v_mov_b32_e32 v129, v122
	v_pk_mul_f32 v[126:127], v[122:123], v[124:125]
	v_pk_mul_f32 v[122:123], v[128:129], v[124:125]
	v_mov_b32_e32 v108, v113
	v_mov_b32_e32 v124, v131
	v_mov_b32_e32 v125, v130
	v_pk_mul_f32 v[112:113], v[130:131], v[108:109]
	v_mul_f32_e32 v120, v153, v147
	v_pk_mul_f32 v[108:109], v[124:125], v[108:109]
	v_mov_b32_e32 v125, v110
	v_mul_f32_e32 v110, v154, v147
	v_fract_f32_e32 v120, v120
	v_fract_f32_e32 v110, v110
	v_sin_f32_e32 v129, v120
	v_cos_f32_e32 v128, v120
	v_sin_f32_e32 v165, v110
	v_cos_f32_e32 v164, v110
	v_mov_b32_e32 v124, v114
	v_pk_mul_f32 v[130:131], v[128:129], v[124:125]
	v_mov_b32_e32 v162, v129
	v_mov_b32_e32 v163, v128
	v_mov_b32_e32 v110, v115
	v_mov_b32_e32 v128, v165
	v_mov_b32_e32 v129, v164
	v_pk_mul_f32 v[114:115], v[164:165], v[110:111]
	v_mul_f32_e32 v120, v155, v147
	v_pk_mul_f32 v[110:111], v[128:129], v[110:111]
	v_mov_b32_e32 v129, v100
	v_mul_f32_e32 v100, v156, v147
	v_fract_f32_e32 v120, v120
	v_fract_f32_e32 v100, v100
	v_pk_mul_f32 v[124:125], v[162:163], v[124:125]
	v_sin_f32_e32 v163, v120
	v_cos_f32_e32 v162, v120
	v_sin_f32_e32 v169, v100
	v_cos_f32_e32 v168, v100
	v_mul_f32_e32 v120, v157, v147
	v_mov_b32_e32 v128, v104
	v_fract_f32_e32 v120, v120
	v_pk_mul_f32 v[164:165], v[162:163], v[128:129]
	v_mov_b32_e32 v166, v163
	v_mov_b32_e32 v167, v162
	v_mov_b32_e32 v100, v105
	v_mov_b32_e32 v162, v169
	v_mov_b32_e32 v163, v168
	v_cos_f32_e32 v144, v120
	v_pk_mul_f32 v[104:105], v[168:169], v[100:101]
	v_pk_mul_f32 v[100:101], v[162:163], v[100:101]
	v_sin_f32_e32 v162, v120
	v_mov_b32_e32 v120, v106
	s_waitcnt lgkmcnt(0)
; __device__ __forceinline__ unsigned cvt_pk_bf16(float lo, float hi) { unsigned r; asm volatile("v_cvt_pk_bf16_f32 %0, %1, %2" : "=v"(r) : "v"(lo), "v"(hi)); return r; }
;     __device__ __forceinline__ void operator()(const f32x4 (&acc)[2][2][4][2], const Unit& u, int wr, int wc, int fr, int fq) const {
;     ...
;             for (int ai = 0; ai < 2; ++ai)
; #pragma unroll
;                 for (int m = 0; m < 4; ++m) { const int row = row0 + ai * HALF + m * 16; const float pos = (float)(row & 2047), r = tab[u.idx * 256 + (row & 255)] * osc;
;                     bf16_t* rowp = O + (size_t)row * ldc + col0;
;                     float o1[8], o2[8];
; #pragma unroll
;                     for (int n = 0; n < 2; ++n)
; #pragma unroll
;                         for (int e = 0; e < 4; ++e) { const int q = n * 4 + e; float t = pos * invf[q]; t = __builtin_amdgcn_fractf(t);
;                             const float sn = __builtin_amdgcn_sinf(t), cs = __builtin_amdgcn_cosf(t);
;                             const float a = acc[ai][0][m][n][e], b = acc[ai][1][m][n][e];
;                             o1[q] = (a * cs - b * sn) * r; o2[q] = (a * sn + b * cs) * r; }
;                     u32x4 w; w.x = cvt_pk_bf16(o1[0], o1[1]); w.y = cvt_pk_bf16(o1[2], o1[3]); w.z = cvt_pk_bf16(o1[4], o1[5]); w.w = cvt_pk_bf16(o1[6], o1[7]);
;                     *(u32x4*)rowp = w;
;                     w.x = cvt_pk_bf16(o2[0], o2[1]); w.y = cvt_pk_bf16(o2[2], o2[3]); w.z = cvt_pk_bf16(o2[4], o2[5]); w.w = cvt_pk_bf16(o2[6], o2[7]);
;                     *(u32x4*)(rowp + HALF) = w; }
	v_pk_mul_f32 v[120:121], v[144:145], v[120:121]
	v_add_f32_e32 v100, v100, v101
	v_sub_f32_e32 v112, v112, v113
	v_add_f32_e32 v113, v124, v125
	v_mul_f32_e32 v124, v100, v121
	v_fma_f32 v100, -v162, v102, v120
	v_mov_b32_e32 v101, v102
	v_mul_f32_e32 v102, v158, v147
	v_sub_f32_e32 v104, v104, v105
	v_fract_f32_e32 v102, v102
	v_add_f32_e32 v122, v122, v123
	v_mul_f32_e32 v123, v104, v121
	v_sin_f32_e32 v105, v102
	v_cos_f32_e32 v104, v102
	v_mul_f32_e32 v120, v100, v121
	v_mov_b32_e32 v163, v144
	v_mov_b32_e32 v100, v106
	v_pk_mul_f32 v[100:101], v[162:163], v[100:101]
	v_mov_b32_e32 v102, v107
	v_add_f32_e32 v100, v100, v101
	v_mul_f32_e32 v106, v100, v121
	v_pk_mul_f32 v[100:101], v[104:105], v[102:103]
	v_or_b32_e32 v118, 16, v146
	v_sub_f32_e32 v100, v100, v101
	v_ashrrev_i32_e32 v119, 31, v118
	v_mul_f32_e32 v107, v100, v121
	v_mov_b32_e32 v100, v105
	v_mov_b32_e32 v101, v104
	v_lshlrev_b64 v[118:119], 12, v[118:119]
	v_pk_mul_f32 v[128:129], v[166:167], v[128:129]
	v_pk_mul_f32 v[100:101], v[100:101], v[102:103]
	v_lshl_add_u64 v[118:119], s[8:9], 0, v[118:119]
	v_sub_f32_e32 v126, v126, v127
	v_add_f32_e32 v108, v108, v109
	v_sub_f32_e32 v109, v130, v131
	v_sub_f32_e32 v114, v114, v115
	v_add_f32_e32 v110, v110, v111
	v_sub_f32_e32 v111, v164, v165
	v_add_f32_e32 v115, v128, v129
	v_add_f32_e32 v100, v100, v101
	v_mul_f32_e32 v126, v126, v121
	v_mul_f32_e32 v122, v122, v121
	v_mul_f32_e32 v112, v112, v121
	v_mul_f32_e32 v108, v108, v121
	v_mul_f32_e32 v109, v109, v121
	v_mul_f32_e32 v113, v113, v121
	v_mul_f32_e32 v114, v114, v121
	v_mul_f32_e32 v110, v110, v121
	v_mul_f32_e32 v111, v111, v121
	v_mul_f32_e32 v115, v115, v121
	v_mul_f32_e32 v121, v100, v121
	v_lshl_add_u64 v[104:105], v[118:119], 0, v[116:117]
	v_cvt_pk_bf16_f32 v100, v126, v112
	v_cvt_pk_bf16_f32 v101, v109, v114
	v_cvt_pk_bf16_f32 v102, v111, v123
	v_cvt_pk_bf16_f32 v103, v120, v107
	global_store_dwordx4 v[104:105], v[100:103], off
	s_movk_i32 s1, 0x7ef
	v_mov_b32_e32 v107, v92
	v_cvt_pk_bf16_f32 v100, v122, v108
	v_cvt_pk_bf16_f32 v101, v113, v110
	v_cvt_pk_bf16_f32 v102, v115, v124
	v_cvt_pk_bf16_f32 v103, v106, v121
	global_store_dwordx4 v[104:105], v[100:103], off offset:256
	v_mov_b32_e32 v106, v96
	s_movk_i32 s70, 0xff
	v_bitop3_b32 v101, v146, s1, 32 bitop3:0xc8
	v_cvt_f32_u32_e32 v124, v101
	s_movk_i32 s1, 0xef
	v_bitop3_b32 v101, v146, s1, 32 bitop3:0xc8
	v_lshl_add_u32 v101, v101, 2, s0
	v_mul_f32_e32 v102, v151, v124
	v_fract_f32_e32 v102, v102
	v_mul_f32_e32 v92, v152, v124
	v_sin_f32_e32 v105, v102
	v_cos_f32_e32 v104, v102
	v_fract_f32_e32 v92, v92
	v_sin_f32_e32 v113, v92
	v_cos_f32_e32 v112, v92
	v_mov_b32_e32 v110, v105
	v_mov_b32_e32 v111, v104
	v_pk_mul_f32 v[108:109], v[104:105], v[106:107]
	v_pk_mul_f32 v[104:105], v[110:111], v[106:107]
	v_mov_b32_e32 v92, v97
	v_mov_b32_e32 v106, v113
	v_mov_b32_e32 v107, v112
	v_pk_mul_f32 v[96:97], v[112:113], v[92:93]
	v_mul_f32_e32 v102, v153, v124
	v_pk_mul_f32 v[92:93], v[106:107], v[92:93]
	v_mov_b32_e32 v107, v94
	v_mul_f32_e32 v94, v154, v124
	v_fract_f32_e32 v102, v102
	v_fract_f32_e32 v94, v94
	v_sin_f32_e32 v111, v102
	v_cos_f32_e32 v110, v102
	v_sin_f32_e32 v119, v94
	v_cos_f32_e32 v118, v94
	v_mov_b32_e32 v106, v98
	v_pk_mul_f32 v[112:113], v[110:111], v[106:107]
	v_mov_b32_e32 v114, v111
	v_mov_b32_e32 v115, v110
	v_mov_b32_e32 v94, v99
	v_mov_b32_e32 v110, v119
	v_mov_b32_e32 v111, v118
	v_pk_mul_f32 v[98:99], v[118:119], v[94:95]
	v_mul_f32_e32 v102, v155, v124
	v_pk_mul_f32 v[94:95], v[110:111], v[94:95]
	v_mov_b32_e32 v111, v84
	v_mul_f32_e32 v84, v156, v124
	v_fract_f32_e32 v102, v102
	v_fract_f32_e32 v84, v84
	v_pk_mul_f32 v[106:107], v[114:115], v[106:107]
	v_sin_f32_e32 v115, v102
	v_cos_f32_e32 v114, v102
	v_sin_f32_e32 v123, v84
	v_cos_f32_e32 v122, v84
	v_mul_f32_e32 v102, v157, v124
	v_mov_b32_e32 v103, v199
	v_mov_b32_e32 v110, v88
	v_fract_f32_e32 v102, v102
	v_pk_mul_f32 v[118:119], v[114:115], v[110:111]
	v_mov_b32_e32 v120, v115
	v_mov_b32_e32 v121, v114
	v_mov_b32_e32 v84, v89
	v_mov_b32_e32 v114, v123
	v_mov_b32_e32 v115, v122
	v_cos_f32_e32 v144, v102
	v_pk_mul_f32 v[88:89], v[122:123], v[84:85]
	v_pk_mul_f32 v[84:85], v[114:115], v[84:85]
	v_sin_f32_e32 v114, v102
	v_mov_b32_e32 v102, v90
	s_waitcnt lgkmcnt(0)
; __device__ __forceinline__ unsigned cvt_pk_bf16(float lo, float hi) { unsigned r; asm volatile("v_cvt_pk_bf16_f32 %0, %1, %2" : "=v"(r) : "v"(lo), "v"(hi)); return r; }
;     __device__ __forceinline__ void operator()(const f32x4 (&acc)[2][2][4][2], const Unit& u, int wr, int wc, int fr, int fq) const {
;     ...
;             for (int ai = 0; ai < 2; ++ai)
; #pragma unroll
;                 for (int m = 0; m < 4; ++m) { const int row = row0 + ai * HALF + m * 16; const float pos = (float)(row & 2047), r = tab[u.idx * 256 + (row & 255)] * osc;
;                     bf16_t* rowp = O + (size_t)row * ldc + col0;
;                     float o1[8], o2[8];
; #pragma unroll
;                     for (int n = 0; n < 2; ++n)
; #pragma unroll
;                         for (int e = 0; e < 4; ++e) { const int q = n * 4 + e; float t = pos * invf[q]; t = __builtin_amdgcn_fractf(t);
;                             const float sn = __builtin_amdgcn_sinf(t), cs = __builtin_amdgcn_cosf(t);
;                             const float a = acc[ai][0][m][n][e], b = acc[ai][1][m][n][e];
;                             o1[q] = (a * cs - b * sn) * r; o2[q] = (a * sn + b * cs) * r; }
;                     u32x4 w; w.x = cvt_pk_bf16(o1[0], o1[1]); w.y = cvt_pk_bf16(o1[2], o1[3]); w.z = cvt_pk_bf16(o1[4], o1[5]); w.w = cvt_pk_bf16(o1[6], o1[7]);
;                     *(u32x4*)rowp = w;
;                     w.x = cvt_pk_bf16(o2[0], o2[1]); w.y = cvt_pk_bf16(o2[2], o2[3]); w.z = cvt_pk_bf16(o2[4], o2[5]); w.w = cvt_pk_bf16(o2[6], o2[7]);
;                     *(u32x4*)(rowp + HALF) = w; }
	v_pk_mul_f32 v[102:103], v[144:145], v[102:103]
	v_add_f32_e32 v84, v84, v85
	v_sub_f32_e32 v96, v96, v97
	v_add_f32_e32 v97, v106, v107
	v_mul_f32_e32 v106, v84, v103
	v_fma_f32 v84, -v114, v86, v102
	v_mov_b32_e32 v85, v86
	v_mul_f32_e32 v86, v158, v124
	v_sub_f32_e32 v88, v88, v89
	v_fract_f32_e32 v86, v86
	v_add_f32_e32 v104, v104, v105
	v_mul_f32_e32 v105, v88, v103
	v_sin_f32_e32 v89, v86
	v_cos_f32_e32 v88, v86
	v_mul_f32_e32 v102, v84, v103
	v_mov_b32_e32 v115, v144
	v_mov_b32_e32 v84, v90
	v_pk_mul_f32 v[84:85], v[114:115], v[84:85]
	v_mov_b32_e32 v86, v91
	v_add_f32_e32 v84, v84, v85
	v_mul_f32_e32 v90, v84, v103
	v_pk_mul_f32 v[84:85], v[88:89], v[86:87]
	v_or_b32_e32 v100, 32, v146
	v_sub_f32_e32 v84, v84, v85
	v_ashrrev_i32_e32 v101, 31, v100
	v_mul_f32_e32 v91, v84, v103
	v_mov_b32_e32 v84, v89
	v_mov_b32_e32 v85, v88
	v_lshlrev_b64 v[100:101], 12, v[100:101]
	v_pk_mul_f32 v[110:111], v[120:121], v[110:111]
	v_pk_mul_f32 v[84:85], v[84:85], v[86:87]
	v_lshl_add_u64 v[100:101], s[8:9], 0, v[100:101]
	v_sub_f32_e32 v108, v108, v109
	v_add_f32_e32 v92, v92, v93
	v_sub_f32_e32 v93, v112, v113
	v_sub_f32_e32 v98, v98, v99
	v_add_f32_e32 v94, v94, v95
	v_sub_f32_e32 v95, v118, v119
	v_add_f32_e32 v99, v110, v111
	v_add_f32_e32 v84, v84, v85
	v_mul_f32_e32 v108, v108, v103
	v_mul_f32_e32 v104, v104, v103
	v_mul_f32_e32 v96, v96, v103
	v_mul_f32_e32 v92, v92, v103
	v_mul_f32_e32 v93, v93, v103
	v_mul_f32_e32 v97, v97, v103
	v_mul_f32_e32 v98, v98, v103
	v_mul_f32_e32 v94, v94, v103
	v_mul_f32_e32 v95, v95, v103
	v_mul_f32_e32 v99, v99, v103
	v_mul_f32_e32 v103, v84, v103
	v_lshl_add_u64 v[88:89], v[100:101], 0, v[116:117]
	v_cvt_pk_bf16_f32 v84, v108, v96
	v_cvt_pk_bf16_f32 v85, v93, v98
	v_cvt_pk_bf16_f32 v86, v95, v105
	v_cvt_pk_bf16_f32 v87, v102, v91
	global_store_dwordx4 v[88:89], v[84:87], off
	s_movk_i32 s1, 0x7ff
	v_mov_b32_e32 v91, v76
	v_cvt_pk_bf16_f32 v84, v104, v92
	v_cvt_pk_bf16_f32 v85, v97, v94
	v_cvt_pk_bf16_f32 v86, v99, v106
	v_cvt_pk_bf16_f32 v87, v90, v103
	global_store_dwordx4 v[88:89], v[84:87], off offset:256
	v_mov_b32_e32 v90, v80
	s_andn2_b64 vcc, exec, s[2:3]
	v_bitop3_b32 v85, v146, s1, 48 bitop3:0xc8
	v_cvt_f32_u32_e32 v106, v85
	v_bitop3_b32 v85, v146, s70, 48 bitop3:0xc8
	v_lshl_add_u32 v85, v85, 2, s0
	v_mov_b32_e32 v87, v200
	v_mul_f32_e32 v86, v151, v106
	v_fract_f32_e32 v86, v86
	v_mul_f32_e32 v76, v152, v106
	v_sin_f32_e32 v89, v86
	v_cos_f32_e32 v88, v86
	v_fract_f32_e32 v76, v76
	v_sin_f32_e32 v97, v76
	v_cos_f32_e32 v96, v76
	v_mov_b32_e32 v94, v89
	v_mov_b32_e32 v95, v88
	v_pk_mul_f32 v[92:93], v[88:89], v[90:91]
	v_pk_mul_f32 v[88:89], v[94:95], v[90:91]
	v_mov_b32_e32 v76, v81
	v_mov_b32_e32 v90, v97
	v_mov_b32_e32 v91, v96
	v_pk_mul_f32 v[80:81], v[96:97], v[76:77]
	v_mul_f32_e32 v86, v153, v106
	v_pk_mul_f32 v[76:77], v[90:91], v[76:77]
	v_mov_b32_e32 v91, v78
	v_mul_f32_e32 v78, v154, v106
	v_fract_f32_e32 v86, v86
	v_fract_f32_e32 v78, v78
	v_sin_f32_e32 v95, v86
	v_cos_f32_e32 v94, v86
	v_sin_f32_e32 v101, v78
	v_cos_f32_e32 v100, v78
	v_mov_b32_e32 v90, v82
	v_pk_mul_f32 v[96:97], v[94:95], v[90:91]
	v_mov_b32_e32 v98, v95
	v_mov_b32_e32 v99, v94
	v_mov_b32_e32 v78, v83
	v_mov_b32_e32 v94, v101
	v_mov_b32_e32 v95, v100
	v_pk_mul_f32 v[82:83], v[100:101], v[78:79]
	v_mul_f32_e32 v86, v155, v106
	v_pk_mul_f32 v[78:79], v[94:95], v[78:79]
	v_mov_b32_e32 v95, v68
	v_mul_f32_e32 v68, v156, v106
	v_fract_f32_e32 v86, v86
	v_fract_f32_e32 v68, v68
	v_pk_mul_f32 v[90:91], v[98:99], v[90:91]
	v_sin_f32_e32 v99, v86
	v_cos_f32_e32 v98, v86
	v_sin_f32_e32 v105, v68
	v_cos_f32_e32 v104, v68
	v_mul_f32_e32 v86, v157, v106
	v_mov_b32_e32 v94, v72
	v_fract_f32_e32 v86, v86
	v_pk_mul_f32 v[100:101], v[98:99], v[94:95]
	v_mov_b32_e32 v102, v99
	v_mov_b32_e32 v103, v98
	v_mov_b32_e32 v68, v73
	v_mov_b32_e32 v98, v105
	v_mov_b32_e32 v99, v104
	v_cos_f32_e32 v144, v86
	v_pk_mul_f32 v[72:73], v[104:105], v[68:69]
	v_pk_mul_f32 v[68:69], v[98:99], v[68:69]
	v_sin_f32_e32 v98, v86
	v_mov_b32_e32 v86, v74
	s_waitcnt lgkmcnt(0)
	v_pk_mul_f32 v[86:87], v[144:145], v[86:87]
	v_add_f32_e32 v68, v68, v69
	v_sub_f32_e32 v80, v80, v81
	v_add_f32_e32 v81, v90, v91
	v_mul_f32_e32 v90, v68, v87
	v_fma_f32 v68, -v98, v70, v86
	v_mov_b32_e32 v69, v70
	v_mul_f32_e32 v70, v158, v106
	v_sub_f32_e32 v72, v72, v73
	v_fract_f32_e32 v70, v70
	v_add_f32_e32 v88, v88, v89
	v_mul_f32_e32 v89, v72, v87
	v_sin_f32_e32 v73, v70
	v_cos_f32_e32 v72, v70
	v_mul_f32_e32 v86, v68, v87
	v_mov_b32_e32 v99, v144
	v_mov_b32_e32 v68, v74
	v_pk_mul_f32 v[68:69], v[98:99], v[68:69]
	v_mov_b32_e32 v70, v75
	v_add_f32_e32 v68, v68, v69
	v_mul_f32_e32 v74, v68, v87
	v_pk_mul_f32 v[68:69], v[72:73], v[70:71]
	v_or_b32_e32 v84, 48, v146
	v_sub_f32_e32 v68, v68, v69
	v_ashrrev_i32_e32 v85, 31, v84
	v_mul_f32_e32 v75, v68, v87
	v_mov_b32_e32 v68, v73
	v_mov_b32_e32 v69, v72
	v_lshlrev_b64 v[84:85], 12, v[84:85]
	v_pk_mul_f32 v[94:95], v[102:103], v[94:95]
	v_pk_mul_f32 v[68:69], v[68:69], v[70:71]
	v_lshl_add_u64 v[84:85], s[8:9], 0, v[84:85]
	v_sub_f32_e32 v92, v92, v93
	v_add_f32_e32 v76, v76, v77
	v_sub_f32_e32 v77, v96, v97
	v_sub_f32_e32 v82, v82, v83
	v_add_f32_e32 v78, v78, v79
	v_sub_f32_e32 v79, v100, v101
	v_add_f32_e32 v83, v94, v95
	v_add_f32_e32 v68, v68, v69
	v_mul_f32_e32 v92, v92, v87
	v_mul_f32_e32 v88, v88, v87
	v_mul_f32_e32 v80, v80, v87
	v_mul_f32_e32 v76, v76, v87
	v_mul_f32_e32 v77, v77, v87
	v_mul_f32_e32 v81, v81, v87
	v_mul_f32_e32 v82, v82, v87
	v_mul_f32_e32 v78, v78, v87
	v_mul_f32_e32 v79, v79, v87
	v_mul_f32_e32 v83, v83, v87
	v_mul_f32_e32 v87, v68, v87
	v_lshl_add_u64 v[72:73], v[84:85], 0, v[116:117]
; __device__ __forceinline__ unsigned cvt_pk_bf16(float lo, float hi) { unsigned r; asm volatile("v_cvt_pk_bf16_f32 %0, %1, %2" : "=v"(r) : "v"(lo), "v"(hi)); return r; }
;     __device__ __forceinline__ void operator()(const f32x4 (&acc)[2][2][4][2], const Unit& u, int wr, int wc, int fr, int fq) const {
;     ...
;             for (int ai = 0; ai < 2; ++ai)
; #pragma unroll
;                 for (int m = 0; m < 4; ++m) { const int row = row0 + ai * HALF + m * 16; const float pos = (float)(row & 2047), r = tab[u.idx * 256 + (row & 255)] * osc;
;                     bf16_t* rowp = O + (size_t)row * ldc + col0;
;                     float o1[8], o2[8];
; #pragma unroll
;                     for (int n = 0; n < 2; ++n)
; #pragma unroll
;                         for (int e = 0; e < 4; ++e) { const int q = n * 4 + e; float t = pos * invf[q]; t = __builtin_amdgcn_fractf(t);
;                             const float sn = __builtin_amdgcn_sinf(t), cs = __builtin_amdgcn_cosf(t);
;                             const float a = acc[ai][0][m][n][e], b = acc[ai][1][m][n][e];
;                             o1[q] = (a * cs - b * sn) * r; o2[q] = (a * sn + b * cs) * r; }
;                     u32x4 w; w.x = cvt_pk_bf16(o1[0], o1[1]); w.y = cvt_pk_bf16(o1[2], o1[3]); w.z = cvt_pk_bf16(o1[4], o1[5]); w.w = cvt_pk_bf16(o1[6], o1[7]);
;                     *(u32x4*)rowp = w;
;                     w.x = cvt_pk_bf16(o2[0], o2[1]); w.y = cvt_pk_bf16(o2[2], o2[3]); w.z = cvt_pk_bf16(o2[4], o2[5]); w.w = cvt_pk_bf16(o2[6], o2[7]);
;                     *(u32x4*)(rowp + HALF) = w; }
	v_cvt_pk_bf16_f32 v68, v92, v80
	v_cvt_pk_bf16_f32 v69, v77, v82
	v_cvt_pk_bf16_f32 v70, v79, v89
	v_cvt_pk_bf16_f32 v71, v86, v75
	global_store_dwordx4 v[72:73], v[68:71], off
	v_mov_b32_e32 v75, v60
	s_mov_b64 s[2:3], -1
	v_cvt_pk_bf16_f32 v68, v88, v76
	v_cvt_pk_bf16_f32 v69, v81, v78
	v_cvt_pk_bf16_f32 v70, v83, v90
	v_cvt_pk_bf16_f32 v71, v74, v87
	global_store_dwordx4 v[72:73], v[68:71], off offset:256
	v_mov_b32_e32 v74, v64
	s_nop 0
	v_add_u32_e32 v68, 0x80, v146
	v_and_b32_e32 v69, 0x7cf, v68
	v_cvt_f32_u32_e32 v90, v69
	v_and_b32_e32 v69, 0xcf, v68
	v_lshl_add_u32 v69, v69, 2, s0
	v_mov_b32_e32 v71, v201
	v_mul_f32_e32 v70, v151, v90
	v_fract_f32_e32 v70, v70
	v_mul_f32_e32 v60, v152, v90
	v_sin_f32_e32 v73, v70
	v_cos_f32_e32 v72, v70
	v_fract_f32_e32 v60, v60
	v_sin_f32_e32 v81, v60
	v_cos_f32_e32 v80, v60
	v_mov_b32_e32 v78, v73
	v_mov_b32_e32 v79, v72
	v_pk_mul_f32 v[76:77], v[72:73], v[74:75]
	v_pk_mul_f32 v[72:73], v[78:79], v[74:75]
	v_mov_b32_e32 v60, v65
	v_mov_b32_e32 v74, v81
	v_mov_b32_e32 v75, v80
	v_pk_mul_f32 v[64:65], v[80:81], v[60:61]
	v_mul_f32_e32 v70, v153, v90
	v_pk_mul_f32 v[60:61], v[74:75], v[60:61]
	v_mov_b32_e32 v75, v62
	v_mul_f32_e32 v62, v154, v90
	v_fract_f32_e32 v70, v70
	v_fract_f32_e32 v62, v62
	v_sin_f32_e32 v79, v70
	v_cos_f32_e32 v78, v70
	v_sin_f32_e32 v85, v62
	v_cos_f32_e32 v84, v62
	v_mov_b32_e32 v74, v66
	v_pk_mul_f32 v[80:81], v[78:79], v[74:75]
	v_mov_b32_e32 v82, v79
	v_mov_b32_e32 v83, v78
	v_mov_b32_e32 v62, v67
	v_mov_b32_e32 v78, v85
	v_mov_b32_e32 v79, v84
	v_pk_mul_f32 v[66:67], v[84:85], v[62:63]
	v_mul_f32_e32 v70, v155, v90
	v_pk_mul_f32 v[62:63], v[78:79], v[62:63]
	v_mov_b32_e32 v79, v52
	v_mul_f32_e32 v52, v156, v90
	v_fract_f32_e32 v70, v70
	v_fract_f32_e32 v52, v52
	v_pk_mul_f32 v[74:75], v[82:83], v[74:75]
	v_sin_f32_e32 v83, v70
	v_cos_f32_e32 v82, v70
	v_sin_f32_e32 v89, v52
	v_cos_f32_e32 v88, v52
	v_mul_f32_e32 v70, v157, v90
	v_mov_b32_e32 v78, v56
	v_fract_f32_e32 v70, v70
	v_pk_mul_f32 v[84:85], v[82:83], v[78:79]
	v_mov_b32_e32 v86, v83
	v_mov_b32_e32 v87, v82
	v_mov_b32_e32 v52, v57
	v_mov_b32_e32 v82, v89
	v_mov_b32_e32 v83, v88
	v_cos_f32_e32 v144, v70
	v_pk_mul_f32 v[56:57], v[88:89], v[52:53]
	v_pk_mul_f32 v[52:53], v[82:83], v[52:53]
	v_sin_f32_e32 v82, v70
	v_mov_b32_e32 v70, v58
	s_waitcnt lgkmcnt(0)
	v_pk_mul_f32 v[70:71], v[144:145], v[70:71]
	v_add_f32_e32 v52, v52, v53
	v_sub_f32_e32 v64, v64, v65
	v_add_f32_e32 v65, v74, v75
	v_mul_f32_e32 v74, v52, v71
	v_fma_f32 v52, -v82, v54, v70
	v_mov_b32_e32 v53, v54
	v_mul_f32_e32 v54, v158, v90
	v_sub_f32_e32 v56, v56, v57
	v_fract_f32_e32 v54, v54
	v_add_f32_e32 v72, v72, v73
	v_mul_f32_e32 v73, v56, v71
	v_sin_f32_e32 v57, v54
	v_cos_f32_e32 v56, v54
	v_mul_f32_e32 v70, v52, v71
	v_mov_b32_e32 v83, v144
	v_mov_b32_e32 v52, v58
	v_pk_mul_f32 v[52:53], v[82:83], v[52:53]
	v_mov_b32_e32 v54, v59
	v_add_f32_e32 v52, v52, v53
	v_mul_f32_e32 v58, v52, v71
	v_pk_mul_f32 v[52:53], v[56:57], v[54:55]
	v_ashrrev_i32_e32 v69, 31, v68
	v_sub_f32_e32 v52, v52, v53
	v_mul_f32_e32 v59, v52, v71
	v_mov_b32_e32 v52, v57
	v_mov_b32_e32 v53, v56
	v_lshlrev_b64 v[68:69], 12, v[68:69]
	v_pk_mul_f32 v[78:79], v[86:87], v[78:79]
	v_pk_mul_f32 v[52:53], v[52:53], v[54:55]
	v_lshl_add_u64 v[68:69], s[8:9], 0, v[68:69]
	v_sub_f32_e32 v76, v76, v77
	v_add_f32_e32 v60, v60, v61
	v_sub_f32_e32 v61, v80, v81
	v_sub_f32_e32 v66, v66, v67
	v_add_f32_e32 v62, v62, v63
	v_sub_f32_e32 v63, v84, v85
	v_add_f32_e32 v67, v78, v79
	v_add_f32_e32 v52, v52, v53
	v_mul_f32_e32 v76, v76, v71
	v_mul_f32_e32 v72, v72, v71
	v_mul_f32_e32 v64, v64, v71
	v_mul_f32_e32 v60, v60, v71
	v_mul_f32_e32 v61, v61, v71
	v_mul_f32_e32 v65, v65, v71
	v_mul_f32_e32 v66, v66, v71
	v_mul_f32_e32 v62, v62, v71
	v_mul_f32_e32 v63, v63, v71
	v_mul_f32_e32 v67, v67, v71
	v_mul_f32_e32 v71, v52, v71
	v_lshl_add_u64 v[56:57], v[68:69], 0, v[116:117]
	v_cvt_pk_bf16_f32 v52, v76, v64
	v_cvt_pk_bf16_f32 v53, v61, v66
	v_cvt_pk_bf16_f32 v54, v63, v73
	v_cvt_pk_bf16_f32 v55, v70, v59
	global_store_dwordx4 v[56:57], v[52:55], off
	v_mov_b32_e32 v59, v44
	s_nop 0
	v_cvt_pk_bf16_f32 v52, v72, v60
	v_cvt_pk_bf16_f32 v53, v65, v62
	v_cvt_pk_bf16_f32 v54, v67, v74
	v_cvt_pk_bf16_f32 v55, v58, v71
	global_store_dwordx4 v[56:57], v[52:55], off offset:256
	v_mov_b32_e32 v58, v48
	s_nop 0
	v_add_u32_e32 v52, 0x90, v146
	v_and_b32_e32 v53, 0x7df, v52
	v_cvt_f32_u32_e32 v74, v53
	v_and_b32_e32 v53, 0xdf, v52
	v_lshl_add_u32 v53, v53, 2, s0
	v_mov_b32_e32 v55, v202
	v_mul_f32_e32 v54, v151, v74
	v_fract_f32_e32 v54, v54
	v_mul_f32_e32 v44, v152, v74
	v_sin_f32_e32 v57, v54
	v_cos_f32_e32 v56, v54
	v_fract_f32_e32 v44, v44
	v_sin_f32_e32 v65, v44
	v_cos_f32_e32 v64, v44
	v_mov_b32_e32 v62, v57
	v_mov_b32_e32 v63, v56
	v_pk_mul_f32 v[60:61], v[56:57], v[58:59]
	v_pk_mul_f32 v[56:57], v[62:63], v[58:59]
	v_mov_b32_e32 v44, v49
	v_mov_b32_e32 v58, v65
	v_mov_b32_e32 v59, v64
	v_pk_mul_f32 v[48:49], v[64:65], v[44:45]
	v_mul_f32_e32 v54, v153, v74
	v_pk_mul_f32 v[44:45], v[58:59], v[44:45]
	v_mov_b32_e32 v59, v46
	v_mul_f32_e32 v46, v154, v74
	v_fract_f32_e32 v54, v54
	v_fract_f32_e32 v46, v46
	v_sin_f32_e32 v63, v54
	v_cos_f32_e32 v62, v54
	v_sin_f32_e32 v69, v46
	v_cos_f32_e32 v68, v46
	v_mov_b32_e32 v58, v50
	v_pk_mul_f32 v[64:65], v[62:63], v[58:59]
	v_mov_b32_e32 v66, v63
	v_mov_b32_e32 v67, v62
	v_mov_b32_e32 v46, v51
	v_mov_b32_e32 v62, v69
	v_mov_b32_e32 v63, v68
	v_pk_mul_f32 v[50:51], v[68:69], v[46:47]
	v_mul_f32_e32 v54, v155, v74
	v_pk_mul_f32 v[46:47], v[62:63], v[46:47]
	v_mov_b32_e32 v63, v36
	v_mul_f32_e32 v36, v156, v74
	v_fract_f32_e32 v54, v54
	v_fract_f32_e32 v36, v36
	v_pk_mul_f32 v[58:59], v[66:67], v[58:59]
	v_sin_f32_e32 v67, v54
	v_cos_f32_e32 v66, v54
	v_sin_f32_e32 v73, v36
	v_cos_f32_e32 v72, v36
	v_mul_f32_e32 v54, v157, v74
	v_mov_b32_e32 v62, v40
	v_fract_f32_e32 v54, v54
	v_pk_mul_f32 v[68:69], v[66:67], v[62:63]
	v_mov_b32_e32 v70, v67
	v_mov_b32_e32 v71, v66
	v_mov_b32_e32 v36, v41
	v_mov_b32_e32 v66, v73
	v_mov_b32_e32 v67, v72
	v_cos_f32_e32 v144, v54
	v_pk_mul_f32 v[40:41], v[72:73], v[36:37]
	v_pk_mul_f32 v[36:37], v[66:67], v[36:37]
	v_sin_f32_e32 v66, v54
	v_mov_b32_e32 v54, v42
	s_waitcnt lgkmcnt(0)
; __device__ __forceinline__ unsigned cvt_pk_bf16(float lo, float hi) { unsigned r; asm volatile("v_cvt_pk_bf16_f32 %0, %1, %2" : "=v"(r) : "v"(lo), "v"(hi)); return r; }
;     __device__ __forceinline__ void operator()(const f32x4 (&acc)[2][2][4][2], const Unit& u, int wr, int wc, int fr, int fq) const {
;     ...
;             for (int ai = 0; ai < 2; ++ai)
; #pragma unroll
;                 for (int m = 0; m < 4; ++m) { const int row = row0 + ai * HALF + m * 16; const float pos = (float)(row & 2047), r = tab[u.idx * 256 + (row & 255)] * osc;
;                     bf16_t* rowp = O + (size_t)row * ldc + col0;
;                     float o1[8], o2[8];
; #pragma unroll
;                     for (int n = 0; n < 2; ++n)
; #pragma unroll
;                         for (int e = 0; e < 4; ++e) { const int q = n * 4 + e; float t = pos * invf[q]; t = __builtin_amdgcn_fractf(t);
;                             const float sn = __builtin_amdgcn_sinf(t), cs = __builtin_amdgcn_cosf(t);
;                             const float a = acc[ai][0][m][n][e], b = acc[ai][1][m][n][e];
;                             o1[q] = (a * cs - b * sn) * r; o2[q] = (a * sn + b * cs) * r; }
;                     u32x4 w; w.x = cvt_pk_bf16(o1[0], o1[1]); w.y = cvt_pk_bf16(o1[2], o1[3]); w.z = cvt_pk_bf16(o1[4], o1[5]); w.w = cvt_pk_bf16(o1[6], o1[7]);
;                     *(u32x4*)rowp = w;
;                     w.x = cvt_pk_bf16(o2[0], o2[1]); w.y = cvt_pk_bf16(o2[2], o2[3]); w.z = cvt_pk_bf16(o2[4], o2[5]); w.w = cvt_pk_bf16(o2[6], o2[7]);
;                     *(u32x4*)(rowp + HALF) = w; }
	v_pk_mul_f32 v[54:55], v[144:145], v[54:55]
	v_add_f32_e32 v36, v36, v37
	v_sub_f32_e32 v48, v48, v49
	v_add_f32_e32 v49, v58, v59
	v_mul_f32_e32 v58, v36, v55
	v_fma_f32 v36, -v66, v38, v54
	v_mov_b32_e32 v37, v38
	v_mul_f32_e32 v38, v158, v74
	v_sub_f32_e32 v40, v40, v41
	v_fract_f32_e32 v38, v38
	v_add_f32_e32 v56, v56, v57
	v_mul_f32_e32 v57, v40, v55
	v_sin_f32_e32 v41, v38
	v_cos_f32_e32 v40, v38
	v_mul_f32_e32 v54, v36, v55
	v_mov_b32_e32 v67, v144
	v_mov_b32_e32 v36, v42
	v_pk_mul_f32 v[36:37], v[66:67], v[36:37]
	v_mov_b32_e32 v38, v43
	v_add_f32_e32 v36, v36, v37
	v_mul_f32_e32 v42, v36, v55
	v_pk_mul_f32 v[36:37], v[40:41], v[38:39]
	v_ashrrev_i32_e32 v53, 31, v52
	v_sub_f32_e32 v36, v36, v37
	v_mul_f32_e32 v43, v36, v55
	v_mov_b32_e32 v36, v41
	v_mov_b32_e32 v37, v40
	v_lshlrev_b64 v[52:53], 12, v[52:53]
	v_pk_mul_f32 v[62:63], v[70:71], v[62:63]
	v_pk_mul_f32 v[36:37], v[36:37], v[38:39]
	v_lshl_add_u64 v[52:53], s[8:9], 0, v[52:53]
	v_sub_f32_e32 v60, v60, v61
	v_add_f32_e32 v44, v44, v45
	v_sub_f32_e32 v45, v64, v65
	v_sub_f32_e32 v50, v50, v51
	v_add_f32_e32 v46, v46, v47
	v_sub_f32_e32 v47, v68, v69
	v_add_f32_e32 v51, v62, v63
	v_add_f32_e32 v36, v36, v37
	v_mul_f32_e32 v60, v60, v55
	v_mul_f32_e32 v56, v56, v55
	v_mul_f32_e32 v48, v48, v55
	v_mul_f32_e32 v44, v44, v55
	v_mul_f32_e32 v45, v45, v55
	v_mul_f32_e32 v49, v49, v55
	v_mul_f32_e32 v50, v50, v55
	v_mul_f32_e32 v46, v46, v55
	v_mul_f32_e32 v47, v47, v55
	v_mul_f32_e32 v51, v51, v55
	v_mul_f32_e32 v55, v36, v55
	v_lshl_add_u64 v[40:41], v[52:53], 0, v[116:117]
	v_cvt_pk_bf16_f32 v36, v60, v48
	v_cvt_pk_bf16_f32 v37, v45, v50
	v_cvt_pk_bf16_f32 v38, v47, v57
	v_cvt_pk_bf16_f32 v39, v54, v43
	global_store_dwordx4 v[40:41], v[36:39], off
	v_mov_b32_e32 v43, v28
	s_nop 0
	v_cvt_pk_bf16_f32 v36, v56, v44
	v_cvt_pk_bf16_f32 v37, v49, v46
	v_cvt_pk_bf16_f32 v38, v51, v58
	v_cvt_pk_bf16_f32 v39, v42, v55
	global_store_dwordx4 v[40:41], v[36:39], off offset:256
	v_mov_b32_e32 v42, v32
	s_nop 0
	v_add_u32_e32 v36, 0xa0, v146
	v_and_b32_e32 v37, 0x7ef, v36
	v_cvt_f32_u32_e32 v58, v37
	v_and_b32_e32 v37, 0xef, v36
	v_lshl_add_u32 v37, v37, 2, s0
	v_mov_b32_e32 v39, v203
	v_mul_f32_e32 v38, v151, v58
	v_fract_f32_e32 v38, v38
	v_mul_f32_e32 v28, v152, v58
	v_sin_f32_e32 v41, v38
	v_cos_f32_e32 v40, v38
	v_fract_f32_e32 v28, v28
	v_sin_f32_e32 v49, v28
	v_cos_f32_e32 v48, v28
	v_mov_b32_e32 v46, v41
	v_mov_b32_e32 v47, v40
	v_pk_mul_f32 v[44:45], v[40:41], v[42:43]
	v_pk_mul_f32 v[40:41], v[46:47], v[42:43]
	v_mov_b32_e32 v28, v33
	v_mov_b32_e32 v42, v49
	v_mov_b32_e32 v43, v48
	v_pk_mul_f32 v[32:33], v[48:49], v[28:29]
	v_mul_f32_e32 v38, v153, v58
	v_pk_mul_f32 v[28:29], v[42:43], v[28:29]
	v_mov_b32_e32 v43, v30
	v_mul_f32_e32 v30, v154, v58
	v_fract_f32_e32 v38, v38
	v_fract_f32_e32 v30, v30
	v_sin_f32_e32 v47, v38
	v_cos_f32_e32 v46, v38
	v_sin_f32_e32 v53, v30
	v_cos_f32_e32 v52, v30
	v_mov_b32_e32 v42, v34
	v_pk_mul_f32 v[48:49], v[46:47], v[42:43]
	v_mov_b32_e32 v50, v47
	v_mov_b32_e32 v51, v46
	v_mov_b32_e32 v30, v35
	v_mov_b32_e32 v46, v53
	v_mov_b32_e32 v47, v52
	v_pk_mul_f32 v[34:35], v[52:53], v[30:31]
	v_mul_f32_e32 v38, v155, v58
	v_pk_mul_f32 v[30:31], v[46:47], v[30:31]
	v_mov_b32_e32 v47, v20
	v_mul_f32_e32 v20, v156, v58
	v_fract_f32_e32 v38, v38
	v_fract_f32_e32 v20, v20
	v_pk_mul_f32 v[42:43], v[50:51], v[42:43]
	v_sin_f32_e32 v51, v38
	v_cos_f32_e32 v50, v38
	v_sin_f32_e32 v57, v20
	v_cos_f32_e32 v56, v20
	v_mul_f32_e32 v38, v157, v58
	v_mov_b32_e32 v46, v24
	v_fract_f32_e32 v38, v38
	v_pk_mul_f32 v[52:53], v[50:51], v[46:47]
	v_mov_b32_e32 v54, v51
	v_mov_b32_e32 v55, v50
	v_mov_b32_e32 v20, v25
	v_mov_b32_e32 v50, v57
	v_mov_b32_e32 v51, v56
	v_cos_f32_e32 v144, v38
	v_pk_mul_f32 v[24:25], v[56:57], v[20:21]
	v_pk_mul_f32 v[20:21], v[50:51], v[20:21]
	v_sin_f32_e32 v50, v38
	v_mov_b32_e32 v38, v26
	s_waitcnt lgkmcnt(0)
; __device__ __forceinline__ unsigned cvt_pk_bf16(float lo, float hi) { unsigned r; asm volatile("v_cvt_pk_bf16_f32 %0, %1, %2" : "=v"(r) : "v"(lo), "v"(hi)); return r; }
;     __device__ __forceinline__ void operator()(const f32x4 (&acc)[2][2][4][2], const Unit& u, int wr, int wc, int fr, int fq) const {
;     ...
;             for (int ai = 0; ai < 2; ++ai)
; #pragma unroll
;                 for (int m = 0; m < 4; ++m) { const int row = row0 + ai * HALF + m * 16; const float pos = (float)(row & 2047), r = tab[u.idx * 256 + (row & 255)] * osc;
;                     bf16_t* rowp = O + (size_t)row * ldc + col0;
;                     float o1[8], o2[8];
; #pragma unroll
;                     for (int n = 0; n < 2; ++n)
; #pragma unroll
;                         for (int e = 0; e < 4; ++e) { const int q = n * 4 + e; float t = pos * invf[q]; t = __builtin_amdgcn_fractf(t);
;                             const float sn = __builtin_amdgcn_sinf(t), cs = __builtin_amdgcn_cosf(t);
;                             const float a = acc[ai][0][m][n][e], b = acc[ai][1][m][n][e];
;                             o1[q] = (a * cs - b * sn) * r; o2[q] = (a * sn + b * cs) * r; }
;                     u32x4 w; w.x = cvt_pk_bf16(o1[0], o1[1]); w.y = cvt_pk_bf16(o1[2], o1[3]); w.z = cvt_pk_bf16(o1[4], o1[5]); w.w = cvt_pk_bf16(o1[6], o1[7]);
;                     *(u32x4*)rowp = w;
;                     w.x = cvt_pk_bf16(o2[0], o2[1]); w.y = cvt_pk_bf16(o2[2], o2[3]); w.z = cvt_pk_bf16(o2[4], o2[5]); w.w = cvt_pk_bf16(o2[6], o2[7]);
;                     *(u32x4*)(rowp + HALF) = w; }
	v_pk_mul_f32 v[38:39], v[144:145], v[38:39]
	v_add_f32_e32 v20, v20, v21
	v_sub_f32_e32 v32, v32, v33
	v_add_f32_e32 v33, v42, v43
	v_mul_f32_e32 v42, v20, v39
	v_fma_f32 v20, -v50, v22, v38
	v_mov_b32_e32 v21, v22
	v_mul_f32_e32 v22, v158, v58
	v_sub_f32_e32 v24, v24, v25
	v_fract_f32_e32 v22, v22
	v_add_f32_e32 v40, v40, v41
	v_mul_f32_e32 v41, v24, v39
	v_sin_f32_e32 v25, v22
	v_cos_f32_e32 v24, v22
	v_mul_f32_e32 v38, v20, v39
	v_mov_b32_e32 v51, v144
	v_mov_b32_e32 v20, v26
	v_pk_mul_f32 v[20:21], v[50:51], v[20:21]
	v_mov_b32_e32 v22, v27
	v_add_f32_e32 v20, v20, v21
	v_mul_f32_e32 v26, v20, v39
	v_pk_mul_f32 v[20:21], v[24:25], v[22:23]
	v_ashrrev_i32_e32 v37, 31, v36
	v_sub_f32_e32 v20, v20, v21
	v_mul_f32_e32 v27, v20, v39
	v_mov_b32_e32 v20, v25
	v_mov_b32_e32 v21, v24
	v_lshlrev_b64 v[36:37], 12, v[36:37]
	v_pk_mul_f32 v[46:47], v[54:55], v[46:47]
	v_pk_mul_f32 v[20:21], v[20:21], v[22:23]
	v_lshl_add_u64 v[36:37], s[8:9], 0, v[36:37]
	v_sub_f32_e32 v44, v44, v45
	v_add_f32_e32 v28, v28, v29
	v_sub_f32_e32 v29, v48, v49
	v_sub_f32_e32 v34, v34, v35
	v_add_f32_e32 v30, v30, v31
	v_sub_f32_e32 v31, v52, v53
	v_add_f32_e32 v35, v46, v47
	v_add_f32_e32 v20, v20, v21
	v_mul_f32_e32 v44, v44, v39
	v_mul_f32_e32 v40, v40, v39
	v_mul_f32_e32 v32, v32, v39
	v_mul_f32_e32 v28, v28, v39
	v_mul_f32_e32 v29, v29, v39
	v_mul_f32_e32 v33, v33, v39
	v_mul_f32_e32 v34, v34, v39
	v_mul_f32_e32 v30, v30, v39
	v_mul_f32_e32 v31, v31, v39
	v_mul_f32_e32 v35, v35, v39
	v_mul_f32_e32 v39, v20, v39
	v_lshl_add_u64 v[24:25], v[36:37], 0, v[116:117]
	v_cvt_pk_bf16_f32 v20, v44, v32
	v_cvt_pk_bf16_f32 v21, v29, v34
	v_cvt_pk_bf16_f32 v22, v31, v41
	v_cvt_pk_bf16_f32 v23, v38, v27
	global_store_dwordx4 v[24:25], v[20:23], off
	v_mov_b32_e32 v27, v12
	s_nop 0
	v_cvt_pk_bf16_f32 v20, v40, v28
	v_cvt_pk_bf16_f32 v21, v33, v30
	v_cvt_pk_bf16_f32 v22, v35, v42
	v_cvt_pk_bf16_f32 v23, v26, v39
	global_store_dwordx4 v[24:25], v[20:23], off offset:256
	v_mov_b32_e32 v26, v16
	s_nop 0
	v_add_u32_e32 v20, 0xb0, v146
	v_and_b32_e32 v21, 0x7ff, v20
	v_cvt_f32_u32_e32 v42, v21
	v_and_b32_e32 v21, 0xff, v20
	v_lshl_add_u32 v21, v21, 2, s0
	v_mov_b32_e32 v23, v204
	v_mul_f32_e32 v22, v151, v42
	v_fract_f32_e32 v22, v22
	v_mul_f32_e32 v12, v152, v42
	v_sin_f32_e32 v25, v22
	v_cos_f32_e32 v24, v22
	v_fract_f32_e32 v12, v12
	v_sin_f32_e32 v33, v12
	v_cos_f32_e32 v32, v12
	v_mov_b32_e32 v30, v25
	v_mov_b32_e32 v31, v24
	v_pk_mul_f32 v[28:29], v[24:25], v[26:27]
	v_pk_mul_f32 v[24:25], v[30:31], v[26:27]
	v_mov_b32_e32 v12, v17
	v_mov_b32_e32 v26, v33
	v_mov_b32_e32 v27, v32
	v_pk_mul_f32 v[16:17], v[32:33], v[12:13]
	v_mul_f32_e32 v22, v153, v42
	v_pk_mul_f32 v[12:13], v[26:27], v[12:13]
	v_mov_b32_e32 v27, v14
	v_mul_f32_e32 v14, v154, v42
	v_fract_f32_e32 v22, v22
	v_fract_f32_e32 v14, v14
	v_sin_f32_e32 v31, v22
	v_cos_f32_e32 v30, v22
	v_sin_f32_e32 v37, v14
	v_cos_f32_e32 v36, v14
	v_mov_b32_e32 v26, v18
	v_pk_mul_f32 v[32:33], v[30:31], v[26:27]
	v_mov_b32_e32 v34, v31
	v_mov_b32_e32 v35, v30
	v_mov_b32_e32 v14, v19
	v_mov_b32_e32 v30, v37
	v_mov_b32_e32 v31, v36
	v_pk_mul_f32 v[18:19], v[36:37], v[14:15]
	v_mul_f32_e32 v22, v155, v42
	v_pk_mul_f32 v[14:15], v[30:31], v[14:15]
	v_mov_b32_e32 v31, v4
	v_mul_f32_e32 v4, v156, v42
	v_fract_f32_e32 v22, v22
	v_fract_f32_e32 v4, v4
	v_pk_mul_f32 v[26:27], v[34:35], v[26:27]
	v_sin_f32_e32 v35, v22
	v_cos_f32_e32 v34, v22
	v_sin_f32_e32 v41, v4
	v_cos_f32_e32 v40, v4
	v_mul_f32_e32 v22, v157, v42
	v_mov_b32_e32 v30, v8
	v_fract_f32_e32 v22, v22
	v_pk_mul_f32 v[36:37], v[34:35], v[30:31]
	v_mov_b32_e32 v38, v35
	v_mov_b32_e32 v39, v34
	v_mov_b32_e32 v4, v9
	v_mov_b32_e32 v34, v41
	v_mov_b32_e32 v35, v40
	v_cos_f32_e32 v144, v22
	v_pk_mul_f32 v[8:9], v[40:41], v[4:5]
	v_pk_mul_f32 v[4:5], v[34:35], v[4:5]
	v_sin_f32_e32 v34, v22
	v_mov_b32_e32 v22, v10
	s_waitcnt lgkmcnt(0)
	v_pk_mul_f32 v[22:23], v[144:145], v[22:23]
	v_add_f32_e32 v4, v4, v5
	v_sub_f32_e32 v16, v16, v17
	v_add_f32_e32 v17, v26, v27
	v_mul_f32_e32 v26, v4, v23
	v_fma_f32 v4, -v34, v6, v22
	v_mov_b32_e32 v5, v6
	v_mul_f32_e32 v6, v158, v42
	v_sub_f32_e32 v8, v8, v9
	v_fract_f32_e32 v6, v6
	v_add_f32_e32 v24, v24, v25
	v_mul_f32_e32 v25, v8, v23
	v_sin_f32_e32 v9, v6
	v_cos_f32_e32 v8, v6
	v_mul_f32_e32 v22, v4, v23
	v_mov_b32_e32 v35, v144
	v_mov_b32_e32 v4, v10
	v_pk_mul_f32 v[4:5], v[34:35], v[4:5]
	v_mov_b32_e32 v6, v11
	v_add_f32_e32 v4, v4, v5
	v_mul_f32_e32 v10, v4, v23
	v_pk_mul_f32 v[4:5], v[8:9], v[6:7]
	v_ashrrev_i32_e32 v21, 31, v20
	v_sub_f32_e32 v4, v4, v5
	v_mul_f32_e32 v11, v4, v23
	v_mov_b32_e32 v4, v9
	v_mov_b32_e32 v5, v8
	v_lshlrev_b64 v[20:21], 12, v[20:21]
	v_pk_mul_f32 v[30:31], v[38:39], v[30:31]
	v_pk_mul_f32 v[4:5], v[4:5], v[6:7]
	v_lshl_add_u64 v[20:21], s[8:9], 0, v[20:21]
	v_sub_f32_e32 v28, v28, v29
	v_add_f32_e32 v12, v12, v13
	v_sub_f32_e32 v13, v32, v33
	v_sub_f32_e32 v18, v18, v19
	v_add_f32_e32 v14, v14, v15
	v_sub_f32_e32 v15, v36, v37
	v_add_f32_e32 v19, v30, v31
	v_add_f32_e32 v4, v4, v5
	v_mul_f32_e32 v28, v28, v23
	v_mul_f32_e32 v24, v24, v23
	v_mul_f32_e32 v16, v16, v23
	v_mul_f32_e32 v12, v12, v23
	v_mul_f32_e32 v13, v13, v23
	v_mul_f32_e32 v17, v17, v23
	v_mul_f32_e32 v18, v18, v23
	v_mul_f32_e32 v14, v14, v23
	v_mul_f32_e32 v15, v15, v23
	v_mul_f32_e32 v19, v19, v23
	v_mul_f32_e32 v23, v4, v23
	v_lshl_add_u64 v[8:9], v[20:21], 0, v[116:117]
	v_cvt_pk_bf16_f32 v4, v28, v16
	v_cvt_pk_bf16_f32 v5, v13, v18
	v_cvt_pk_bf16_f32 v6, v15, v25
	v_cvt_pk_bf16_f32 v7, v22, v11
	global_store_dwordx4 v[8:9], v[4:7], off
	s_nop 1
	v_cvt_pk_bf16_f32 v4, v24, v12
	v_cvt_pk_bf16_f32 v5, v17, v14
	v_cvt_pk_bf16_f32 v6, v19, v26
	v_cvt_pk_bf16_f32 v7, v10, v23
	global_store_dwordx4 v[8:9], v[4:7], off offset:256
	s_cbranch_vccnz .LBB0_93
	s_andn2_b64 vcc, exec, s[6:7]
	s_cbranch_vccnz .LBB0_92
	s_barrier
	s_branch .LBB0_92

; __device__ __forceinline__ unsigned cvt_pk_bf16(float lo, float hi) { unsigned r; asm volatile("v_cvt_pk_bf16_f32 %0, %1, %2" : "=v"(r) : "v"(lo), "v"(hi)); return r; }
;     __device__ __forceinline__ void operator()(const f32x4 (&acc)[2][2][4][2], const Unit& u, int wr, int wc, int fr, int fq) const {
;         const int row0 = u.pm * BM + wr * 64 + fr, col0 = u.pn * BM + wc * 32 + 8 * fq, dilm = (1 << ldil) - 1, lLs = 11 - ldil;
; #pragma unroll
;         for (int ai = 0; ai < 2; ++ai)
; #pragma unroll
;             for (int m = 0; m < 4; ++m) { const int row = row0 + ai * HALF + m * 16; const float r = tab[u.idx * 256 + (row & 255)];
;                 const int b = row >> 11, pos = row & 2047, rr = pos & dilm, t = pos >> ldil;
; #pragma unroll
;                 for (int bj = 0; bj < 2; ++bj) { const int c = col0 + bj * HALF, which = c >> 10, head = (c >> 6) & 15, d = c & 63;
;                     bf16_t* dst = O + (size_t)which * 32768 * 1024 + ((((size_t)(b * 16 + head) << ldil) | rr) << lLs | t) * 64 + d;
;                     const f32x4 v0 = acc[ai][bj][m][0] * r, v1 = acc[ai][bj][m][1] * r;
;                     u32x4 w; w.x = cvt_pk_bf16(v0[0], v0[1]); w.y = cvt_pk_bf16(v0[2], v0[3]); w.z = cvt_pk_bf16(v1[0], v1[1]); w.w = cvt_pk_bf16(v1[2], v1[3]);
;                     *(u32x4*)dst = w; } }
.LBB0_302:
	s_lshl_b32 s9, s45, 8
	s_or_b32 s9, s9, s54
	v_lshl_add_u32 v150, s44, 8, v146
	v_ashrrev_i32_e32 v151, 7, v150
	s_lshr_b32 s9, s9, 6
	v_and_b32_e32 v151, -16, v151
	s_and_b32 s11, s9, 13
	s_lshl_b32 s9, s63, 10
	s_add_i32 s9, s9, 0
	v_or_b32_e32 v154, s11, v151
	s_add_i32 s9, s9, 0x20000
	v_mov_b32_e32 v161, 0x7cf
	v_ashrrev_i32_e32 v155, 31, v154
	s_ashr_i32 s36, s45, 2
	v_lshl_add_u32 v152, v148, 2, s9
	v_bitop3_b32 v160, v150, s58, v161 bitop3:0x80
	v_lshlrev_b64 v[154:155], s51, v[154:155]
	s_ashr_i32 s37, s36, 31
	ds_read_b32 v198, v152 offset:64
	ds_read_b32 v199, v152 offset:128
	ds_read_b32 v200, v152 offset:192
	ds_read_b32 v201, v152 offset:512
	ds_read_b32 v202, v152 offset:576
	ds_read_b32 v203, v152 offset:640
	ds_read_b32 v204, v152 offset:704
	ds_read_b32 v152, v152
	v_and_b32_e32 v153, 0x7cf, v150
	v_or_b32_e32 v156, v154, v160
	v_mov_b32_e32 v157, v155
	s_lshl_b64 s[36:37], s[36:37], 26
	v_lshrrev_b32_e32 v153, s51, v153
	v_lshlrev_b64 v[156:157], s59, v[156:157]
	s_add_u32 s44, s49, s36
	v_or_b32_e32 v156, v156, v153
	s_addc_u32 s45, s50, s37
	v_lshlrev_b64 v[156:157], 7, v[156:157]
	v_lshl_add_u64 v[156:157], s[44:45], 0, v[156:157]
	v_lshl_add_u64 v[156:157], v[156:157], 0, v[2:3]
	s_waitcnt lgkmcnt(0)
	v_pk_mul_f32 v[128:129], v[128:129], v[152:153] op_sel_hi:[1,0]
	v_pk_mul_f32 v[158:159], v[126:127], v[152:153] op_sel_hi:[1,0]
	v_pk_mul_f32 v[126:127], v[124:125], v[152:153] op_sel_hi:[1,0]
	v_cvt_pk_bf16_f32 v124, v128, v129
	s_or_b32 s36, s11, 2
	v_pk_mul_f32 v[130:131], v[130:131], v[152:153] op_sel_hi:[1,0]
	v_pk_mul_f32 v[122:123], v[122:123], v[152:153] op_sel_hi:[1,0]
	v_cvt_pk_bf16_f32 v125, v130, v131
	v_cvt_pk_bf16_f32 v126, v126, v127
	v_cvt_pk_bf16_f32 v127, v158, v159
	global_store_dwordx4 v[156:157], v[124:127], off
	v_pk_mul_f32 v[120:121], v[120:121], v[152:153] op_sel_hi:[1,0]
	v_pk_mul_f32 v[128:129], v[118:119], v[152:153] op_sel_hi:[1,0]
	v_or_b32_e32 v124, s36, v151
	v_ashrrev_i32_e32 v125, 31, v124
	v_lshlrev_b64 v[124:125], s51, v[124:125]
	v_or_b32_e32 v126, v124, v160
	v_mov_b32_e32 v127, v125
	v_lshlrev_b64 v[126:127], s59, v[126:127]
	v_or_b32_e32 v126, v126, v153
	v_lshlrev_b64 v[126:127], 7, v[126:127]
	v_lshl_add_u64 v[126:127], s[44:45], 0, v[126:127]
	v_lshl_add_u64 v[126:127], v[126:127], 0, v[2:3]
	v_pk_mul_f32 v[118:119], v[116:117], v[152:153] op_sel_hi:[1,0]
	v_cvt_pk_bf16_f32 v116, v120, v121
	v_cvt_pk_bf16_f32 v117, v122, v123
	s_movk_i32 s16, 0x7df
	v_cvt_pk_bf16_f32 v118, v118, v119
	v_cvt_pk_bf16_f32 v119, v128, v129
	global_store_dwordx4 v[126:127], v[116:119], off
	v_mov_b32_e32 v123, 0x7df
	s_andn2_b64 vcc, exec, s[2:3]
	v_or_b32_e32 v117, 16, v150
	v_bitop3_b32 v116, v150, s71, 16 bitop3:0xc8
	v_lshl_add_u32 v116, v116, 2, s9
	v_bitop3_b32 v118, v150, s16, 16 bitop3:0xc8
	v_bitop3_b32 v117, v117, s58, v123 bitop3:0x80
	v_mov_b32_e32 v116, v198
	v_lshrrev_b32_e32 v122, s51, v118
	v_or_b32_e32 v118, v154, v117
	v_mov_b32_e32 v119, v155
	v_lshlrev_b64 v[118:119], s59, v[118:119]
	v_or_b32_e32 v118, v118, v122
	v_lshlrev_b64 v[118:119], 7, v[118:119]
	v_lshl_add_u64 v[118:119], s[44:45], 0, v[118:119]
	v_lshl_add_u64 v[118:119], v[118:119], 0, v[2:3]
	s_waitcnt lgkmcnt(0)
	v_pk_mul_f32 v[114:115], v[114:115], v[116:117] op_sel_hi:[1,0]
	v_pk_mul_f32 v[112:113], v[112:113], v[116:117] op_sel_hi:[1,0]
	v_pk_mul_f32 v[120:121], v[110:111], v[116:117] op_sel_hi:[1,0]
	v_pk_mul_f32 v[110:111], v[108:109], v[116:117] op_sel_hi:[1,0]
	v_cvt_pk_bf16_f32 v108, v112, v113
	v_cvt_pk_bf16_f32 v109, v114, v115
	v_pk_mul_f32 v[106:107], v[106:107], v[116:117] op_sel_hi:[1,0]
	v_cvt_pk_bf16_f32 v110, v110, v111
	v_cvt_pk_bf16_f32 v111, v120, v121
	global_store_dwordx4 v[118:119], v[108:111], off
	v_pk_mul_f32 v[104:105], v[104:105], v[116:117] op_sel_hi:[1,0]
	s_movk_i32 s16, 0xef
	v_or_b32_e32 v108, v124, v117
	v_mov_b32_e32 v109, v125
	v_lshlrev_b64 v[108:109], s59, v[108:109]
	v_or_b32_e32 v108, v108, v122
	v_lshlrev_b64 v[108:109], 7, v[108:109]
	v_lshl_add_u64 v[108:109], s[44:45], 0, v[108:109]
	v_lshl_add_u64 v[108:109], v[108:109], 0, v[2:3]
	v_pk_mul_f32 v[110:111], v[102:103], v[116:117] op_sel_hi:[1,0]
	v_pk_mul_f32 v[102:103], v[100:101], v[116:117] op_sel_hi:[1,0]
	v_cvt_pk_bf16_f32 v100, v104, v105
	v_cvt_pk_bf16_f32 v101, v106, v107
	v_mov_b32_e32 v107, 0x7ef
	v_cvt_pk_bf16_f32 v102, v102, v103
	v_cvt_pk_bf16_f32 v103, v110, v111
	global_store_dwordx4 v[108:109], v[100:103], off
	s_mov_b64 s[2:3], -1
	s_nop 0
	v_or_b32_e32 v101, 32, v150
	v_bitop3_b32 v100, v150, s16, 32 bitop3:0xc8
	s_movk_i32 s16, 0x7ef
	v_lshl_add_u32 v100, v100, 2, s9
	v_bitop3_b32 v102, v150, s16, 32 bitop3:0xc8
	v_bitop3_b32 v101, v101, s58, v107 bitop3:0x80
	v_mov_b32_e32 v100, v199
	v_lshrrev_b32_e32 v106, s51, v102
	v_or_b32_e32 v102, v154, v101
	v_mov_b32_e32 v103, v155
	v_lshlrev_b64 v[102:103], s59, v[102:103]
	v_or_b32_e32 v102, v102, v106
	v_lshlrev_b64 v[102:103], 7, v[102:103]
	v_lshl_add_u64 v[102:103], s[44:45], 0, v[102:103]
	v_lshl_add_u64 v[102:103], v[102:103], 0, v[2:3]
	s_waitcnt lgkmcnt(0)
; __device__ __forceinline__ unsigned cvt_pk_bf16(float lo, float hi) { unsigned r; asm volatile("v_cvt_pk_bf16_f32 %0, %1, %2" : "=v"(r) : "v"(lo), "v"(hi)); return r; }
;     __device__ __forceinline__ void operator()(const f32x4 (&acc)[2][2][4][2], const Unit& u, int wr, int wc, int fr, int fq) const {
;     ...
;         for (int ai = 0; ai < 2; ++ai)
; #pragma unroll
;             for (int m = 0; m < 4; ++m) { const int row = row0 + ai * HALF + m * 16; const float r = tab[u.idx * 256 + (row & 255)];
;                 const int b = row >> 11, pos = row & 2047, rr = pos & dilm, t = pos >> ldil;
; #pragma unroll
;                 for (int bj = 0; bj < 2; ++bj) { const int c = col0 + bj * HALF, which = c >> 10, head = (c >> 6) & 15, d = c & 63;
;                     bf16_t* dst = O + (size_t)which * 32768 * 1024 + ((((size_t)(b * 16 + head) << ldil) | rr) << lLs | t) * 64 + d;
;                     const f32x4 v0 = acc[ai][bj][m][0] * r, v1 = acc[ai][bj][m][1] * r;
;                     u32x4 w; w.x = cvt_pk_bf16(v0[0], v0[1]); w.y = cvt_pk_bf16(v0[2], v0[3]); w.z = cvt_pk_bf16(v1[0], v1[1]); w.w = cvt_pk_bf16(v1[2], v1[3]);
;                     *(u32x4*)dst = w; } }
	v_pk_mul_f32 v[98:99], v[98:99], v[100:101] op_sel_hi:[1,0]
	v_pk_mul_f32 v[96:97], v[96:97], v[100:101] op_sel_hi:[1,0]
	v_pk_mul_f32 v[104:105], v[94:95], v[100:101] op_sel_hi:[1,0]
	v_pk_mul_f32 v[94:95], v[92:93], v[100:101] op_sel_hi:[1,0]
	v_cvt_pk_bf16_f32 v92, v96, v97
	v_cvt_pk_bf16_f32 v93, v98, v99
	v_pk_mul_f32 v[90:91], v[90:91], v[100:101] op_sel_hi:[1,0]
	v_cvt_pk_bf16_f32 v94, v94, v95
	v_cvt_pk_bf16_f32 v95, v104, v105
	global_store_dwordx4 v[102:103], v[92:95], off
	v_pk_mul_f32 v[88:89], v[88:89], v[100:101] op_sel_hi:[1,0]
	s_movk_i32 s16, 0x7ff
	v_or_b32_e32 v92, v124, v101
	v_mov_b32_e32 v93, v125
	v_lshlrev_b64 v[92:93], s59, v[92:93]
	v_or_b32_e32 v92, v92, v106
	v_lshlrev_b64 v[92:93], 7, v[92:93]
	v_lshl_add_u64 v[92:93], s[44:45], 0, v[92:93]
	v_lshl_add_u64 v[92:93], v[92:93], 0, v[2:3]
	v_pk_mul_f32 v[94:95], v[86:87], v[100:101] op_sel_hi:[1,0]
	v_pk_mul_f32 v[86:87], v[84:85], v[100:101] op_sel_hi:[1,0]
	v_cvt_pk_bf16_f32 v84, v88, v89
	v_cvt_pk_bf16_f32 v85, v90, v91
	v_mov_b32_e32 v91, 0x7ff
	v_cvt_pk_bf16_f32 v86, v86, v87
	v_cvt_pk_bf16_f32 v87, v94, v95
	global_store_dwordx4 v[92:93], v[84:87], off
	s_nop 1
	v_or_b32_e32 v85, 48, v150
	v_bitop3_b32 v84, v150, s70, 48 bitop3:0xc8
	v_lshl_add_u32 v84, v84, 2, s9
	v_bitop3_b32 v85, v85, s58, v91 bitop3:0x80
	v_mov_b32_e32 v84, v200
	v_bitop3_b32 v86, v150, s16, 48 bitop3:0xc8
	v_or_b32_e32 v154, v154, v85
	v_lshrrev_b32_e32 v90, s51, v86
	v_lshlrev_b64 v[86:87], s59, v[154:155]
	v_or_b32_e32 v86, v86, v90
	v_lshlrev_b64 v[86:87], 7, v[86:87]
	v_lshl_add_u64 v[86:87], s[44:45], 0, v[86:87]
	v_lshl_add_u64 v[86:87], v[86:87], 0, v[2:3]
	s_waitcnt lgkmcnt(0)
	v_pk_mul_f32 v[82:83], v[82:83], v[84:85] op_sel_hi:[1,0]
	v_pk_mul_f32 v[80:81], v[80:81], v[84:85] op_sel_hi:[1,0]
	v_pk_mul_f32 v[88:89], v[78:79], v[84:85] op_sel_hi:[1,0]
	v_pk_mul_f32 v[78:79], v[76:77], v[84:85] op_sel_hi:[1,0]
	v_cvt_pk_bf16_f32 v76, v80, v81
	v_cvt_pk_bf16_f32 v77, v82, v83
	v_or_b32_e32 v124, v124, v85
	v_cvt_pk_bf16_f32 v78, v78, v79
	v_cvt_pk_bf16_f32 v79, v88, v89
	global_store_dwordx4 v[86:87], v[76:79], off
	v_pk_mul_f32 v[74:75], v[74:75], v[84:85] op_sel_hi:[1,0]
	v_pk_mul_f32 v[72:73], v[72:73], v[84:85] op_sel_hi:[1,0]
	v_lshlrev_b64 v[76:77], s59, v[124:125]
	v_or_b32_e32 v76, v76, v90
	v_lshlrev_b64 v[76:77], 7, v[76:77]
	v_lshl_add_u64 v[76:77], s[44:45], 0, v[76:77]
	v_lshl_add_u64 v[76:77], v[76:77], 0, v[2:3]
	v_pk_mul_f32 v[78:79], v[70:71], v[84:85] op_sel_hi:[1,0]
	v_pk_mul_f32 v[70:71], v[68:69], v[84:85] op_sel_hi:[1,0]
	v_cvt_pk_bf16_f32 v68, v72, v73
	v_cvt_pk_bf16_f32 v69, v74, v75
	s_nop 0
	v_cvt_pk_bf16_f32 v70, v70, v71
	v_cvt_pk_bf16_f32 v71, v78, v79
	global_store_dwordx4 v[76:77], v[68:71], off
	s_nop 1
	v_add_u32_e32 v69, 0x80, v150
	v_ashrrev_i32_e32 v68, 7, v69
	v_and_b32_e32 v76, -16, v68
	v_and_b32_e32 v70, 0x7cf, v69
	v_lshrrev_b32_e32 v77, s51, v70
	v_or_b32_e32 v70, s11, v76
	v_and_b32_e32 v68, 0xcf, v69
	v_ashrrev_i32_e32 v71, 31, v70
	v_lshl_add_u32 v68, v68, 2, s9
	v_bitop3_b32 v69, v69, s58, v161 bitop3:0x80
	v_lshlrev_b64 v[70:71], s51, v[70:71]
	v_mov_b32_e32 v68, v201
	v_or_b32_e32 v72, v70, v69
	v_mov_b32_e32 v73, v71
	v_lshlrev_b64 v[72:73], s59, v[72:73]
	v_or_b32_e32 v72, v72, v77
	v_lshlrev_b64 v[72:73], 7, v[72:73]
	v_lshl_add_u64 v[72:73], s[44:45], 0, v[72:73]
	v_lshl_add_u64 v[72:73], v[72:73], 0, v[2:3]
	s_waitcnt lgkmcnt(0)
	v_pk_mul_f32 v[64:65], v[64:65], v[68:69] op_sel_hi:[1,0]
	v_pk_mul_f32 v[74:75], v[62:63], v[68:69] op_sel_hi:[1,0]
	v_pk_mul_f32 v[62:63], v[60:61], v[68:69] op_sel_hi:[1,0]
	v_cvt_pk_bf16_f32 v60, v64, v65
	v_pk_mul_f32 v[66:67], v[66:67], v[68:69] op_sel_hi:[1,0]
	v_pk_mul_f32 v[58:59], v[58:59], v[68:69] op_sel_hi:[1,0]
	v_cvt_pk_bf16_f32 v61, v66, v67
	v_cvt_pk_bf16_f32 v62, v62, v63
	v_cvt_pk_bf16_f32 v63, v74, v75
	global_store_dwordx4 v[72:73], v[60:63], off
	v_pk_mul_f32 v[56:57], v[56:57], v[68:69] op_sel_hi:[1,0]
	v_pk_mul_f32 v[64:65], v[54:55], v[68:69] op_sel_hi:[1,0]
	v_or_b32_e32 v60, s36, v76
	v_ashrrev_i32_e32 v61, 31, v60
	v_lshlrev_b64 v[60:61], s51, v[60:61]
	v_or_b32_e32 v62, v60, v69
	v_mov_b32_e32 v63, v61
	v_lshlrev_b64 v[62:63], s59, v[62:63]
	v_or_b32_e32 v62, v62, v77
	v_lshlrev_b64 v[62:63], 7, v[62:63]
	v_lshl_add_u64 v[62:63], s[44:45], 0, v[62:63]
	v_lshl_add_u64 v[62:63], v[62:63], 0, v[2:3]
	v_pk_mul_f32 v[54:55], v[52:53], v[68:69] op_sel_hi:[1,0]
	v_cvt_pk_bf16_f32 v52, v56, v57
	v_cvt_pk_bf16_f32 v53, v58, v59
	s_nop 0
	v_cvt_pk_bf16_f32 v54, v54, v55
	v_cvt_pk_bf16_f32 v55, v64, v65
	global_store_dwordx4 v[62:63], v[52:55], off
	s_nop 1
	v_add_u32_e32 v53, 0x90, v150
	v_and_b32_e32 v52, 0xdf, v53
	v_lshl_add_u32 v52, v52, 2, s9
	v_and_b32_e32 v54, 0x7df, v53
	v_bitop3_b32 v53, v53, s58, v123 bitop3:0x80
	v_mov_b32_e32 v52, v202
	v_lshrrev_b32_e32 v58, s51, v54
	v_or_b32_e32 v54, v70, v53
	v_mov_b32_e32 v55, v71
	v_lshlrev_b64 v[54:55], s59, v[54:55]
	v_or_b32_e32 v54, v54, v58
	v_lshlrev_b64 v[54:55], 7, v[54:55]
	v_lshl_add_u64 v[54:55], s[44:45], 0, v[54:55]
	v_lshl_add_u64 v[54:55], v[54:55], 0, v[2:3]
	s_waitcnt lgkmcnt(0)
; __device__ __forceinline__ unsigned cvt_pk_bf16(float lo, float hi) { unsigned r; asm volatile("v_cvt_pk_bf16_f32 %0, %1, %2" : "=v"(r) : "v"(lo), "v"(hi)); return r; }
;     __device__ __forceinline__ void operator()(const f32x4 (&acc)[2][2][4][2], const Unit& u, int wr, int wc, int fr, int fq) const {
;     ...
;             for (int m = 0; m < 4; ++m) { const int row = row0 + ai * HALF + m * 16; const float r = tab[u.idx * 256 + (row & 255)];
;                 const int b = row >> 11, pos = row & 2047, rr = pos & dilm, t = pos >> ldil;
; #pragma unroll
;                 for (int bj = 0; bj < 2; ++bj) { const int c = col0 + bj * HALF, which = c >> 10, head = (c >> 6) & 15, d = c & 63;
;                     bf16_t* dst = O + (size_t)which * 32768 * 1024 + ((((size_t)(b * 16 + head) << ldil) | rr) << lLs | t) * 64 + d;
;                     const f32x4 v0 = acc[ai][bj][m][0] * r, v1 = acc[ai][bj][m][1] * r;
;                     u32x4 w; w.x = cvt_pk_bf16(v0[0], v0[1]); w.y = cvt_pk_bf16(v0[2], v0[3]); w.z = cvt_pk_bf16(v1[0], v1[1]); w.w = cvt_pk_bf16(v1[2], v1[3]);
;                     *(u32x4*)dst = w; } }
	v_pk_mul_f32 v[50:51], v[50:51], v[52:53] op_sel_hi:[1,0]
	v_pk_mul_f32 v[48:49], v[48:49], v[52:53] op_sel_hi:[1,0]
	v_pk_mul_f32 v[56:57], v[46:47], v[52:53] op_sel_hi:[1,0]
	v_pk_mul_f32 v[46:47], v[44:45], v[52:53] op_sel_hi:[1,0]
	v_cvt_pk_bf16_f32 v44, v48, v49
	v_cvt_pk_bf16_f32 v45, v50, v51
	v_pk_mul_f32 v[42:43], v[42:43], v[52:53] op_sel_hi:[1,0]
	v_cvt_pk_bf16_f32 v46, v46, v47
	v_cvt_pk_bf16_f32 v47, v56, v57
	global_store_dwordx4 v[54:55], v[44:47], off
	v_pk_mul_f32 v[40:41], v[40:41], v[52:53] op_sel_hi:[1,0]
	s_nop 0
	v_or_b32_e32 v44, v60, v53
	v_mov_b32_e32 v45, v61
	v_lshlrev_b64 v[44:45], s59, v[44:45]
	v_or_b32_e32 v44, v44, v58
	v_lshlrev_b64 v[44:45], 7, v[44:45]
	v_lshl_add_u64 v[44:45], s[44:45], 0, v[44:45]
	v_lshl_add_u64 v[44:45], v[44:45], 0, v[2:3]
	v_pk_mul_f32 v[46:47], v[38:39], v[52:53] op_sel_hi:[1,0]
	v_pk_mul_f32 v[38:39], v[36:37], v[52:53] op_sel_hi:[1,0]
	v_cvt_pk_bf16_f32 v36, v40, v41
	v_cvt_pk_bf16_f32 v37, v42, v43
	s_nop 0
	v_cvt_pk_bf16_f32 v38, v38, v39
	v_cvt_pk_bf16_f32 v39, v46, v47
	global_store_dwordx4 v[44:45], v[36:39], off
	s_nop 1
	v_add_u32_e32 v37, 0xa0, v150
	v_and_b32_e32 v36, 0xef, v37
	v_lshl_add_u32 v36, v36, 2, s9
	v_and_b32_e32 v38, 0x7ef, v37
	v_bitop3_b32 v37, v37, s58, v107 bitop3:0x80
	v_mov_b32_e32 v36, v203
	v_lshrrev_b32_e32 v42, s51, v38
	v_or_b32_e32 v38, v70, v37
	v_mov_b32_e32 v39, v71
	v_lshlrev_b64 v[38:39], s59, v[38:39]
	v_or_b32_e32 v38, v38, v42
	v_lshlrev_b64 v[38:39], 7, v[38:39]
	v_lshl_add_u64 v[38:39], s[44:45], 0, v[38:39]
	v_lshl_add_u64 v[38:39], v[38:39], 0, v[2:3]
	s_waitcnt lgkmcnt(0)
	v_pk_mul_f32 v[34:35], v[34:35], v[36:37] op_sel_hi:[1,0]
	v_pk_mul_f32 v[32:33], v[32:33], v[36:37] op_sel_hi:[1,0]
	v_pk_mul_f32 v[40:41], v[30:31], v[36:37] op_sel_hi:[1,0]
	v_pk_mul_f32 v[30:31], v[28:29], v[36:37] op_sel_hi:[1,0]
	v_cvt_pk_bf16_f32 v28, v32, v33
	v_cvt_pk_bf16_f32 v29, v34, v35
	v_pk_mul_f32 v[26:27], v[26:27], v[36:37] op_sel_hi:[1,0]
	v_cvt_pk_bf16_f32 v30, v30, v31
	v_cvt_pk_bf16_f32 v31, v40, v41
	global_store_dwordx4 v[38:39], v[28:31], off
	v_pk_mul_f32 v[24:25], v[24:25], v[36:37] op_sel_hi:[1,0]
	s_nop 0
	v_or_b32_e32 v28, v60, v37
	v_mov_b32_e32 v29, v61
	v_lshlrev_b64 v[28:29], s59, v[28:29]
	v_or_b32_e32 v28, v28, v42
	v_lshlrev_b64 v[28:29], 7, v[28:29]
	v_lshl_add_u64 v[28:29], s[44:45], 0, v[28:29]
	v_lshl_add_u64 v[28:29], v[28:29], 0, v[2:3]
	v_pk_mul_f32 v[30:31], v[22:23], v[36:37] op_sel_hi:[1,0]
	v_pk_mul_f32 v[22:23], v[20:21], v[36:37] op_sel_hi:[1,0]
	v_cvt_pk_bf16_f32 v20, v24, v25
	v_cvt_pk_bf16_f32 v21, v26, v27
	s_nop 0
	v_cvt_pk_bf16_f32 v22, v22, v23
	v_cvt_pk_bf16_f32 v23, v30, v31
	global_store_dwordx4 v[28:29], v[20:23], off
	s_nop 1
	v_add_u32_e32 v21, 0xb0, v150
	v_and_b32_e32 v20, 0xff, v21
	v_lshl_add_u32 v20, v20, 2, s9
	v_and_b32_e32 v22, 0x7ff, v21
	v_bitop3_b32 v21, v21, s58, v91 bitop3:0x80
	v_mov_b32_e32 v20, v204
	v_or_b32_e32 v70, v70, v21
	v_lshrrev_b32_e32 v26, s51, v22
	v_lshlrev_b64 v[22:23], s59, v[70:71]
	v_or_b32_e32 v22, v22, v26
	v_lshlrev_b64 v[22:23], 7, v[22:23]
	v_lshl_add_u64 v[22:23], s[44:45], 0, v[22:23]
	v_lshl_add_u64 v[22:23], v[22:23], 0, v[2:3]
	s_waitcnt lgkmcnt(0)
	v_pk_mul_f32 v[18:19], v[18:19], v[20:21] op_sel_hi:[1,0]
	v_pk_mul_f32 v[16:17], v[16:17], v[20:21] op_sel_hi:[1,0]
	v_pk_mul_f32 v[24:25], v[14:15], v[20:21] op_sel_hi:[1,0]
	v_pk_mul_f32 v[14:15], v[12:13], v[20:21] op_sel_hi:[1,0]
	v_cvt_pk_bf16_f32 v12, v16, v17
	v_cvt_pk_bf16_f32 v13, v18, v19
	v_or_b32_e32 v60, v60, v21
	v_cvt_pk_bf16_f32 v14, v14, v15
	v_cvt_pk_bf16_f32 v15, v24, v25
	global_store_dwordx4 v[22:23], v[12:15], off
	v_pk_mul_f32 v[10:11], v[10:11], v[20:21] op_sel_hi:[1,0]
	v_pk_mul_f32 v[8:9], v[8:9], v[20:21] op_sel_hi:[1,0]
	v_lshlrev_b64 v[12:13], s59, v[60:61]
	v_or_b32_e32 v12, v12, v26
	v_lshlrev_b64 v[12:13], 7, v[12:13]
	v_lshl_add_u64 v[12:13], s[44:45], 0, v[12:13]
	v_lshl_add_u64 v[12:13], v[12:13], 0, v[2:3]
	v_pk_mul_f32 v[14:15], v[6:7], v[20:21] op_sel_hi:[1,0]
	v_pk_mul_f32 v[6:7], v[4:5], v[20:21] op_sel_hi:[1,0]
	v_cvt_pk_bf16_f32 v4, v8, v9
	v_cvt_pk_bf16_f32 v5, v10, v11
	s_nop 0
	v_cvt_pk_bf16_f32 v6, v6, v7
	v_cvt_pk_bf16_f32 v7, v14, v15
	global_store_dwordx4 v[12:13], v[4:7], off
	s_cbranch_vccnz .LBB0_295
	s_andn2_b64 vcc, exec, s[4:5]
	s_cbranch_vccnz .LBB0_294
	s_barrier
	s_branch .LBB0_294

;     __device__ __forceinline__ void operator()(const f32x4 (&acc)[2][2][4][2], const Unit& u, int wr, int wc, int fr, int fq) const {
;     ...
;         for (int ai = 0; ai < 2; ++ai) {
;             f32x4 stv[4]; u32x4 yfv[4], ybv[4];
; #pragma unroll
;             for (int m = 0; m < 4; ++m) { const int row = row0 + ai * HALF + m * 16;
;                 stv[m] = *(const f32x4*)(ST + (size_t)row * 16 + head * 4); yfv[m] = *(const u32x4*)(Y + (size_t)row * 2048 + col0); ybv[m] = *(const u32x4*)(YB + (size_t)row * 2048 + col0); }
; #pragma unroll
;             for (int m = 0; m < 4; ++m) { const int row = row0 + ai * HALF + m * 16; const float r = tab[u.idx * 256 + (row & 255)];
;                 const f32x4 st = stv[m];
;                 const float muf = __builtin_amdgcn_ldexpf(st[0], -9), mub = __builtin_amdgcn_ldexpf(st[2], -9); float eps = 1e-6f; asm volatile("" : "+s"(eps));
;                 const float rf = __builtin_amdgcn_rsqf(fmaxf(__builtin_amdgcn_ldexpf(st[1], -9) - muf * muf, 0.f) + eps), rb = __builtin_amdgcn_rsqf(fmaxf(__builtin_amdgcn_ldexpf(st[3], -9) - mub * mub, 0.f) + eps);
;                 const float cf = rf * r, cb = rb * r, df = -muf * cf, db = -mub * cb, kr = -1.4426950409f * r;
;                 const u32x4 yfw = yfv[m], ybw = ybv[m];
;                 float o[8];
; #pragma unroll
;                 for (int n = 0; n < 2; ++n)
; #pragma unroll
;                     for (int e = 0; e < 4; e += 2) { const int q = n * 4 + e; const unsigned wf = yfw[q >> 1], wb = ybw[q >> 1];
;                         const f32x2 yf2 = {__builtin_bit_cast(float, wf << 16), __builtin_bit_cast(float, wf & 0xffff0000u)}, yb2 = {__builtin_bit_cast(float, wb << 16), __builtin_bit_cast(float, wb & 0xffff0000u)};
;                         const f32x2 af = {acc[ai][0][m][n][e], acc[ai][0][m][n][e + 1]}, ab = {acc[ai][1][m][n][e], acc[ai][1][m][n][e + 1]};
;                         const f32x2 nf = yf2 * cf + df, nb = yb2 * cb + db;
;                         const f32x2 xf = __builtin_elementwise_min(af * kr, (f32x2){60.f, 60.f}), xb = __builtin_elementwise_min(ab * kr, (f32x2){60.f, 60.f});
;                         const f32x2 pf = (f32x2){__builtin_amdgcn_exp2f(xf[0]), __builtin_amdgcn_exp2f(xf[1])} + 1.0f, pb = (f32x2){__builtin_amdgcn_exp2f(xb[0]), __builtin_amdgcn_exp2f(xb[1])} + 1.0f;
.LBB0_346:
	s_and_b32 s36, s33, -4
	s_ashr_i32 s37, s36, 31
	v_lshl_add_u32 v190, s44, 8, v217
	v_lshl_or_b32 v108, s33, 7, v223
	s_lshl_b64 s[36:37], s[36:37], 2
	v_ashrrev_i32_e32 v109, 31, v108
	s_add_u32 s44, s74, s36
	v_ashrrev_i32_e32 v191, 31, v190
	s_addc_u32 s45, s75, s37
	v_lshlrev_b64 v[188:189], 1, v[108:109]
	v_lshlrev_b64 v[108:109], 6, v[190:191]
	v_lshl_add_u64 v[108:109], s[44:45], 0, v[108:109]
	global_load_dwordx4 v[200:203], v[108:109], off
	v_readlane_b32 s16, v254, 5
	v_lshl_add_u64 v[192:193], s[4:5], 0, v[188:189]
	v_readlane_b32 s22, v254, 11
	v_readlane_b32 s23, v254, 12
	v_lshlrev_b64 v[214:215], 12, v[190:191]
	v_lshl_add_u64 v[108:109], v[192:193], 0, v[214:215]
	v_lshl_add_u64 v[194:195], s[22:23], 0, v[188:189]
	global_load_dwordx4 v[168:171], v[108:109], off
	v_lshl_add_u64 v[108:109], v[194:195], 0, v[214:215]
	global_load_dwordx4 v[172:175], v[108:109], off
	v_or_b32_e32 v108, 16, v190
	v_ashrrev_i32_e32 v109, 31, v108
	v_lshlrev_b64 v[110:111], 6, v[108:109]
	v_lshl_add_u64 v[110:111], s[44:45], 0, v[110:111]
	global_load_dwordx4 v[164:167], v[110:111], off
	v_lshlrev_b64 v[212:213], 12, v[108:109]
	v_lshl_add_u64 v[108:109], v[192:193], 0, v[212:213]
	global_load_dwordx4 v[160:163], v[108:109], off
	v_lshl_add_u64 v[108:109], v[194:195], 0, v[212:213]
	global_load_dwordx4 v[156:159], v[108:109], off
	v_or_b32_e32 v108, 32, v190
	v_ashrrev_i32_e32 v109, 31, v108
	v_lshlrev_b64 v[110:111], 6, v[108:109]
	v_lshlrev_b64 v[198:199], 12, v[108:109]
	v_lshl_add_u64 v[110:111], s[44:45], 0, v[110:111]
	v_lshl_add_u64 v[108:109], v[192:193], 0, v[198:199]
	global_load_dwordx4 v[152:155], v[110:111], off
	global_load_dwordx4 v[140:143], v[108:109], off
	v_lshl_add_u64 v[108:109], v[194:195], 0, v[198:199]
	global_load_dwordx4 v[136:139], v[108:109], off
	v_or_b32_e32 v108, 48, v190
	s_lshl_b32 s9, s38, 10
	v_ashrrev_i32_e32 v109, 31, v108
	s_add_i32 s9, s9, 0
	v_lshlrev_b64 v[110:111], 6, v[108:109]
	v_lshlrev_b64 v[196:197], 12, v[108:109]
	s_add_i32 s9, s9, 0x20000
	v_lshl_add_u64 v[110:111], s[44:45], 0, v[110:111]
	v_lshl_add_u64 v[108:109], v[192:193], 0, v[196:197]
	v_lshl_add_u32 v191, v221, 2, s9
	global_load_dwordx4 v[124:127], v[110:111], off
	global_load_dwordx4 v[112:115], v[108:109], off
	v_lshl_add_u64 v[108:109], v[194:195], 0, v[196:197]
	ds_read_b32 v226, v191 offset:64
	ds_read_b32 v227, v191 offset:128
	ds_read_b32 v228, v191 offset:192
	ds_read_b32 v229, v191 offset:512
	ds_read_b32 v230, v191 offset:576
	ds_read_b32 v231, v191 offset:640
	ds_read_b32 v232, v191 offset:704
	ds_read_b32 v191, v191
	s_mov_b32 s11, 0x358637bd
	global_load_dwordx4 v[108:111], v[108:109], off
	s_mov_b64 s[36:37], -1
	s_waitcnt lgkmcnt(0)
	v_mul_f32_e32 v224, 0xbfb8aa3b, v191
	v_pk_mul_f32 v[204:205], v[148:149], v[224:225] op_sel_hi:[1,0]
	s_andn2_b64 vcc, exec, s[2:3]
	v_readlane_b32 s17, v254, 6
	v_readlane_b32 s18, v254, 7
	v_readlane_b32 s19, v254, 8
	v_readlane_b32 s20, v254, 9
	v_readlane_b32 s21, v254, 10
	s_waitcnt vmcnt(0)
	v_ldexp_f32 v200, v200, -9
	v_ldexp_f32 v202, v202, -9
	v_ldexp_f32 v201, v201, -9
	v_ldexp_f32 v203, v203, -9
	v_fma_f32 v201, -v200, v200, v201
	v_fma_f32 v203, -v202, v202, v203
	v_max_f32_e32 v201, 0, v201
	v_max_f32_e32 v203, 0, v203
	v_add_f32_e32 v201, s11, v201
	v_add_f32_e32 v203, s11, v203
	v_rsq_f32_e32 v201, v201
	v_rsq_f32_e32 v203, v203
	s_mov_b32 s11, 0x358637bd
	v_mul_f32_e32 v216, v191, v201
	v_mul_f32_e32 v218, v191, v203
	v_mul_f32_e64 v220, v216, -v200
	v_mul_f32_e64 v222, v218, -v202
	v_lshlrev_b32_e32 v200, 16, v168
	v_and_b32_e32 v201, 0xffff0000, v168
	v_lshlrev_b32_e32 v202, 16, v172
	v_and_b32_e32 v203, 0xffff0000, v172
	v_min_f32_e32 v168, 0x42700000, v205
	v_min_f32_e32 v172, 0x42700000, v204
	v_pk_mul_f32 v[204:205], v[144:145], v[224:225] op_sel_hi:[1,0]
	v_pk_fma_f32 v[200:201], v[216:217], v[200:201], v[220:221] op_sel_hi:[0,1,0]
	v_min_f32_e32 v191, 0x42700000, v205
	v_min_f32_e32 v208, 0x42700000, v204
	v_exp_f32_e32 v204, v172
	v_exp_f32_e32 v205, v168
	v_exp_f32_e32 v208, v208
	v_exp_f32_e32 v209, v191
	v_pk_fma_f32 v[202:203], v[218:219], v[202:203], v[222:223] op_sel_hi:[0,1,0]
	v_pk_add_f32 v[204:205], v[204:205], 1.0 op_sel_hi:[1,0]
	v_pk_mul_f32 v[148:149], v[148:149], v[200:201]
	v_pk_add_f32 v[208:209], v[208:209], 1.0 op_sel_hi:[1,0]
	v_pk_mul_f32 v[144:145], v[144:145], v[202:203]
	v_pk_mul_f32 v[210:211], v[204:205], v[208:209]
	v_pk_mul_f32 v[148:149], v[148:149], v[208:209]
	v_lshlrev_b32_e32 v168, 16, v173
	v_pk_fma_f32 v[144:145], v[144:145], v[204:205], v[148:149]
	v_rcp_f32_e32 v148, v210
	v_rcp_f32_e32 v149, v211
	s_nop 0
	v_pk_mul_f32 v[144:145], v[144:145], v[148:149]
	v_lshlrev_b32_e32 v148, 16, v169
	v_and_b32_e32 v149, 0xffff0000, v169
	v_and_b32_e32 v169, 0xffff0000, v173
	v_pk_mul_f32 v[172:173], v[150:151], v[224:225] op_sel_hi:[1,0]
	v_pk_fma_f32 v[148:149], v[216:217], v[148:149], v[220:221] op_sel_hi:[0,1,0]
	v_min_f32_e32 v191, 0x42700000, v173
	v_min_f32_e32 v200, 0x42700000, v172
	v_pk_mul_f32 v[172:173], v[146:147], v[224:225] op_sel_hi:[1,0]
	v_pk_fma_f32 v[168:169], v[218:219], v[168:169], v[222:223] op_sel_hi:[0,1,0]
	v_min_f32_e32 v201, 0x42700000, v173
	v_min_f32_e32 v202, 0x42700000, v172
	v_exp_f32_e32 v172, v200
	v_exp_f32_e32 v173, v191
	v_exp_f32_e32 v200, v202
	v_exp_f32_e32 v201, v201
	v_pk_mul_f32 v[148:149], v[150:151], v[148:149]
	v_pk_add_f32 v[172:173], v[172:173], 1.0 op_sel_hi:[1,0]
	v_pk_mul_f32 v[146:147], v[146:147], v[168:169]
	v_pk_add_f32 v[200:201], v[200:201], 1.0 op_sel_hi:[1,0]
	v_pk_mul_f32 v[168:169], v[132:133], v[224:225] op_sel_hi:[1,0]
	v_pk_mul_f32 v[202:203], v[172:173], v[200:201]
;     __device__ __forceinline__ void operator()(const f32x4 (&acc)[2][2][4][2], const Unit& u, int wr, int wc, int fr, int fq) const {
;     ...
;             for (int m = 0; m < 4; ++m) { const int row = row0 + ai * HALF + m * 16; const float r = tab[u.idx * 256 + (row & 255)];
;                 const f32x4 st = stv[m];
;                 const float muf = __builtin_amdgcn_ldexpf(st[0], -9), mub = __builtin_amdgcn_ldexpf(st[2], -9); float eps = 1e-6f; asm volatile("" : "+s"(eps));
;                 const float rf = __builtin_amdgcn_rsqf(fmaxf(__builtin_amdgcn_ldexpf(st[1], -9) - muf * muf, 0.f) + eps), rb = __builtin_amdgcn_rsqf(fmaxf(__builtin_amdgcn_ldexpf(st[3], -9) - mub * mub, 0.f) + eps);
;                 const float cf = rf * r, cb = rb * r, df = -muf * cf, db = -mub * cb, kr = -1.4426950409f * r;
;                 const u32x4 yfw = yfv[m], ybw = ybv[m];
;                 float o[8];
; #pragma unroll
;                 for (int n = 0; n < 2; ++n)
; #pragma unroll
;                     for (int e = 0; e < 4; e += 2) { const int q = n * 4 + e; const unsigned wf = yfw[q >> 1], wb = ybw[q >> 1];
;                         const f32x2 yf2 = {__builtin_bit_cast(float, wf << 16), __builtin_bit_cast(float, wf & 0xffff0000u)}, yb2 = {__builtin_bit_cast(float, wb << 16), __builtin_bit_cast(float, wb & 0xffff0000u)};
;                         const f32x2 af = {acc[ai][0][m][n][e], acc[ai][0][m][n][e + 1]}, ab = {acc[ai][1][m][n][e], acc[ai][1][m][n][e + 1]};
;                         const f32x2 nf = yf2 * cf + df, nb = yb2 * cb + db;
;                         const f32x2 xf = __builtin_elementwise_min(af * kr, (f32x2){60.f, 60.f}), xb = __builtin_elementwise_min(ab * kr, (f32x2){60.f, 60.f});
;                         const f32x2 pf = (f32x2){__builtin_amdgcn_exp2f(xf[0]), __builtin_amdgcn_exp2f(xf[1])} + 1.0f, pb = (f32x2){__builtin_amdgcn_exp2f(xb[0]), __builtin_amdgcn_exp2f(xb[1])} + 1.0f;
;                         const f32x2 den = pf * pb, num = (af * nf) * pb + (ab * nb) * pf;
;                         const f32x2 res = num * (f32x2){__builtin_amdgcn_rcpf(den[0]), __builtin_amdgcn_rcpf(den[1])};
;                         o[q] = res[0]; o[q + 1] = res[1]; }
;                 u32x4 w; w.x = cvt_pk_bf16(o[0], o[1]); w.y = cvt_pk_bf16(o[2], o[3]); w.z = cvt_pk_bf16(o[4], o[5]); w.w = cvt_pk_bf16(o[6], o[7]);
	v_pk_mul_f32 v[148:149], v[148:149], v[200:201]
	v_lshlrev_b32_e32 v150, 16, v174
	v_pk_fma_f32 v[146:147], v[146:147], v[172:173], v[148:149]
	v_rcp_f32_e32 v148, v202
	v_rcp_f32_e32 v149, v203
	v_min_f32_e32 v172, 0x42700000, v168
	v_and_b32_e32 v151, 0xffff0000, v174
	v_pk_fma_f32 v[150:151], v[218:219], v[150:151], v[222:223] op_sel_hi:[0,1,0]
	v_pk_mul_f32 v[146:147], v[146:147], v[148:149]
	v_lshlrev_b32_e32 v148, 16, v170
	v_and_b32_e32 v149, 0xffff0000, v170
	v_min_f32_e32 v170, 0x42700000, v169
	v_pk_mul_f32 v[168:169], v[128:129], v[224:225] op_sel_hi:[1,0]
	v_pk_fma_f32 v[148:149], v[216:217], v[148:149], v[220:221] op_sel_hi:[0,1,0]
	v_min_f32_e32 v173, 0x42700000, v169
	v_min_f32_e32 v174, 0x42700000, v168
	v_exp_f32_e32 v168, v172
	v_exp_f32_e32 v169, v170
	v_exp_f32_e32 v172, v174
	v_exp_f32_e32 v173, v173
	v_pk_mul_f32 v[132:133], v[132:133], v[148:149]
	v_pk_add_f32 v[168:169], v[168:169], 1.0 op_sel_hi:[1,0]
	v_pk_mul_f32 v[128:129], v[128:129], v[150:151]
	v_pk_add_f32 v[172:173], v[172:173], 1.0 op_sel_hi:[1,0]
	v_pk_mul_f32 v[150:151], v[134:135], v[224:225] op_sel_hi:[1,0]
	v_pk_mul_f32 v[200:201], v[168:169], v[172:173]
	v_pk_mul_f32 v[132:133], v[132:133], v[172:173]
	v_lshlrev_b32_e32 v148, 16, v175
	v_pk_fma_f32 v[128:129], v[128:129], v[168:169], v[132:133]
	v_rcp_f32_e32 v132, v200
	v_rcp_f32_e32 v133, v201
	v_min_f32_e32 v168, 0x42700000, v151
	v_min_f32_e32 v169, 0x42700000, v150
	v_pk_mul_f32 v[150:151], v[130:131], v[224:225] op_sel_hi:[1,0]
	v_pk_mul_f32 v[132:133], v[128:129], v[132:133]
	v_lshlrev_b32_e32 v128, 16, v171
	v_and_b32_e32 v129, 0xffff0000, v171
	v_min_f32_e32 v170, 0x42700000, v151
	v_min_f32_e32 v171, 0x42700000, v150
	v_exp_f32_e32 v150, v169
	v_exp_f32_e32 v151, v168
	v_exp_f32_e32 v168, v171
	v_exp_f32_e32 v169, v170
	v_and_b32_e32 v149, 0xffff0000, v175
	v_pk_fma_f32 v[128:129], v[216:217], v[128:129], v[220:221] op_sel_hi:[0,1,0]
	v_pk_fma_f32 v[148:149], v[218:219], v[148:149], v[222:223] op_sel_hi:[0,1,0]
	v_pk_add_f32 v[150:151], v[150:151], 1.0 op_sel_hi:[1,0]
	v_pk_add_f32 v[168:169], v[168:169], 1.0 op_sel_hi:[1,0]
	v_pk_mul_f32 v[128:129], v[134:135], v[128:129]
	v_pk_mul_f32 v[170:171], v[150:151], v[168:169]
	v_pk_mul_f32 v[128:129], v[128:129], v[168:169]
	v_pk_mul_f32 v[130:131], v[130:131], v[148:149]
	v_lshlrev_b32_e32 v148, 16, v156
	v_pk_fma_f32 v[128:129], v[130:131], v[150:151], v[128:129]
	v_rcp_f32_e32 v130, v170
	v_rcp_f32_e32 v131, v171
	v_and_b32_e32 v149, 0xffff0000, v156
	v_pk_mul_f32 v[134:135], v[128:129], v[130:131]
	v_cvt_pk_bf16_f32 v128, v144, v145
	v_cvt_pk_bf16_f32 v129, v146, v147
	v_cvt_pk_bf16_f32 v130, v132, v133
	v_lshl_add_u64 v[132:133], s[4:5], 0, v[214:215]
	v_cvt_pk_bf16_f32 v131, v134, v135
	v_lshl_add_u64 v[132:133], v[132:133], 0, v[188:189]
	global_store_dwordx4 v[132:133], v[128:131], off
	v_ldexp_f32 v132, v167, -9
	v_lshlrev_b32_e32 v146, 16, v160
	v_ldexp_f32 v129, v164, -9
	v_ldexp_f32 v131, v166, -9
	v_ldexp_f32 v130, v165, -9
	v_bitop3_b32 v128, v190, s71, 16 bitop3:0xc8
	v_fma_f32 v130, -v129, v129, v130
	v_fma_f32 v132, -v131, v131, v132
	v_lshl_add_u32 v128, v128, 2, s9
	v_max_f32_e32 v130, 0, v130
	v_max_f32_e32 v132, 0, v132
	v_mov_b32_e32 v128, v226
	v_and_b32_e32 v147, 0xffff0000, v160
	v_add_f32_e32 v130, s11, v130
	v_add_f32_e32 v132, s11, v132
	v_rsq_f32_e32 v130, v130
	v_rsq_f32_e32 v132, v132
	s_movk_i32 s11, 0xef
	s_waitcnt lgkmcnt(0)
	v_mul_f32_e32 v130, v128, v130
	v_mul_f32_e32 v132, v128, v132
	v_mul_f32_e32 v128, 0xbfb8aa3b, v128
	v_pk_mul_f32 v[150:151], v[120:121], v[128:129] op_sel_hi:[1,0]
	v_mul_f32_e64 v134, v130, -v129
	v_min_f32_e32 v129, 0x42700000, v151
	v_mul_f32_e64 v144, v132, -v131
	v_pk_fma_f32 v[146:147], v[130:131], v[146:147], v[134:135] op_sel_hi:[0,1,0]
	v_min_f32_e32 v131, 0x42700000, v150
	v_pk_mul_f32 v[150:151], v[116:117], v[128:129] op_sel_hi:[1,0]
	v_pk_fma_f32 v[148:149], v[132:133], v[148:149], v[144:145] op_sel_hi:[0,1,0]
	v_min_f32_e32 v133, 0x42700000, v151
	v_min_f32_e32 v135, 0x42700000, v150
	v_exp_f32_e32 v150, v131
	v_exp_f32_e32 v151, v129
	v_exp_f32_e32 v164, v135
	v_exp_f32_e32 v165, v133
	v_pk_mul_f32 v[120:121], v[120:121], v[146:147]
	v_pk_add_f32 v[150:151], v[150:151], 1.0 op_sel_hi:[1,0]
	v_pk_mul_f32 v[116:117], v[116:117], v[148:149]
	v_pk_add_f32 v[164:165], v[164:165], 1.0 op_sel_hi:[1,0]
	v_pk_mul_f32 v[148:149], v[122:123], v[128:129] op_sel_hi:[1,0]
	v_pk_mul_f32 v[166:167], v[150:151], v[164:165]
	v_pk_mul_f32 v[120:121], v[120:121], v[164:165]
	v_min_f32_e32 v129, 0x42700000, v149
	v_pk_fma_f32 v[116:117], v[116:117], v[150:151], v[120:121]
	v_rcp_f32_e32 v120, v166
	v_rcp_f32_e32 v121, v167
	v_lshlrev_b32_e32 v146, 16, v157
	v_and_b32_e32 v147, 0xffff0000, v157
	v_pk_fma_f32 v[146:147], v[132:133], v[146:147], v[144:145] op_sel_hi:[0,1,0]
	v_pk_mul_f32 v[116:117], v[116:117], v[120:121]
	v_lshlrev_b32_e32 v120, 16, v161
	v_and_b32_e32 v121, 0xffff0000, v161
	v_pk_fma_f32 v[120:121], v[130:131], v[120:121], v[134:135] op_sel_hi:[0,1,0]
	v_min_f32_e32 v131, 0x42700000, v148
	v_pk_mul_f32 v[148:149], v[118:119], v[128:129] op_sel_hi:[1,0]
	v_pk_mul_f32 v[120:121], v[122:123], v[120:121]
	v_min_f32_e32 v133, 0x42700000, v149
	v_min_f32_e32 v135, 0x42700000, v148
	v_exp_f32_e32 v148, v131
	v_exp_f32_e32 v149, v129
	v_exp_f32_e32 v150, v135
	v_exp_f32_e32 v151, v133
	v_pk_mul_f32 v[118:119], v[118:119], v[146:147]
	v_pk_add_f32 v[148:149], v[148:149], 1.0 op_sel_hi:[1,0]
	v_pk_mul_f32 v[146:147], v[104:105], v[128:129] op_sel_hi:[1,0]
	v_pk_add_f32 v[150:151], v[150:151], 1.0 op_sel_hi:[1,0]
	v_min_f32_e32 v129, 0x42700000, v147
	v_pk_mul_f32 v[156:157], v[148:149], v[150:151]
;     __device__ __forceinline__ void operator()(const f32x4 (&acc)[2][2][4][2], const Unit& u, int wr, int wc, int fr, int fq) const {
;     ...
;             for (int m = 0; m < 4; ++m) { const int row = row0 + ai * HALF + m * 16; const float r = tab[u.idx * 256 + (row & 255)];
;                 const f32x4 st = stv[m];
;                 const float muf = __builtin_amdgcn_ldexpf(st[0], -9), mub = __builtin_amdgcn_ldexpf(st[2], -9); float eps = 1e-6f; asm volatile("" : "+s"(eps));
;                 const float rf = __builtin_amdgcn_rsqf(fmaxf(__builtin_amdgcn_ldexpf(st[1], -9) - muf * muf, 0.f) + eps), rb = __builtin_amdgcn_rsqf(fmaxf(__builtin_amdgcn_ldexpf(st[3], -9) - mub * mub, 0.f) + eps);
;                 const float cf = rf * r, cb = rb * r, df = -muf * cf, db = -mub * cb, kr = -1.4426950409f * r;
;                 const u32x4 yfw = yfv[m], ybw = ybv[m];
;                 float o[8];
; #pragma unroll
;                 for (int n = 0; n < 2; ++n)
; #pragma unroll
;                     for (int e = 0; e < 4; e += 2) { const int q = n * 4 + e; const unsigned wf = yfw[q >> 1], wb = ybw[q >> 1];
;                         const f32x2 yf2 = {__builtin_bit_cast(float, wf << 16), __builtin_bit_cast(float, wf & 0xffff0000u)}, yb2 = {__builtin_bit_cast(float, wb << 16), __builtin_bit_cast(float, wb & 0xffff0000u)};
;                         const f32x2 af = {acc[ai][0][m][n][e], acc[ai][0][m][n][e + 1]}, ab = {acc[ai][1][m][n][e], acc[ai][1][m][n][e + 1]};
;                         const f32x2 nf = yf2 * cf + df, nb = yb2 * cb + db;
;                         const f32x2 xf = __builtin_elementwise_min(af * kr, (f32x2){60.f, 60.f}), xb = __builtin_elementwise_min(ab * kr, (f32x2){60.f, 60.f});
;                         const f32x2 pf = (f32x2){__builtin_amdgcn_exp2f(xf[0]), __builtin_amdgcn_exp2f(xf[1])} + 1.0f, pb = (f32x2){__builtin_amdgcn_exp2f(xb[0]), __builtin_amdgcn_exp2f(xb[1])} + 1.0f;
;                         const f32x2 den = pf * pb, num = (af * nf) * pb + (ab * nb) * pf;
;                         const f32x2 res = num * (f32x2){__builtin_amdgcn_rcpf(den[0]), __builtin_amdgcn_rcpf(den[1])};
;                         o[q] = res[0]; o[q + 1] = res[1]; }
;                 u32x4 w; w.x = cvt_pk_bf16(o[0], o[1]); w.y = cvt_pk_bf16(o[2], o[3]); w.z = cvt_pk_bf16(o[4], o[5]); w.w = cvt_pk_bf16(o[6], o[7]);
	v_pk_mul_f32 v[120:121], v[120:121], v[150:151]
	v_lshlrev_b32_e32 v122, 16, v158
	v_pk_fma_f32 v[118:119], v[118:119], v[148:149], v[120:121]
	v_rcp_f32_e32 v120, v156
	v_rcp_f32_e32 v121, v157
	v_and_b32_e32 v123, 0xffff0000, v158
	v_pk_fma_f32 v[122:123], v[132:133], v[122:123], v[144:145] op_sel_hi:[0,1,0]
	v_pk_mul_f32 v[118:119], v[118:119], v[120:121]
	v_lshlrev_b32_e32 v120, 16, v162
	v_and_b32_e32 v121, 0xffff0000, v162
	v_pk_fma_f32 v[120:121], v[130:131], v[120:121], v[134:135] op_sel_hi:[0,1,0]
	v_min_f32_e32 v131, 0x42700000, v146
	v_pk_mul_f32 v[146:147], v[100:101], v[128:129] op_sel_hi:[1,0]
	v_pk_mul_f32 v[104:105], v[104:105], v[120:121]
	v_min_f32_e32 v133, 0x42700000, v147
	v_min_f32_e32 v135, 0x42700000, v146
	v_exp_f32_e32 v146, v131
	v_exp_f32_e32 v147, v129
	v_exp_f32_e32 v148, v135
	v_exp_f32_e32 v149, v133
	v_pk_mul_f32 v[100:101], v[100:101], v[122:123]
	v_pk_add_f32 v[146:147], v[146:147], 1.0 op_sel_hi:[1,0]
	v_pk_mul_f32 v[122:123], v[106:107], v[128:129] op_sel_hi:[1,0]
	v_pk_add_f32 v[148:149], v[148:149], 1.0 op_sel_hi:[1,0]
	v_min_f32_e32 v129, 0x42700000, v123
	v_pk_mul_f32 v[150:151], v[146:147], v[148:149]
	v_pk_mul_f32 v[104:105], v[104:105], v[148:149]
	v_lshlrev_b32_e32 v120, 16, v159
	v_pk_fma_f32 v[100:101], v[100:101], v[146:147], v[104:105]
	v_rcp_f32_e32 v104, v150
	v_rcp_f32_e32 v105, v151
	v_and_b32_e32 v121, 0xffff0000, v159
	v_pk_fma_f32 v[120:121], v[132:133], v[120:121], v[144:145] op_sel_hi:[0,1,0]
	v_pk_mul_f32 v[104:105], v[100:101], v[104:105]
	v_lshlrev_b32_e32 v100, 16, v163
	v_and_b32_e32 v101, 0xffff0000, v163
	v_pk_fma_f32 v[100:101], v[130:131], v[100:101], v[134:135] op_sel_hi:[0,1,0]
	v_min_f32_e32 v130, 0x42700000, v122
	v_pk_mul_f32 v[122:123], v[102:103], v[128:129] op_sel_hi:[1,0]
	v_pk_mul_f32 v[100:101], v[106:107], v[100:101]
	v_min_f32_e32 v131, 0x42700000, v123
	v_min_f32_e32 v128, 0x42700000, v122
	v_exp_f32_e32 v122, v130
	v_exp_f32_e32 v123, v129
	v_exp_f32_e32 v128, v128
	v_exp_f32_e32 v129, v131
	v_pk_mul_f32 v[102:103], v[102:103], v[120:121]
	v_pk_add_f32 v[122:123], v[122:123], 1.0 op_sel_hi:[1,0]
	v_lshlrev_b32_e32 v120, 16, v136
	v_pk_add_f32 v[128:129], v[128:129], 1.0 op_sel_hi:[1,0]
	v_and_b32_e32 v121, 0xffff0000, v136
	v_pk_mul_f32 v[130:131], v[122:123], v[128:129]
	v_pk_mul_f32 v[100:101], v[100:101], v[128:129]
	s_nop 0
	v_pk_fma_f32 v[100:101], v[102:103], v[122:123], v[100:101]
	v_rcp_f32_e32 v102, v130
	v_rcp_f32_e32 v103, v131
	s_nop 0
	v_pk_mul_f32 v[106:107], v[100:101], v[102:103]
	v_cvt_pk_bf16_f32 v100, v116, v117
	v_cvt_pk_bf16_f32 v101, v118, v119
	v_cvt_pk_bf16_f32 v102, v104, v105
	v_lshl_add_u64 v[104:105], s[4:5], 0, v[212:213]
	v_cvt_pk_bf16_f32 v103, v106, v107
	v_lshl_add_u64 v[104:105], v[104:105], 0, v[188:189]
	global_store_dwordx4 v[104:105], v[100:103], off
	v_ldexp_f32 v104, v155, -9
	v_lshlrev_b32_e32 v118, 16, v140
	v_ldexp_f32 v101, v152, -9
	v_ldexp_f32 v103, v154, -9
	v_ldexp_f32 v102, v153, -9
	v_bitop3_b32 v100, v190, s11, 32 bitop3:0xc8
	v_fma_f32 v102, -v101, v101, v102
	v_fma_f32 v104, -v103, v103, v104
	v_lshl_add_u32 v100, v100, 2, s9
	s_mov_b32 s11, 0x358637bd
	v_max_f32_e32 v102, 0, v102
	v_max_f32_e32 v104, 0, v104
	v_mov_b32_e32 v100, v227
	v_and_b32_e32 v119, 0xffff0000, v140
	v_add_f32_e32 v102, s11, v102
	v_add_f32_e32 v104, s11, v104
	v_rsq_f32_e32 v102, v102
	v_rsq_f32_e32 v104, v104
	s_mov_b32 s11, 0x358637bd
	s_waitcnt lgkmcnt(0)
	v_mul_f32_e32 v102, v100, v102
	v_mul_f32_e32 v104, v100, v104
	v_mul_f32_e32 v100, 0xbfb8aa3b, v100
	v_pk_mul_f32 v[122:123], v[96:97], v[100:101] op_sel_hi:[1,0]
	v_mul_f32_e64 v106, v102, -v101
	v_min_f32_e32 v101, 0x42700000, v123
	v_mul_f32_e64 v116, v104, -v103
	v_pk_fma_f32 v[118:119], v[102:103], v[118:119], v[106:107] op_sel_hi:[0,1,0]
	v_min_f32_e32 v103, 0x42700000, v122
	v_pk_mul_f32 v[122:123], v[92:93], v[100:101] op_sel_hi:[1,0]
	v_pk_fma_f32 v[120:121], v[104:105], v[120:121], v[116:117] op_sel_hi:[0,1,0]
	v_min_f32_e32 v105, 0x42700000, v123
	v_min_f32_e32 v107, 0x42700000, v122
	v_exp_f32_e32 v122, v103
	v_exp_f32_e32 v123, v101
	v_exp_f32_e32 v128, v107
	v_exp_f32_e32 v129, v105
	v_pk_mul_f32 v[96:97], v[96:97], v[118:119]
	v_pk_add_f32 v[122:123], v[122:123], 1.0 op_sel_hi:[1,0]
	v_pk_mul_f32 v[92:93], v[92:93], v[120:121]
	v_pk_add_f32 v[128:129], v[128:129], 1.0 op_sel_hi:[1,0]
	v_pk_mul_f32 v[120:121], v[98:99], v[100:101] op_sel_hi:[1,0]
	v_pk_mul_f32 v[130:131], v[122:123], v[128:129]
	v_pk_mul_f32 v[96:97], v[96:97], v[128:129]
	v_min_f32_e32 v101, 0x42700000, v121
	v_pk_fma_f32 v[92:93], v[92:93], v[122:123], v[96:97]
	v_rcp_f32_e32 v96, v130
	v_rcp_f32_e32 v97, v131
	v_lshlrev_b32_e32 v118, 16, v137
	v_and_b32_e32 v119, 0xffff0000, v137
	v_pk_fma_f32 v[118:119], v[104:105], v[118:119], v[116:117] op_sel_hi:[0,1,0]
	v_pk_mul_f32 v[92:93], v[92:93], v[96:97]
	v_lshlrev_b32_e32 v96, 16, v141
	v_and_b32_e32 v97, 0xffff0000, v141
	v_pk_fma_f32 v[96:97], v[102:103], v[96:97], v[106:107] op_sel_hi:[0,1,0]
	v_min_f32_e32 v103, 0x42700000, v120
	v_pk_mul_f32 v[120:121], v[94:95], v[100:101] op_sel_hi:[1,0]
	v_pk_mul_f32 v[96:97], v[98:99], v[96:97]
	v_min_f32_e32 v105, 0x42700000, v121
	v_min_f32_e32 v107, 0x42700000, v120
	v_exp_f32_e32 v120, v103
	v_exp_f32_e32 v121, v101
	v_exp_f32_e32 v122, v107
	v_exp_f32_e32 v123, v105
	v_pk_mul_f32 v[94:95], v[94:95], v[118:119]
	v_pk_add_f32 v[120:121], v[120:121], 1.0 op_sel_hi:[1,0]
	v_pk_mul_f32 v[118:119], v[88:89], v[100:101] op_sel_hi:[1,0]
	v_pk_add_f32 v[122:123], v[122:123], 1.0 op_sel_hi:[1,0]
	v_min_f32_e32 v101, 0x42700000, v119
	v_pk_mul_f32 v[128:129], v[120:121], v[122:123]
	v_pk_mul_f32 v[96:97], v[96:97], v[122:123]
;     __device__ __forceinline__ void operator()(const f32x4 (&acc)[2][2][4][2], const Unit& u, int wr, int wc, int fr, int fq) const {
;     ...
;             for (int m = 0; m < 4; ++m) { const int row = row0 + ai * HALF + m * 16; const float r = tab[u.idx * 256 + (row & 255)];
;                 const f32x4 st = stv[m];
;                 const float muf = __builtin_amdgcn_ldexpf(st[0], -9), mub = __builtin_amdgcn_ldexpf(st[2], -9); float eps = 1e-6f; asm volatile("" : "+s"(eps));
;                 const float rf = __builtin_amdgcn_rsqf(fmaxf(__builtin_amdgcn_ldexpf(st[1], -9) - muf * muf, 0.f) + eps), rb = __builtin_amdgcn_rsqf(fmaxf(__builtin_amdgcn_ldexpf(st[3], -9) - mub * mub, 0.f) + eps);
;                 const float cf = rf * r, cb = rb * r, df = -muf * cf, db = -mub * cb, kr = -1.4426950409f * r;
;                 const u32x4 yfw = yfv[m], ybw = ybv[m];
;                 float o[8];
; #pragma unroll
;                 for (int n = 0; n < 2; ++n)
; #pragma unroll
;                     for (int e = 0; e < 4; e += 2) { const int q = n * 4 + e; const unsigned wf = yfw[q >> 1], wb = ybw[q >> 1];
;                         const f32x2 yf2 = {__builtin_bit_cast(float, wf << 16), __builtin_bit_cast(float, wf & 0xffff0000u)}, yb2 = {__builtin_bit_cast(float, wb << 16), __builtin_bit_cast(float, wb & 0xffff0000u)};
;                         const f32x2 af = {acc[ai][0][m][n][e], acc[ai][0][m][n][e + 1]}, ab = {acc[ai][1][m][n][e], acc[ai][1][m][n][e + 1]};
;                         const f32x2 nf = yf2 * cf + df, nb = yb2 * cb + db;
;                         const f32x2 xf = __builtin_elementwise_min(af * kr, (f32x2){60.f, 60.f}), xb = __builtin_elementwise_min(ab * kr, (f32x2){60.f, 60.f});
;                         const f32x2 pf = (f32x2){__builtin_amdgcn_exp2f(xf[0]), __builtin_amdgcn_exp2f(xf[1])} + 1.0f, pb = (f32x2){__builtin_amdgcn_exp2f(xb[0]), __builtin_amdgcn_exp2f(xb[1])} + 1.0f;
;                         const f32x2 den = pf * pb, num = (af * nf) * pb + (ab * nb) * pf;
;                         const f32x2 res = num * (f32x2){__builtin_amdgcn_rcpf(den[0]), __builtin_amdgcn_rcpf(den[1])};
;                         o[q] = res[0]; o[q + 1] = res[1]; }
;                 u32x4 w; w.x = cvt_pk_bf16(o[0], o[1]); w.y = cvt_pk_bf16(o[2], o[3]); w.z = cvt_pk_bf16(o[4], o[5]); w.w = cvt_pk_bf16(o[6], o[7]);
	v_lshlrev_b32_e32 v98, 16, v138
	v_pk_fma_f32 v[94:95], v[94:95], v[120:121], v[96:97]
	v_rcp_f32_e32 v96, v128
	v_rcp_f32_e32 v97, v129
	v_and_b32_e32 v99, 0xffff0000, v138
	v_pk_fma_f32 v[98:99], v[104:105], v[98:99], v[116:117] op_sel_hi:[0,1,0]
	v_add_u32_e32 v130, 0x80, v190
	v_pk_mul_f32 v[94:95], v[94:95], v[96:97]
	v_lshlrev_b32_e32 v96, 16, v142
	v_and_b32_e32 v97, 0xffff0000, v142
	v_pk_fma_f32 v[96:97], v[102:103], v[96:97], v[106:107] op_sel_hi:[0,1,0]
	v_min_f32_e32 v103, 0x42700000, v118
	v_pk_mul_f32 v[118:119], v[84:85], v[100:101] op_sel_hi:[1,0]
	v_pk_mul_f32 v[88:89], v[88:89], v[96:97]
	v_min_f32_e32 v105, 0x42700000, v119
	v_min_f32_e32 v107, 0x42700000, v118
	v_exp_f32_e32 v118, v103
	v_exp_f32_e32 v119, v101
	v_exp_f32_e32 v120, v107
	v_exp_f32_e32 v121, v105
	v_pk_mul_f32 v[84:85], v[84:85], v[98:99]
	v_pk_add_f32 v[118:119], v[118:119], 1.0 op_sel_hi:[1,0]
	v_pk_mul_f32 v[98:99], v[90:91], v[100:101] op_sel_hi:[1,0]
	v_pk_add_f32 v[120:121], v[120:121], 1.0 op_sel_hi:[1,0]
	v_min_f32_e32 v101, 0x42700000, v99
	v_pk_mul_f32 v[122:123], v[118:119], v[120:121]
	v_pk_mul_f32 v[88:89], v[88:89], v[120:121]
	v_lshlrev_b32_e32 v96, 16, v139
	v_pk_fma_f32 v[84:85], v[84:85], v[118:119], v[88:89]
	v_rcp_f32_e32 v88, v122
	v_rcp_f32_e32 v89, v123
	v_and_b32_e32 v97, 0xffff0000, v139
	v_pk_fma_f32 v[96:97], v[104:105], v[96:97], v[116:117] op_sel_hi:[0,1,0]
	v_ashrrev_i32_e32 v131, 31, v130
	v_pk_mul_f32 v[88:89], v[84:85], v[88:89]
	v_lshlrev_b32_e32 v84, 16, v143
	v_and_b32_e32 v85, 0xffff0000, v143
	v_pk_fma_f32 v[84:85], v[102:103], v[84:85], v[106:107] op_sel_hi:[0,1,0]
	v_min_f32_e32 v102, 0x42700000, v98
	v_pk_mul_f32 v[98:99], v[86:87], v[100:101] op_sel_hi:[1,0]
	v_pk_mul_f32 v[84:85], v[90:91], v[84:85]
	v_min_f32_e32 v103, 0x42700000, v99
	v_min_f32_e32 v100, 0x42700000, v98
	v_exp_f32_e32 v98, v102
	v_exp_f32_e32 v99, v101
	v_exp_f32_e32 v100, v100
	v_exp_f32_e32 v101, v103
	v_pk_mul_f32 v[86:87], v[86:87], v[96:97]
	v_pk_add_f32 v[98:99], v[98:99], 1.0 op_sel_hi:[1,0]
	v_lshlrev_b32_e32 v96, 16, v108
	v_pk_add_f32 v[100:101], v[100:101], 1.0 op_sel_hi:[1,0]
	v_and_b32_e32 v97, 0xffff0000, v108
	v_pk_mul_f32 v[102:103], v[98:99], v[100:101]
	v_pk_mul_f32 v[84:85], v[84:85], v[100:101]
	v_lshlrev_b64 v[122:123], 12, v[130:131]
	v_pk_fma_f32 v[84:85], v[86:87], v[98:99], v[84:85]
	v_rcp_f32_e32 v86, v102
	v_rcp_f32_e32 v87, v103
	v_add_u32_e32 v120, 0xa0, v190
	v_ashrrev_i32_e32 v121, 31, v120
	v_add_u32_e32 v116, 0xb0, v190
	v_pk_mul_f32 v[90:91], v[84:85], v[86:87]
	v_cvt_pk_bf16_f32 v84, v92, v93
	v_cvt_pk_bf16_f32 v85, v94, v95
	v_cvt_pk_bf16_f32 v86, v88, v89
	v_lshl_add_u64 v[88:89], s[4:5], 0, v[198:199]
	v_cvt_pk_bf16_f32 v87, v90, v91
	v_lshl_add_u64 v[88:89], v[88:89], 0, v[188:189]
	global_store_dwordx4 v[88:89], v[84:87], off
	v_ldexp_f32 v88, v127, -9
	v_lshlrev_b32_e32 v94, 16, v112
	v_ldexp_f32 v85, v124, -9
	v_ldexp_f32 v87, v126, -9
	v_ldexp_f32 v86, v125, -9
	v_bitop3_b32 v84, v190, s70, 48 bitop3:0xc8
	v_fma_f32 v86, -v85, v85, v86
	v_fma_f32 v88, -v87, v87, v88
	v_lshl_add_u32 v84, v84, 2, s9
	v_max_f32_e32 v86, 0, v86
	v_max_f32_e32 v88, 0, v88
	v_mov_b32_e32 v84, v228
	v_and_b32_e32 v95, 0xffff0000, v112
	v_add_f32_e32 v86, s11, v86
	v_add_f32_e32 v88, s11, v88
	v_rsq_f32_e32 v86, v86
	v_rsq_f32_e32 v88, v88
	v_add_u32_e32 v124, 0x90, v190
	v_ashrrev_i32_e32 v125, 31, v124
	s_waitcnt lgkmcnt(0)
	v_mul_f32_e32 v86, v84, v86
	v_mul_f32_e32 v88, v84, v88
	v_mul_f32_e32 v84, 0xbfb8aa3b, v84
	v_pk_mul_f32 v[98:99], v[80:81], v[84:85] op_sel_hi:[1,0]
	v_mul_f32_e64 v90, v86, -v85
	v_min_f32_e32 v85, 0x42700000, v99
	v_mul_f32_e64 v92, v88, -v87
	v_pk_fma_f32 v[94:95], v[86:87], v[94:95], v[90:91] op_sel_hi:[0,1,0]
	v_min_f32_e32 v87, 0x42700000, v98
	v_pk_mul_f32 v[98:99], v[76:77], v[84:85] op_sel_hi:[1,0]
	v_pk_fma_f32 v[96:97], v[88:89], v[96:97], v[92:93] op_sel_hi:[0,1,0]
	v_min_f32_e32 v89, 0x42700000, v99
	v_min_f32_e32 v91, 0x42700000, v98
	v_exp_f32_e32 v98, v87
	v_exp_f32_e32 v99, v85
	v_exp_f32_e32 v100, v91
	v_exp_f32_e32 v101, v89
	v_pk_mul_f32 v[80:81], v[80:81], v[94:95]
	v_pk_add_f32 v[98:99], v[98:99], 1.0 op_sel_hi:[1,0]
	v_pk_mul_f32 v[76:77], v[76:77], v[96:97]
	v_pk_add_f32 v[100:101], v[100:101], 1.0 op_sel_hi:[1,0]
	v_pk_mul_f32 v[96:97], v[82:83], v[84:85] op_sel_hi:[1,0]
	v_pk_mul_f32 v[102:103], v[98:99], v[100:101]
	v_pk_mul_f32 v[80:81], v[80:81], v[100:101]
	v_min_f32_e32 v85, 0x42700000, v97
	v_pk_fma_f32 v[76:77], v[76:77], v[98:99], v[80:81]
	v_rcp_f32_e32 v80, v102
	v_rcp_f32_e32 v81, v103
	v_lshlrev_b32_e32 v94, 16, v109
	v_and_b32_e32 v95, 0xffff0000, v109
	v_pk_fma_f32 v[94:95], v[88:89], v[94:95], v[92:93] op_sel_hi:[0,1,0]
	v_pk_mul_f32 v[76:77], v[76:77], v[80:81]
	v_lshlrev_b32_e32 v80, 16, v113
	v_and_b32_e32 v81, 0xffff0000, v113
	v_pk_fma_f32 v[80:81], v[86:87], v[80:81], v[90:91] op_sel_hi:[0,1,0]
	v_min_f32_e32 v87, 0x42700000, v96
	v_pk_mul_f32 v[96:97], v[78:79], v[84:85] op_sel_hi:[1,0]
	v_pk_mul_f32 v[80:81], v[82:83], v[80:81]
	v_min_f32_e32 v89, 0x42700000, v97
	v_min_f32_e32 v91, 0x42700000, v96
	v_exp_f32_e32 v96, v87
	v_exp_f32_e32 v97, v85
	v_exp_f32_e32 v98, v91
	v_exp_f32_e32 v99, v89
	v_pk_mul_f32 v[78:79], v[78:79], v[94:95]
	v_pk_add_f32 v[96:97], v[96:97], 1.0 op_sel_hi:[1,0]
	v_pk_mul_f32 v[94:95], v[72:73], v[84:85] op_sel_hi:[1,0]
	v_pk_add_f32 v[98:99], v[98:99], 1.0 op_sel_hi:[1,0]
	v_min_f32_e32 v85, 0x42700000, v95
	v_pk_mul_f32 v[100:101], v[96:97], v[98:99]
	v_pk_mul_f32 v[80:81], v[80:81], v[98:99]
	v_lshlrev_b32_e32 v82, 16, v110
	v_pk_fma_f32 v[78:79], v[78:79], v[96:97], v[80:81]
	v_rcp_f32_e32 v80, v100
	v_rcp_f32_e32 v81, v101
;     __device__ __forceinline__ void operator()(const f32x4 (&acc)[2][2][4][2], const Unit& u, int wr, int wc, int fr, int fq) const {
;     ...
;         for (int ai = 0; ai < 2; ++ai) {
;             f32x4 stv[4]; u32x4 yfv[4], ybv[4];
; #pragma unroll
;             for (int m = 0; m < 4; ++m) { const int row = row0 + ai * HALF + m * 16;
;                 stv[m] = *(const f32x4*)(ST + (size_t)row * 16 + head * 4); yfv[m] = *(const u32x4*)(Y + (size_t)row * 2048 + col0); ybv[m] = *(const u32x4*)(YB + (size_t)row * 2048 + col0); }
; #pragma unroll
;             for (int m = 0; m < 4; ++m) { const int row = row0 + ai * HALF + m * 16; const float r = tab[u.idx * 256 + (row & 255)];
;                 const f32x4 st = stv[m];
;                 const float muf = __builtin_amdgcn_ldexpf(st[0], -9), mub = __builtin_amdgcn_ldexpf(st[2], -9); float eps = 1e-6f; asm volatile("" : "+s"(eps));
;                 const float rf = __builtin_amdgcn_rsqf(fmaxf(__builtin_amdgcn_ldexpf(st[1], -9) - muf * muf, 0.f) + eps), rb = __builtin_amdgcn_rsqf(fmaxf(__builtin_amdgcn_ldexpf(st[3], -9) - mub * mub, 0.f) + eps);
;                 const float cf = rf * r, cb = rb * r, df = -muf * cf, db = -mub * cb, kr = -1.4426950409f * r;
;                 const u32x4 yfw = yfv[m], ybw = ybv[m];
;                 float o[8];
; #pragma unroll
;                 for (int n = 0; n < 2; ++n)
; #pragma unroll
;                     for (int e = 0; e < 4; e += 2) { const int q = n * 4 + e; const unsigned wf = yfw[q >> 1], wb = ybw[q >> 1];
;                         const f32x2 yf2 = {__builtin_bit_cast(float, wf << 16), __builtin_bit_cast(float, wf & 0xffff0000u)}, yb2 = {__builtin_bit_cast(float, wb << 16), __builtin_bit_cast(float, wb & 0xffff0000u)};
;                         const f32x2 af = {acc[ai][0][m][n][e], acc[ai][0][m][n][e + 1]}, ab = {acc[ai][1][m][n][e], acc[ai][1][m][n][e + 1]};
;                         const f32x2 nf = yf2 * cf + df, nb = yb2 * cb + db;
;                         const f32x2 xf = __builtin_elementwise_min(af * kr, (f32x2){60.f, 60.f}), xb = __builtin_elementwise_min(ab * kr, (f32x2){60.f, 60.f});
;                         const f32x2 pf = (f32x2){__builtin_amdgcn_exp2f(xf[0]), __builtin_amdgcn_exp2f(xf[1])} + 1.0f, pb = (f32x2){__builtin_amdgcn_exp2f(xb[0]), __builtin_amdgcn_exp2f(xb[1])} + 1.0f;
	v_and_b32_e32 v83, 0xffff0000, v110
	v_pk_fma_f32 v[82:83], v[88:89], v[82:83], v[92:93] op_sel_hi:[0,1,0]
	v_lshlrev_b64 v[118:119], 12, v[124:125]
	v_pk_mul_f32 v[78:79], v[78:79], v[80:81]
	v_lshlrev_b32_e32 v80, 16, v114
	v_and_b32_e32 v81, 0xffff0000, v114
	v_pk_fma_f32 v[80:81], v[86:87], v[80:81], v[90:91] op_sel_hi:[0,1,0]
	v_min_f32_e32 v87, 0x42700000, v94
	v_pk_mul_f32 v[94:95], v[68:69], v[84:85] op_sel_hi:[1,0]
	v_pk_mul_f32 v[72:73], v[72:73], v[80:81]
	v_min_f32_e32 v89, 0x42700000, v95
	v_min_f32_e32 v91, 0x42700000, v94
	v_exp_f32_e32 v94, v87
	v_exp_f32_e32 v95, v85
	v_exp_f32_e32 v96, v91
	v_exp_f32_e32 v97, v89
	v_pk_mul_f32 v[68:69], v[68:69], v[82:83]
	v_pk_add_f32 v[94:95], v[94:95], 1.0 op_sel_hi:[1,0]
	v_pk_mul_f32 v[82:83], v[74:75], v[84:85] op_sel_hi:[1,0]
	v_pk_add_f32 v[96:97], v[96:97], 1.0 op_sel_hi:[1,0]
	v_min_f32_e32 v85, 0x42700000, v83
	v_pk_mul_f32 v[98:99], v[94:95], v[96:97]
	v_pk_mul_f32 v[72:73], v[72:73], v[96:97]
	v_lshlrev_b32_e32 v80, 16, v111
	v_pk_fma_f32 v[68:69], v[68:69], v[94:95], v[72:73]
	v_rcp_f32_e32 v72, v98
	v_rcp_f32_e32 v73, v99
	v_and_b32_e32 v81, 0xffff0000, v111
	v_pk_fma_f32 v[80:81], v[88:89], v[80:81], v[92:93] op_sel_hi:[0,1,0]
	v_ashrrev_i32_e32 v117, 31, v116
	v_pk_mul_f32 v[72:73], v[68:69], v[72:73]
	v_lshlrev_b32_e32 v68, 16, v115
	v_and_b32_e32 v69, 0xffff0000, v115
	v_pk_fma_f32 v[68:69], v[86:87], v[68:69], v[90:91] op_sel_hi:[0,1,0]
	v_min_f32_e32 v86, 0x42700000, v82
	v_pk_mul_f32 v[82:83], v[70:71], v[84:85] op_sel_hi:[1,0]
	v_pk_mul_f32 v[68:69], v[74:75], v[68:69]
	v_min_f32_e32 v87, 0x42700000, v83
	v_min_f32_e32 v84, 0x42700000, v82
	v_exp_f32_e32 v82, v86
	v_exp_f32_e32 v83, v85
	v_exp_f32_e32 v84, v84
	v_exp_f32_e32 v85, v87
	v_pk_mul_f32 v[70:71], v[70:71], v[80:81]
	v_pk_add_f32 v[82:83], v[82:83], 1.0 op_sel_hi:[1,0]
	v_lshlrev_b64 v[114:115], 12, v[120:121]
	v_pk_add_f32 v[84:85], v[84:85], 1.0 op_sel_hi:[1,0]
	v_lshlrev_b64 v[112:113], 12, v[116:117]
	v_pk_mul_f32 v[86:87], v[82:83], v[84:85]
	v_pk_mul_f32 v[68:69], v[68:69], v[84:85]
	s_mov_b32 s11, 0x358637bd
	v_pk_fma_f32 v[68:69], v[70:71], v[82:83], v[68:69]
	v_rcp_f32_e32 v70, v86
	v_rcp_f32_e32 v71, v87
	s_nop 0
	v_pk_mul_f32 v[74:75], v[68:69], v[70:71]
	v_cvt_pk_bf16_f32 v68, v76, v77
	v_cvt_pk_bf16_f32 v69, v78, v79
	v_cvt_pk_bf16_f32 v70, v72, v73
	v_lshl_add_u64 v[72:73], s[4:5], 0, v[196:197]
	v_lshl_add_u64 v[72:73], v[72:73], 0, v[188:189]
	v_cvt_pk_bf16_f32 v71, v74, v75
	global_store_dwordx4 v[72:73], v[68:71], off
	s_nop 1
	v_lshlrev_b64 v[68:69], 6, v[130:131]
	v_lshl_add_u64 v[68:69], s[44:45], 0, v[68:69]
	global_load_dwordx4 v[126:129], v[68:69], off
	v_lshl_add_u64 v[68:69], v[192:193], 0, v[122:123]
	global_load_dwordx4 v[108:111], v[68:69], off
	v_lshl_add_u64 v[68:69], v[194:195], 0, v[122:123]
	global_load_dwordx4 v[104:107], v[68:69], off
	v_lshlrev_b64 v[68:69], 6, v[124:125]
	v_lshl_add_u64 v[68:69], s[44:45], 0, v[68:69]
	global_load_dwordx4 v[100:103], v[68:69], off
	v_lshl_add_u64 v[68:69], v[192:193], 0, v[118:119]
	global_load_dwordx4 v[96:99], v[68:69], off
	v_lshl_add_u64 v[68:69], v[194:195], 0, v[118:119]
	global_load_dwordx4 v[92:95], v[68:69], off
	v_lshlrev_b64 v[68:69], 6, v[120:121]
	v_lshl_add_u64 v[68:69], s[44:45], 0, v[68:69]
	global_load_dwordx4 v[88:91], v[68:69], off
	v_lshl_add_u64 v[68:69], v[192:193], 0, v[114:115]
	global_load_dwordx4 v[84:87], v[68:69], off
	v_lshl_add_u64 v[68:69], v[194:195], 0, v[114:115]
	global_load_dwordx4 v[80:83], v[68:69], off
	v_lshlrev_b64 v[68:69], 6, v[116:117]
	v_lshl_add_u64 v[68:69], s[44:45], 0, v[68:69]
	global_load_dwordx4 v[76:79], v[68:69], off
	v_lshl_add_u64 v[68:69], v[192:193], 0, v[112:113]
	v_and_b32_e32 v117, 0xcf, v130
	global_load_dwordx4 v[72:75], v[68:69], off
	v_lshl_add_u64 v[68:69], v[194:195], 0, v[112:113]
	v_lshl_add_u32 v117, v117, 2, s9
	global_load_dwordx4 v[68:71], v[68:69], off
	v_mov_b32_e32 v117, v229
	s_waitcnt vmcnt(11)
	v_ldexp_f32 v121, v126, -9
	v_ldexp_f32 v126, v127, -9
	v_ldexp_f32 v125, v128, -9
	v_fma_f32 v126, -v121, v121, v126
	v_ldexp_f32 v127, v129, -9
	v_max_f32_e32 v126, 0, v126
	v_fma_f32 v127, -v125, v125, v127
	v_add_f32_e32 v126, s11, v126
	v_max_f32_e32 v127, 0, v127
	v_rsq_f32_e32 v126, v126
	v_add_f32_e32 v127, s11, v127
	v_rsq_f32_e32 v127, v127
	s_waitcnt vmcnt(10)
	v_lshlrev_b32_e32 v136, 16, v108
	s_waitcnt lgkmcnt(0)
	v_mul_f32_e32 v128, v117, v126
	v_mul_f32_e32 v126, 0xbfb8aa3b, v117
	v_pk_mul_f32 v[140:141], v[64:65], v[126:127] op_sel_hi:[1,0]
	v_and_b32_e32 v137, 0xffff0000, v108
	s_waitcnt vmcnt(9)
;     __device__ __forceinline__ void operator()(const f32x4 (&acc)[2][2][4][2], const Unit& u, int wr, int wc, int fr, int fq) const {
;     ...
;             for (int m = 0; m < 4; ++m) { const int row = row0 + ai * HALF + m * 16; const float r = tab[u.idx * 256 + (row & 255)];
;                 const f32x4 st = stv[m];
;                 const float muf = __builtin_amdgcn_ldexpf(st[0], -9), mub = __builtin_amdgcn_ldexpf(st[2], -9); float eps = 1e-6f; asm volatile("" : "+s"(eps));
;                 const float rf = __builtin_amdgcn_rsqf(fmaxf(__builtin_amdgcn_ldexpf(st[1], -9) - muf * muf, 0.f) + eps), rb = __builtin_amdgcn_rsqf(fmaxf(__builtin_amdgcn_ldexpf(st[3], -9) - mub * mub, 0.f) + eps);
;                 const float cf = rf * r, cb = rb * r, df = -muf * cf, db = -mub * cb, kr = -1.4426950409f * r;
;                 const u32x4 yfw = yfv[m], ybw = ybv[m];
;                 float o[8];
; #pragma unroll
;                 for (int n = 0; n < 2; ++n)
; #pragma unroll
;                     for (int e = 0; e < 4; e += 2) { const int q = n * 4 + e; const unsigned wf = yfw[q >> 1], wb = ybw[q >> 1];
;                         const f32x2 yf2 = {__builtin_bit_cast(float, wf << 16), __builtin_bit_cast(float, wf & 0xffff0000u)}, yb2 = {__builtin_bit_cast(float, wb << 16), __builtin_bit_cast(float, wb & 0xffff0000u)};
;                         const f32x2 af = {acc[ai][0][m][n][e], acc[ai][0][m][n][e + 1]}, ab = {acc[ai][1][m][n][e], acc[ai][1][m][n][e + 1]};
;                         const f32x2 nf = yf2 * cf + df, nb = yb2 * cb + db;
;                         const f32x2 xf = __builtin_elementwise_min(af * kr, (f32x2){60.f, 60.f}), xb = __builtin_elementwise_min(ab * kr, (f32x2){60.f, 60.f});
;                         const f32x2 pf = (f32x2){__builtin_amdgcn_exp2f(xf[0]), __builtin_amdgcn_exp2f(xf[1])} + 1.0f, pb = (f32x2){__builtin_amdgcn_exp2f(xb[0]), __builtin_amdgcn_exp2f(xb[1])} + 1.0f;
;                         const f32x2 den = pf * pb, num = (af * nf) * pb + (ab * nb) * pf;
;                         const f32x2 res = num * (f32x2){__builtin_amdgcn_rcpf(den[0]), __builtin_amdgcn_rcpf(den[1])};
;                         o[q] = res[0]; o[q + 1] = res[1]; }
;                 u32x4 w; w.x = cvt_pk_bf16(o[0], o[1]); w.y = cvt_pk_bf16(o[2], o[3]); w.z = cvt_pk_bf16(o[4], o[5]); w.w = cvt_pk_bf16(o[6], o[7]);
	v_lshlrev_b32_e32 v138, 16, v104
	v_and_b32_e32 v139, 0xffff0000, v104
	v_min_f32_e32 v104, 0x42700000, v141
	v_min_f32_e32 v108, 0x42700000, v140
	v_pk_mul_f32 v[140:141], v[60:61], v[126:127] op_sel_hi:[1,0]
	v_mul_f32_e32 v130, v117, v127
	v_mul_f32_e64 v132, v128, -v121
	v_min_f32_e32 v117, 0x42700000, v141
	v_min_f32_e32 v121, 0x42700000, v140
	v_exp_f32_e32 v140, v108
	v_exp_f32_e32 v141, v104
	v_exp_f32_e32 v142, v121
	v_exp_f32_e32 v143, v117
	v_mul_f32_e64 v134, v130, -v125
	v_pk_fma_f32 v[136:137], v[128:129], v[136:137], v[132:133] op_sel_hi:[0,1,0]
	v_pk_fma_f32 v[138:139], v[130:131], v[138:139], v[134:135] op_sel_hi:[0,1,0]
	v_pk_add_f32 v[140:141], v[140:141], 1.0 op_sel_hi:[1,0]
	v_pk_add_f32 v[142:143], v[142:143], 1.0 op_sel_hi:[1,0]
	v_pk_mul_f32 v[64:65], v[64:65], v[136:137]
	v_pk_mul_f32 v[144:145], v[140:141], v[142:143]
	v_pk_mul_f32 v[64:65], v[64:65], v[142:143]
	v_pk_mul_f32 v[60:61], v[60:61], v[138:139]
	v_lshlrev_b32_e32 v104, 16, v105
	v_pk_fma_f32 v[60:61], v[60:61], v[140:141], v[64:65]
	v_rcp_f32_e32 v64, v144
	v_rcp_f32_e32 v65, v145
	v_and_b32_e32 v105, 0xffff0000, v105
	v_pk_fma_f32 v[104:105], v[130:131], v[104:105], v[134:135] op_sel_hi:[0,1,0]
	s_mov_b32 s11, 0x358637bd
	v_pk_mul_f32 v[60:61], v[60:61], v[64:65]
	v_lshlrev_b32_e32 v64, 16, v109
	v_and_b32_e32 v65, 0xffff0000, v109
	v_pk_mul_f32 v[108:109], v[66:67], v[126:127] op_sel_hi:[1,0]
	v_pk_fma_f32 v[64:65], v[128:129], v[64:65], v[132:133] op_sel_hi:[0,1,0]
	v_min_f32_e32 v117, 0x42700000, v109
	v_min_f32_e32 v121, 0x42700000, v108
	v_pk_mul_f32 v[108:109], v[62:63], v[126:127] op_sel_hi:[1,0]
	v_pk_mul_f32 v[64:65], v[66:67], v[64:65]
	v_min_f32_e32 v125, 0x42700000, v109
	v_min_f32_e32 v127, 0x42700000, v108
	v_exp_f32_e32 v108, v121
	v_exp_f32_e32 v109, v117
	v_exp_f32_e32 v136, v127
	v_exp_f32_e32 v137, v125
	v_pk_mul_f32 v[62:63], v[62:63], v[104:105]
	v_pk_add_f32 v[108:109], v[108:109], 1.0 op_sel_hi:[1,0]
	v_pk_mul_f32 v[104:105], v[56:57], v[126:127] op_sel_hi:[1,0]
	v_pk_add_f32 v[136:137], v[136:137], 1.0 op_sel_hi:[1,0]
	v_lshlrev_b32_e32 v66, 16, v106
	v_pk_mul_f32 v[138:139], v[108:109], v[136:137]
	v_pk_mul_f32 v[64:65], v[64:65], v[136:137]
	v_and_b32_e32 v67, 0xffff0000, v106
	v_pk_fma_f32 v[62:63], v[62:63], v[108:109], v[64:65]
	v_rcp_f32_e32 v64, v138
	v_rcp_f32_e32 v65, v139
	v_min_f32_e32 v106, 0x42700000, v105
	v_min_f32_e32 v108, 0x42700000, v104
	v_pk_mul_f32 v[104:105], v[52:53], v[126:127] op_sel_hi:[1,0]
	v_pk_mul_f32 v[62:63], v[62:63], v[64:65]
	v_lshlrev_b32_e32 v64, 16, v110
	v_and_b32_e32 v65, 0xffff0000, v110
	v_min_f32_e32 v109, 0x42700000, v105
	v_min_f32_e32 v110, 0x42700000, v104
	v_exp_f32_e32 v104, v108
	v_exp_f32_e32 v105, v106
	v_exp_f32_e32 v108, v110
	v_exp_f32_e32 v109, v109
	v_pk_fma_f32 v[64:65], v[128:129], v[64:65], v[132:133] op_sel_hi:[0,1,0]
	v_pk_fma_f32 v[66:67], v[130:131], v[66:67], v[134:135] op_sel_hi:[0,1,0]
	v_pk_add_f32 v[104:105], v[104:105], 1.0 op_sel_hi:[1,0]
	v_pk_add_f32 v[108:109], v[108:109], 1.0 op_sel_hi:[1,0]
	v_pk_mul_f32 v[56:57], v[56:57], v[64:65]
	v_pk_mul_f32 v[136:137], v[104:105], v[108:109]
	v_pk_mul_f32 v[56:57], v[56:57], v[108:109]
	v_pk_mul_f32 v[52:53], v[52:53], v[66:67]
	v_pk_mul_f32 v[66:67], v[58:59], v[126:127] op_sel_hi:[1,0]
	v_pk_fma_f32 v[52:53], v[52:53], v[104:105], v[56:57]
	v_rcp_f32_e32 v56, v136
	v_rcp_f32_e32 v57, v137
	v_min_f32_e32 v104, 0x42700000, v67
	v_min_f32_e32 v105, 0x42700000, v66
	v_pk_mul_f32 v[66:67], v[54:55], v[126:127] op_sel_hi:[1,0]
	v_lshlrev_b32_e32 v64, 16, v107
	v_and_b32_e32 v65, 0xffff0000, v107
	v_min_f32_e32 v106, 0x42700000, v67
	v_min_f32_e32 v107, 0x42700000, v66
	v_exp_f32_e32 v66, v105
	v_exp_f32_e32 v67, v104
	v_exp_f32_e32 v104, v107
	v_exp_f32_e32 v105, v106
	v_pk_mul_f32 v[56:57], v[52:53], v[56:57]
	v_lshlrev_b32_e32 v52, 16, v111
	v_and_b32_e32 v53, 0xffff0000, v111
	v_pk_fma_f32 v[52:53], v[128:129], v[52:53], v[132:133] op_sel_hi:[0,1,0]
	v_pk_fma_f32 v[64:65], v[130:131], v[64:65], v[134:135] op_sel_hi:[0,1,0]
	v_pk_add_f32 v[66:67], v[66:67], 1.0 op_sel_hi:[1,0]
	v_pk_add_f32 v[104:105], v[104:105], 1.0 op_sel_hi:[1,0]
	v_pk_mul_f32 v[52:53], v[58:59], v[52:53]
	v_pk_mul_f32 v[106:107], v[66:67], v[104:105]
	v_pk_mul_f32 v[52:53], v[52:53], v[104:105]
	v_pk_mul_f32 v[54:55], v[54:55], v[64:65]
	s_waitcnt vmcnt(6)
	v_lshlrev_b32_e32 v64, 16, v92
	v_pk_fma_f32 v[52:53], v[54:55], v[66:67], v[52:53]
	v_rcp_f32_e32 v54, v106
	v_rcp_f32_e32 v55, v107
	v_and_b32_e32 v65, 0xffff0000, v92
	v_pk_mul_f32 v[58:59], v[52:53], v[54:55]
	v_cvt_pk_bf16_f32 v52, v60, v61
	v_cvt_pk_bf16_f32 v53, v62, v63
	v_cvt_pk_bf16_f32 v54, v56, v57
	v_lshl_add_u64 v[56:57], s[4:5], 0, v[122:123]
	v_cvt_pk_bf16_f32 v55, v58, v59
	v_lshl_add_u64 v[56:57], v[56:57], 0, v[188:189]
	global_store_dwordx4 v[56:57], v[52:55], off
	v_ldexp_f32 v56, v103, -9
	v_lshlrev_b32_e32 v62, 16, v96
	v_ldexp_f32 v53, v100, -9
	v_ldexp_f32 v55, v102, -9
	v_ldexp_f32 v54, v101, -9
	v_and_b32_e32 v52, 0xdf, v124
	v_fma_f32 v54, -v53, v53, v54
	v_fma_f32 v56, -v55, v55, v56
	v_lshl_add_u32 v52, v52, 2, s9
	v_max_f32_e32 v54, 0, v54
	v_max_f32_e32 v56, 0, v56
	v_mov_b32_e32 v52, v230
	v_and_b32_e32 v63, 0xffff0000, v96
	v_add_f32_e32 v54, s11, v54
	v_add_f32_e32 v56, s11, v56
	v_rsq_f32_e32 v54, v54
	v_rsq_f32_e32 v56, v56
	s_mov_b32 s11, 0x358637bd
	s_waitcnt lgkmcnt(0)
;     __device__ __forceinline__ void operator()(const f32x4 (&acc)[2][2][4][2], const Unit& u, int wr, int wc, int fr, int fq) const {
;     ...
;             for (int m = 0; m < 4; ++m) { const int row = row0 + ai * HALF + m * 16; const float r = tab[u.idx * 256 + (row & 255)];
;                 const f32x4 st = stv[m];
;                 const float muf = __builtin_amdgcn_ldexpf(st[0], -9), mub = __builtin_amdgcn_ldexpf(st[2], -9); float eps = 1e-6f; asm volatile("" : "+s"(eps));
;                 const float rf = __builtin_amdgcn_rsqf(fmaxf(__builtin_amdgcn_ldexpf(st[1], -9) - muf * muf, 0.f) + eps), rb = __builtin_amdgcn_rsqf(fmaxf(__builtin_amdgcn_ldexpf(st[3], -9) - mub * mub, 0.f) + eps);
;                 const float cf = rf * r, cb = rb * r, df = -muf * cf, db = -mub * cb, kr = -1.4426950409f * r;
;                 const u32x4 yfw = yfv[m], ybw = ybv[m];
;                 float o[8];
; #pragma unroll
;                 for (int n = 0; n < 2; ++n)
; #pragma unroll
;                     for (int e = 0; e < 4; e += 2) { const int q = n * 4 + e; const unsigned wf = yfw[q >> 1], wb = ybw[q >> 1];
;                         const f32x2 yf2 = {__builtin_bit_cast(float, wf << 16), __builtin_bit_cast(float, wf & 0xffff0000u)}, yb2 = {__builtin_bit_cast(float, wb << 16), __builtin_bit_cast(float, wb & 0xffff0000u)};
;                         const f32x2 af = {acc[ai][0][m][n][e], acc[ai][0][m][n][e + 1]}, ab = {acc[ai][1][m][n][e], acc[ai][1][m][n][e + 1]};
;                         const f32x2 nf = yf2 * cf + df, nb = yb2 * cb + db;
;                         const f32x2 xf = __builtin_elementwise_min(af * kr, (f32x2){60.f, 60.f}), xb = __builtin_elementwise_min(ab * kr, (f32x2){60.f, 60.f});
;                         const f32x2 pf = (f32x2){__builtin_amdgcn_exp2f(xf[0]), __builtin_amdgcn_exp2f(xf[1])} + 1.0f, pb = (f32x2){__builtin_amdgcn_exp2f(xb[0]), __builtin_amdgcn_exp2f(xb[1])} + 1.0f;
;                         const f32x2 den = pf * pb, num = (af * nf) * pb + (ab * nb) * pf;
;                         const f32x2 res = num * (f32x2){__builtin_amdgcn_rcpf(den[0]), __builtin_amdgcn_rcpf(den[1])};
;                         o[q] = res[0]; o[q + 1] = res[1]; }
;                 u32x4 w; w.x = cvt_pk_bf16(o[0], o[1]); w.y = cvt_pk_bf16(o[2], o[3]); w.z = cvt_pk_bf16(o[4], o[5]); w.w = cvt_pk_bf16(o[6], o[7]);
	v_mul_f32_e32 v54, v52, v54
	v_mul_f32_e32 v56, v52, v56
	v_mul_f32_e32 v52, 0xbfb8aa3b, v52
	v_pk_mul_f32 v[66:67], v[48:49], v[52:53] op_sel_hi:[1,0]
	v_mul_f32_e64 v58, v54, -v53
	v_min_f32_e32 v53, 0x42700000, v67
	v_mul_f32_e64 v60, v56, -v55
	v_pk_fma_f32 v[62:63], v[54:55], v[62:63], v[58:59] op_sel_hi:[0,1,0]
	v_min_f32_e32 v55, 0x42700000, v66
	v_pk_mul_f32 v[66:67], v[44:45], v[52:53] op_sel_hi:[1,0]
	v_pk_fma_f32 v[64:65], v[56:57], v[64:65], v[60:61] op_sel_hi:[0,1,0]
	v_min_f32_e32 v57, 0x42700000, v67
	v_min_f32_e32 v59, 0x42700000, v66
	v_exp_f32_e32 v66, v55
	v_exp_f32_e32 v67, v53
	v_exp_f32_e32 v100, v59
	v_exp_f32_e32 v101, v57
	v_pk_mul_f32 v[48:49], v[48:49], v[62:63]
	v_pk_add_f32 v[66:67], v[66:67], 1.0 op_sel_hi:[1,0]
	v_pk_mul_f32 v[44:45], v[44:45], v[64:65]
	v_pk_add_f32 v[100:101], v[100:101], 1.0 op_sel_hi:[1,0]
	v_pk_mul_f32 v[64:65], v[50:51], v[52:53] op_sel_hi:[1,0]
	v_pk_mul_f32 v[102:103], v[66:67], v[100:101]
	v_pk_mul_f32 v[48:49], v[48:49], v[100:101]
	v_min_f32_e32 v53, 0x42700000, v65
	v_pk_fma_f32 v[44:45], v[44:45], v[66:67], v[48:49]
	v_rcp_f32_e32 v48, v102
	v_rcp_f32_e32 v49, v103
	v_lshlrev_b32_e32 v62, 16, v93
	v_and_b32_e32 v63, 0xffff0000, v93
	v_pk_fma_f32 v[62:63], v[56:57], v[62:63], v[60:61] op_sel_hi:[0,1,0]
	v_pk_mul_f32 v[44:45], v[44:45], v[48:49]
	v_lshlrev_b32_e32 v48, 16, v97
	v_and_b32_e32 v49, 0xffff0000, v97
	v_pk_fma_f32 v[48:49], v[54:55], v[48:49], v[58:59] op_sel_hi:[0,1,0]
	v_min_f32_e32 v55, 0x42700000, v64
	v_pk_mul_f32 v[64:65], v[46:47], v[52:53] op_sel_hi:[1,0]
	v_pk_mul_f32 v[48:49], v[50:51], v[48:49]
	v_min_f32_e32 v57, 0x42700000, v65
	v_min_f32_e32 v59, 0x42700000, v64
	v_exp_f32_e32 v64, v55
	v_exp_f32_e32 v65, v53
	v_exp_f32_e32 v66, v59
	v_exp_f32_e32 v67, v57
	v_pk_mul_f32 v[46:47], v[46:47], v[62:63]
	v_pk_add_f32 v[64:65], v[64:65], 1.0 op_sel_hi:[1,0]
	v_pk_mul_f32 v[62:63], v[40:41], v[52:53] op_sel_hi:[1,0]
	v_pk_add_f32 v[66:67], v[66:67], 1.0 op_sel_hi:[1,0]
	v_min_f32_e32 v53, 0x42700000, v63
	v_pk_mul_f32 v[92:93], v[64:65], v[66:67]
	v_pk_mul_f32 v[48:49], v[48:49], v[66:67]
	v_lshlrev_b32_e32 v50, 16, v94
	v_pk_fma_f32 v[46:47], v[46:47], v[64:65], v[48:49]
	v_rcp_f32_e32 v48, v92
	v_rcp_f32_e32 v49, v93
	v_and_b32_e32 v51, 0xffff0000, v94
	v_pk_fma_f32 v[50:51], v[56:57], v[50:51], v[60:61] op_sel_hi:[0,1,0]
	v_pk_mul_f32 v[46:47], v[46:47], v[48:49]
	v_lshlrev_b32_e32 v48, 16, v98
	v_and_b32_e32 v49, 0xffff0000, v98
	v_pk_fma_f32 v[48:49], v[54:55], v[48:49], v[58:59] op_sel_hi:[0,1,0]
	v_min_f32_e32 v55, 0x42700000, v62
	v_pk_mul_f32 v[62:63], v[36:37], v[52:53] op_sel_hi:[1,0]
	v_pk_mul_f32 v[40:41], v[40:41], v[48:49]
	v_min_f32_e32 v57, 0x42700000, v63
	v_min_f32_e32 v59, 0x42700000, v62
	v_exp_f32_e32 v62, v55
	v_exp_f32_e32 v63, v53
	v_exp_f32_e32 v64, v59
	v_exp_f32_e32 v65, v57
	v_pk_mul_f32 v[36:37], v[36:37], v[50:51]
	v_pk_add_f32 v[62:63], v[62:63], 1.0 op_sel_hi:[1,0]
	v_pk_mul_f32 v[50:51], v[42:43], v[52:53] op_sel_hi:[1,0]
	v_pk_add_f32 v[64:65], v[64:65], 1.0 op_sel_hi:[1,0]
	v_min_f32_e32 v53, 0x42700000, v51
	v_pk_mul_f32 v[66:67], v[62:63], v[64:65]
	v_pk_mul_f32 v[40:41], v[40:41], v[64:65]
	v_lshlrev_b32_e32 v48, 16, v95
	v_pk_fma_f32 v[36:37], v[36:37], v[62:63], v[40:41]
	v_rcp_f32_e32 v40, v66
	v_rcp_f32_e32 v41, v67
	v_and_b32_e32 v49, 0xffff0000, v95
	v_pk_fma_f32 v[48:49], v[56:57], v[48:49], v[60:61] op_sel_hi:[0,1,0]
	v_pk_mul_f32 v[40:41], v[36:37], v[40:41]
	v_lshlrev_b32_e32 v36, 16, v99
	v_and_b32_e32 v37, 0xffff0000, v99
	v_pk_fma_f32 v[36:37], v[54:55], v[36:37], v[58:59] op_sel_hi:[0,1,0]
	v_min_f32_e32 v54, 0x42700000, v50
	v_pk_mul_f32 v[50:51], v[38:39], v[52:53] op_sel_hi:[1,0]
	v_pk_mul_f32 v[36:37], v[42:43], v[36:37]
	v_min_f32_e32 v55, 0x42700000, v51
	v_min_f32_e32 v52, 0x42700000, v50
	v_exp_f32_e32 v50, v54
	v_exp_f32_e32 v51, v53
	v_exp_f32_e32 v52, v52
	v_exp_f32_e32 v53, v55
	v_pk_mul_f32 v[38:39], v[38:39], v[48:49]
	v_pk_add_f32 v[50:51], v[50:51], 1.0 op_sel_hi:[1,0]
	s_waitcnt vmcnt(4)
	v_lshlrev_b32_e32 v48, 16, v80
	v_pk_add_f32 v[52:53], v[52:53], 1.0 op_sel_hi:[1,0]
	v_and_b32_e32 v49, 0xffff0000, v80
	v_pk_mul_f32 v[54:55], v[50:51], v[52:53]
	v_pk_mul_f32 v[36:37], v[36:37], v[52:53]
	s_nop 0
	v_pk_fma_f32 v[36:37], v[38:39], v[50:51], v[36:37]
	v_rcp_f32_e32 v38, v54
	v_rcp_f32_e32 v39, v55
	s_nop 0
	v_pk_mul_f32 v[42:43], v[36:37], v[38:39]
	v_cvt_pk_bf16_f32 v36, v44, v45
	v_cvt_pk_bf16_f32 v37, v46, v47
	v_cvt_pk_bf16_f32 v38, v40, v41
	v_lshl_add_u64 v[40:41], s[4:5], 0, v[118:119]
	v_cvt_pk_bf16_f32 v39, v42, v43
	v_lshl_add_u64 v[40:41], v[40:41], 0, v[188:189]
	global_store_dwordx4 v[40:41], v[36:39], off
	v_ldexp_f32 v40, v91, -9
	v_lshlrev_b32_e32 v46, 16, v84
	v_ldexp_f32 v37, v88, -9
	v_ldexp_f32 v39, v90, -9
	v_ldexp_f32 v38, v89, -9
	v_and_b32_e32 v36, 0xef, v120
	v_fma_f32 v38, -v37, v37, v38
	v_fma_f32 v40, -v39, v39, v40
	v_lshl_add_u32 v36, v36, 2, s9
	v_max_f32_e32 v38, 0, v38
	v_max_f32_e32 v40, 0, v40
	v_mov_b32_e32 v36, v231
	v_and_b32_e32 v47, 0xffff0000, v84
	v_add_f32_e32 v38, s11, v38
	v_add_f32_e32 v40, s11, v40
	v_rsq_f32_e32 v38, v38
	v_rsq_f32_e32 v40, v40
	s_waitcnt lgkmcnt(0)
;     __device__ __forceinline__ void operator()(const f32x4 (&acc)[2][2][4][2], const Unit& u, int wr, int wc, int fr, int fq) const {
;     ...
;             for (int m = 0; m < 4; ++m) { const int row = row0 + ai * HALF + m * 16; const float r = tab[u.idx * 256 + (row & 255)];
;                 const f32x4 st = stv[m];
;                 const float muf = __builtin_amdgcn_ldexpf(st[0], -9), mub = __builtin_amdgcn_ldexpf(st[2], -9); float eps = 1e-6f; asm volatile("" : "+s"(eps));
;                 const float rf = __builtin_amdgcn_rsqf(fmaxf(__builtin_amdgcn_ldexpf(st[1], -9) - muf * muf, 0.f) + eps), rb = __builtin_amdgcn_rsqf(fmaxf(__builtin_amdgcn_ldexpf(st[3], -9) - mub * mub, 0.f) + eps);
;                 const float cf = rf * r, cb = rb * r, df = -muf * cf, db = -mub * cb, kr = -1.4426950409f * r;
;                 const u32x4 yfw = yfv[m], ybw = ybv[m];
;                 float o[8];
; #pragma unroll
;                 for (int n = 0; n < 2; ++n)
; #pragma unroll
;                     for (int e = 0; e < 4; e += 2) { const int q = n * 4 + e; const unsigned wf = yfw[q >> 1], wb = ybw[q >> 1];
;                         const f32x2 yf2 = {__builtin_bit_cast(float, wf << 16), __builtin_bit_cast(float, wf & 0xffff0000u)}, yb2 = {__builtin_bit_cast(float, wb << 16), __builtin_bit_cast(float, wb & 0xffff0000u)};
;                         const f32x2 af = {acc[ai][0][m][n][e], acc[ai][0][m][n][e + 1]}, ab = {acc[ai][1][m][n][e], acc[ai][1][m][n][e + 1]};
;                         const f32x2 nf = yf2 * cf + df, nb = yb2 * cb + db;
;                         const f32x2 xf = __builtin_elementwise_min(af * kr, (f32x2){60.f, 60.f}), xb = __builtin_elementwise_min(ab * kr, (f32x2){60.f, 60.f});
;                         const f32x2 pf = (f32x2){__builtin_amdgcn_exp2f(xf[0]), __builtin_amdgcn_exp2f(xf[1])} + 1.0f, pb = (f32x2){__builtin_amdgcn_exp2f(xb[0]), __builtin_amdgcn_exp2f(xb[1])} + 1.0f;
;                         const f32x2 den = pf * pb, num = (af * nf) * pb + (ab * nb) * pf;
;                         const f32x2 res = num * (f32x2){__builtin_amdgcn_rcpf(den[0]), __builtin_amdgcn_rcpf(den[1])};
;                         o[q] = res[0]; o[q + 1] = res[1]; }
;                 u32x4 w; w.x = cvt_pk_bf16(o[0], o[1]); w.y = cvt_pk_bf16(o[2], o[3]); w.z = cvt_pk_bf16(o[4], o[5]); w.w = cvt_pk_bf16(o[6], o[7]);
	v_mul_f32_e32 v38, v36, v38
	v_mul_f32_e32 v40, v36, v40
	v_mul_f32_e32 v36, 0xbfb8aa3b, v36
	v_pk_mul_f32 v[50:51], v[32:33], v[36:37] op_sel_hi:[1,0]
	v_mul_f32_e64 v42, v38, -v37
	v_min_f32_e32 v37, 0x42700000, v51
	v_mul_f32_e64 v44, v40, -v39
	v_pk_fma_f32 v[46:47], v[38:39], v[46:47], v[42:43] op_sel_hi:[0,1,0]
	v_min_f32_e32 v39, 0x42700000, v50
	v_pk_mul_f32 v[50:51], v[28:29], v[36:37] op_sel_hi:[1,0]
	v_pk_fma_f32 v[48:49], v[40:41], v[48:49], v[44:45] op_sel_hi:[0,1,0]
	v_min_f32_e32 v41, 0x42700000, v51
	v_min_f32_e32 v43, 0x42700000, v50
	v_exp_f32_e32 v50, v39
	v_exp_f32_e32 v51, v37
	v_exp_f32_e32 v52, v43
	v_exp_f32_e32 v53, v41
	v_pk_mul_f32 v[32:33], v[32:33], v[46:47]
	v_pk_add_f32 v[50:51], v[50:51], 1.0 op_sel_hi:[1,0]
	v_pk_mul_f32 v[28:29], v[28:29], v[48:49]
	v_pk_add_f32 v[52:53], v[52:53], 1.0 op_sel_hi:[1,0]
	v_pk_mul_f32 v[48:49], v[34:35], v[36:37] op_sel_hi:[1,0]
	v_pk_mul_f32 v[54:55], v[50:51], v[52:53]
	v_pk_mul_f32 v[32:33], v[32:33], v[52:53]
	v_min_f32_e32 v37, 0x42700000, v49
	v_pk_fma_f32 v[28:29], v[28:29], v[50:51], v[32:33]
	v_rcp_f32_e32 v32, v54
	v_rcp_f32_e32 v33, v55
	v_lshlrev_b32_e32 v46, 16, v81
	v_and_b32_e32 v47, 0xffff0000, v81
	v_pk_fma_f32 v[46:47], v[40:41], v[46:47], v[44:45] op_sel_hi:[0,1,0]
	v_pk_mul_f32 v[28:29], v[28:29], v[32:33]
	v_lshlrev_b32_e32 v32, 16, v85
	v_and_b32_e32 v33, 0xffff0000, v85
	v_pk_fma_f32 v[32:33], v[38:39], v[32:33], v[42:43] op_sel_hi:[0,1,0]
	v_min_f32_e32 v39, 0x42700000, v48
	v_pk_mul_f32 v[48:49], v[30:31], v[36:37] op_sel_hi:[1,0]
	v_pk_mul_f32 v[32:33], v[34:35], v[32:33]
	v_min_f32_e32 v41, 0x42700000, v49
	v_min_f32_e32 v43, 0x42700000, v48
	v_exp_f32_e32 v48, v39
	v_exp_f32_e32 v49, v37
	v_exp_f32_e32 v50, v43
	v_exp_f32_e32 v51, v41
	v_pk_mul_f32 v[30:31], v[30:31], v[46:47]
	v_pk_add_f32 v[48:49], v[48:49], 1.0 op_sel_hi:[1,0]
	v_pk_mul_f32 v[46:47], v[24:25], v[36:37] op_sel_hi:[1,0]
	v_pk_add_f32 v[50:51], v[50:51], 1.0 op_sel_hi:[1,0]
	v_min_f32_e32 v37, 0x42700000, v47
	v_pk_mul_f32 v[52:53], v[48:49], v[50:51]
	v_pk_mul_f32 v[32:33], v[32:33], v[50:51]
	v_lshlrev_b32_e32 v34, 16, v82
	v_pk_fma_f32 v[30:31], v[30:31], v[48:49], v[32:33]
	v_rcp_f32_e32 v32, v52
	v_rcp_f32_e32 v33, v53
	v_and_b32_e32 v35, 0xffff0000, v82
	v_pk_fma_f32 v[34:35], v[40:41], v[34:35], v[44:45] op_sel_hi:[0,1,0]
	v_pk_mul_f32 v[30:31], v[30:31], v[32:33]
	v_lshlrev_b32_e32 v32, 16, v86
	v_and_b32_e32 v33, 0xffff0000, v86
	v_pk_fma_f32 v[32:33], v[38:39], v[32:33], v[42:43] op_sel_hi:[0,1,0]
	v_min_f32_e32 v39, 0x42700000, v46
	v_pk_mul_f32 v[46:47], v[20:21], v[36:37] op_sel_hi:[1,0]
	v_pk_mul_f32 v[24:25], v[24:25], v[32:33]
	v_min_f32_e32 v41, 0x42700000, v47
	v_min_f32_e32 v43, 0x42700000, v46
	v_exp_f32_e32 v46, v39
	v_exp_f32_e32 v47, v37
	v_exp_f32_e32 v48, v43
	v_exp_f32_e32 v49, v41
	v_pk_mul_f32 v[20:21], v[20:21], v[34:35]
	v_pk_add_f32 v[46:47], v[46:47], 1.0 op_sel_hi:[1,0]
	v_pk_mul_f32 v[34:35], v[26:27], v[36:37] op_sel_hi:[1,0]
	v_pk_add_f32 v[48:49], v[48:49], 1.0 op_sel_hi:[1,0]
	v_min_f32_e32 v37, 0x42700000, v35
	v_pk_mul_f32 v[50:51], v[46:47], v[48:49]
	v_pk_mul_f32 v[24:25], v[24:25], v[48:49]
	v_lshlrev_b32_e32 v32, 16, v83
	v_pk_fma_f32 v[20:21], v[20:21], v[46:47], v[24:25]
	v_rcp_f32_e32 v24, v50
	v_rcp_f32_e32 v25, v51
	v_and_b32_e32 v33, 0xffff0000, v83
	v_pk_fma_f32 v[32:33], v[40:41], v[32:33], v[44:45] op_sel_hi:[0,1,0]
	v_pk_mul_f32 v[24:25], v[20:21], v[24:25]
	v_lshlrev_b32_e32 v20, 16, v87
	v_and_b32_e32 v21, 0xffff0000, v87
	v_pk_fma_f32 v[20:21], v[38:39], v[20:21], v[42:43] op_sel_hi:[0,1,0]
	v_min_f32_e32 v38, 0x42700000, v34
	v_pk_mul_f32 v[34:35], v[22:23], v[36:37] op_sel_hi:[1,0]
	v_pk_mul_f32 v[20:21], v[26:27], v[20:21]
	v_min_f32_e32 v39, 0x42700000, v35
	v_min_f32_e32 v36, 0x42700000, v34
	v_exp_f32_e32 v34, v38
	v_exp_f32_e32 v35, v37
	v_exp_f32_e32 v36, v36
	v_exp_f32_e32 v37, v39
	v_pk_mul_f32 v[22:23], v[22:23], v[32:33]
	v_pk_add_f32 v[34:35], v[34:35], 1.0 op_sel_hi:[1,0]
	s_waitcnt vmcnt(2)
	v_lshlrev_b32_e32 v32, 16, v68
	v_pk_add_f32 v[36:37], v[36:37], 1.0 op_sel_hi:[1,0]
	v_and_b32_e32 v33, 0xffff0000, v68
	v_pk_mul_f32 v[38:39], v[34:35], v[36:37]
	v_pk_mul_f32 v[20:21], v[20:21], v[36:37]
	s_nop 0
	v_pk_fma_f32 v[20:21], v[22:23], v[34:35], v[20:21]
	v_rcp_f32_e32 v22, v38
	v_rcp_f32_e32 v23, v39
	s_nop 0
	v_pk_mul_f32 v[26:27], v[20:21], v[22:23]
	v_cvt_pk_bf16_f32 v20, v28, v29
	v_cvt_pk_bf16_f32 v21, v30, v31
	v_cvt_pk_bf16_f32 v22, v24, v25
	v_lshl_add_u64 v[24:25], s[4:5], 0, v[114:115]
	v_cvt_pk_bf16_f32 v23, v26, v27
	v_lshl_add_u64 v[24:25], v[24:25], 0, v[188:189]
	global_store_dwordx4 v[24:25], v[20:23], off
	v_ldexp_f32 v24, v79, -9
	v_lshlrev_b32_e32 v30, 16, v72
	v_ldexp_f32 v21, v76, -9
	v_ldexp_f32 v23, v78, -9
	v_ldexp_f32 v22, v77, -9
	v_and_b32_e32 v20, 0xff, v116
	v_fma_f32 v22, -v21, v21, v22
	v_fma_f32 v24, -v23, v23, v24
	v_lshl_add_u32 v20, v20, 2, s9
	s_mov_b32 s9, 0x358637bd
	v_max_f32_e32 v22, 0, v22
	v_max_f32_e32 v24, 0, v24
	v_mov_b32_e32 v20, v232
	v_and_b32_e32 v31, 0xffff0000, v72
	v_add_f32_e32 v22, s9, v22
	v_add_f32_e32 v24, s9, v24
	v_rsq_f32_e32 v22, v22
	v_rsq_f32_e32 v24, v24
	s_waitcnt lgkmcnt(0)
;     __device__ __forceinline__ void operator()(const f32x4 (&acc)[2][2][4][2], const Unit& u, int wr, int wc, int fr, int fq) const {
;     ...
;             for (int m = 0; m < 4; ++m) { const int row = row0 + ai * HALF + m * 16; const float r = tab[u.idx * 256 + (row & 255)];
;                 const f32x4 st = stv[m];
;                 const float muf = __builtin_amdgcn_ldexpf(st[0], -9), mub = __builtin_amdgcn_ldexpf(st[2], -9); float eps = 1e-6f; asm volatile("" : "+s"(eps));
;                 const float rf = __builtin_amdgcn_rsqf(fmaxf(__builtin_amdgcn_ldexpf(st[1], -9) - muf * muf, 0.f) + eps), rb = __builtin_amdgcn_rsqf(fmaxf(__builtin_amdgcn_ldexpf(st[3], -9) - mub * mub, 0.f) + eps);
;                 const float cf = rf * r, cb = rb * r, df = -muf * cf, db = -mub * cb, kr = -1.4426950409f * r;
;                 const u32x4 yfw = yfv[m], ybw = ybv[m];
;                 float o[8];
; #pragma unroll
;                 for (int n = 0; n < 2; ++n)
; #pragma unroll
;                     for (int e = 0; e < 4; e += 2) { const int q = n * 4 + e; const unsigned wf = yfw[q >> 1], wb = ybw[q >> 1];
;                         const f32x2 yf2 = {__builtin_bit_cast(float, wf << 16), __builtin_bit_cast(float, wf & 0xffff0000u)}, yb2 = {__builtin_bit_cast(float, wb << 16), __builtin_bit_cast(float, wb & 0xffff0000u)};
;                         const f32x2 af = {acc[ai][0][m][n][e], acc[ai][0][m][n][e + 1]}, ab = {acc[ai][1][m][n][e], acc[ai][1][m][n][e + 1]};
;                         const f32x2 nf = yf2 * cf + df, nb = yb2 * cb + db;
;                         const f32x2 xf = __builtin_elementwise_min(af * kr, (f32x2){60.f, 60.f}), xb = __builtin_elementwise_min(ab * kr, (f32x2){60.f, 60.f});
;                         const f32x2 pf = (f32x2){__builtin_amdgcn_exp2f(xf[0]), __builtin_amdgcn_exp2f(xf[1])} + 1.0f, pb = (f32x2){__builtin_amdgcn_exp2f(xb[0]), __builtin_amdgcn_exp2f(xb[1])} + 1.0f;
;                         const f32x2 den = pf * pb, num = (af * nf) * pb + (ab * nb) * pf;
;                         const f32x2 res = num * (f32x2){__builtin_amdgcn_rcpf(den[0]), __builtin_amdgcn_rcpf(den[1])};
;                         o[q] = res[0]; o[q + 1] = res[1]; }
;                 u32x4 w; w.x = cvt_pk_bf16(o[0], o[1]); w.y = cvt_pk_bf16(o[2], o[3]); w.z = cvt_pk_bf16(o[4], o[5]); w.w = cvt_pk_bf16(o[6], o[7]);
	v_mul_f32_e32 v22, v20, v22
	v_mul_f32_e32 v24, v20, v24
	v_mul_f32_e32 v20, 0xbfb8aa3b, v20
	v_pk_mul_f32 v[34:35], v[16:17], v[20:21] op_sel_hi:[1,0]
	v_mul_f32_e64 v26, v22, -v21
	v_min_f32_e32 v21, 0x42700000, v35
	v_mul_f32_e64 v28, v24, -v23
	v_pk_fma_f32 v[30:31], v[22:23], v[30:31], v[26:27] op_sel_hi:[0,1,0]
	v_min_f32_e32 v23, 0x42700000, v34
	v_pk_mul_f32 v[34:35], v[12:13], v[20:21] op_sel_hi:[1,0]
	v_pk_fma_f32 v[32:33], v[24:25], v[32:33], v[28:29] op_sel_hi:[0,1,0]
	v_min_f32_e32 v25, 0x42700000, v35
	v_min_f32_e32 v27, 0x42700000, v34
	v_exp_f32_e32 v34, v23
	v_exp_f32_e32 v35, v21
	v_exp_f32_e32 v36, v27
	v_exp_f32_e32 v37, v25
	v_pk_mul_f32 v[16:17], v[16:17], v[30:31]
	v_pk_add_f32 v[34:35], v[34:35], 1.0 op_sel_hi:[1,0]
	v_pk_mul_f32 v[12:13], v[12:13], v[32:33]
	v_pk_add_f32 v[36:37], v[36:37], 1.0 op_sel_hi:[1,0]
	v_pk_mul_f32 v[32:33], v[18:19], v[20:21] op_sel_hi:[1,0]
	v_pk_mul_f32 v[38:39], v[34:35], v[36:37]
	v_pk_mul_f32 v[16:17], v[16:17], v[36:37]
	v_min_f32_e32 v21, 0x42700000, v33
	v_pk_fma_f32 v[12:13], v[12:13], v[34:35], v[16:17]
	v_rcp_f32_e32 v16, v38
	v_rcp_f32_e32 v17, v39
	v_lshlrev_b32_e32 v30, 16, v69
	v_and_b32_e32 v31, 0xffff0000, v69
	v_pk_fma_f32 v[30:31], v[24:25], v[30:31], v[28:29] op_sel_hi:[0,1,0]
	v_pk_mul_f32 v[12:13], v[12:13], v[16:17]
	v_lshlrev_b32_e32 v16, 16, v73
	v_and_b32_e32 v17, 0xffff0000, v73
	v_pk_fma_f32 v[16:17], v[22:23], v[16:17], v[26:27] op_sel_hi:[0,1,0]
	v_min_f32_e32 v23, 0x42700000, v32
	v_pk_mul_f32 v[32:33], v[14:15], v[20:21] op_sel_hi:[1,0]
	v_pk_mul_f32 v[16:17], v[18:19], v[16:17]
	v_min_f32_e32 v25, 0x42700000, v33
	v_min_f32_e32 v27, 0x42700000, v32
	v_exp_f32_e32 v32, v23
	v_exp_f32_e32 v33, v21
	v_exp_f32_e32 v34, v27
	v_exp_f32_e32 v35, v25
	v_pk_mul_f32 v[14:15], v[14:15], v[30:31]
	v_pk_add_f32 v[32:33], v[32:33], 1.0 op_sel_hi:[1,0]
	v_pk_mul_f32 v[30:31], v[8:9], v[20:21] op_sel_hi:[1,0]
	v_pk_add_f32 v[34:35], v[34:35], 1.0 op_sel_hi:[1,0]
	v_min_f32_e32 v21, 0x42700000, v31
	v_pk_mul_f32 v[36:37], v[32:33], v[34:35]
	v_pk_mul_f32 v[16:17], v[16:17], v[34:35]
	v_lshlrev_b32_e32 v18, 16, v70
	v_pk_fma_f32 v[14:15], v[14:15], v[32:33], v[16:17]
	v_rcp_f32_e32 v16, v36
	v_rcp_f32_e32 v17, v37
	v_and_b32_e32 v19, 0xffff0000, v70
	v_pk_fma_f32 v[18:19], v[24:25], v[18:19], v[28:29] op_sel_hi:[0,1,0]
	v_pk_mul_f32 v[14:15], v[14:15], v[16:17]
	v_lshlrev_b32_e32 v16, 16, v74
	v_and_b32_e32 v17, 0xffff0000, v74
	v_pk_fma_f32 v[16:17], v[22:23], v[16:17], v[26:27] op_sel_hi:[0,1,0]
	v_min_f32_e32 v23, 0x42700000, v30
	v_pk_mul_f32 v[30:31], v[4:5], v[20:21] op_sel_hi:[1,0]
	v_pk_mul_f32 v[8:9], v[8:9], v[16:17]
	v_min_f32_e32 v25, 0x42700000, v31
	v_min_f32_e32 v27, 0x42700000, v30
	v_exp_f32_e32 v30, v23
	v_exp_f32_e32 v31, v21
	v_exp_f32_e32 v32, v27
	v_exp_f32_e32 v33, v25
	v_pk_mul_f32 v[4:5], v[4:5], v[18:19]
	v_pk_add_f32 v[30:31], v[30:31], 1.0 op_sel_hi:[1,0]
	v_pk_mul_f32 v[18:19], v[10:11], v[20:21] op_sel_hi:[1,0]
	v_pk_add_f32 v[32:33], v[32:33], 1.0 op_sel_hi:[1,0]
	v_min_f32_e32 v21, 0x42700000, v19
	v_pk_mul_f32 v[34:35], v[30:31], v[32:33]
	v_pk_mul_f32 v[8:9], v[8:9], v[32:33]
	v_lshlrev_b32_e32 v16, 16, v71
	v_pk_fma_f32 v[4:5], v[4:5], v[30:31], v[8:9]
	v_rcp_f32_e32 v8, v34
	v_rcp_f32_e32 v9, v35
	v_and_b32_e32 v17, 0xffff0000, v71
	v_pk_fma_f32 v[16:17], v[24:25], v[16:17], v[28:29] op_sel_hi:[0,1,0]
	v_pk_mul_f32 v[8:9], v[4:5], v[8:9]
	v_lshlrev_b32_e32 v4, 16, v75
	v_and_b32_e32 v5, 0xffff0000, v75
	v_pk_fma_f32 v[4:5], v[22:23], v[4:5], v[26:27] op_sel_hi:[0,1,0]
	v_min_f32_e32 v22, 0x42700000, v18
	v_pk_mul_f32 v[18:19], v[6:7], v[20:21] op_sel_hi:[1,0]
	v_pk_mul_f32 v[4:5], v[10:11], v[4:5]
	v_min_f32_e32 v23, 0x42700000, v19
	v_min_f32_e32 v20, 0x42700000, v18
	v_exp_f32_e32 v18, v22
	v_exp_f32_e32 v19, v21
	v_exp_f32_e32 v20, v20
	v_exp_f32_e32 v21, v23
	v_pk_mul_f32 v[6:7], v[6:7], v[16:17]
	v_pk_add_f32 v[18:19], v[18:19], 1.0 op_sel_hi:[1,0]
	v_pk_add_f32 v[20:21], v[20:21], 1.0 op_sel_hi:[1,0]
	s_nop 0
	v_pk_mul_f32 v[22:23], v[18:19], v[20:21]
	v_pk_mul_f32 v[4:5], v[4:5], v[20:21]
	s_nop 0
	v_pk_fma_f32 v[4:5], v[6:7], v[18:19], v[4:5]
	v_rcp_f32_e32 v6, v22
	v_rcp_f32_e32 v7, v23
	s_nop 0
	v_pk_mul_f32 v[10:11], v[4:5], v[6:7]
	v_cvt_pk_bf16_f32 v4, v12, v13
	v_cvt_pk_bf16_f32 v5, v14, v15
	v_cvt_pk_bf16_f32 v6, v8, v9
	v_lshl_add_u64 v[8:9], s[4:5], 0, v[112:113]
	v_lshl_add_u64 v[8:9], v[8:9], 0, v[188:189]
	v_cvt_pk_bf16_f32 v7, v10, v11
	global_store_dwordx4 v[8:9], v[4:7], off
	s_cbranch_vccnz .LBB0_335
	s_andn2_b64 vcc, exec, s[0:1]
	s_cbranch_vccnz .LBB0_334
	s_barrier
	s_branch .LBB0_334

; __device__ __forceinline__ unsigned cvt_pk_bf16(float lo, float hi) { unsigned r; asm volatile("v_cvt_pk_bf16_f32 %0, %1, %2" : "=v"(r) : "v"(lo), "v"(hi)); return r; }
;     __device__ __forceinline__ void operator()(const f32x4 (&acc)[2][2][4][2], const Unit& u, int wr, int wc, int fr, int fq) const {
;     ...
;             for (int m = 0; m < 4; ++m) { const int row = row0 + ai * HALF + m * 16; bf16_t* rowp = O + (size_t)row * ldc + col0; const float r = tab[u.idx * 256 + (row & 255)];
;                 float o[8];
;                 const float kr = -1.4426950409f * r, r2 = r * r;
; #pragma unroll
;                 for (int n = 0; n < 2; ++n)
; #pragma unroll
;                     for (int e = 0; e < 4; e += 2) { const f32x2 g2 = {acc[ai][0][m][n][e], acc[ai][0][m][n][e + 1]}, u2 = {acc[ai][1][m][n][e], acc[ai][1][m][n][e + 1]};
;                         if (CHEAP) { const f32x2 p = g2 * u2 * r2; o[n * 4 + e] = p[0]; o[n * 4 + e + 1] = p[1]; }
;                         else { const f32x2 x = g2 * kr; const f32x2 d = (f32x2){__builtin_amdgcn_exp2f(x[0]), __builtin_amdgcn_exp2f(x[1])} + 1.0f;
;                             const f32x2 rc = (f32x2){__builtin_amdgcn_rcpf(d[0]), __builtin_amdgcn_rcpf(d[1])} * r2; const f32x2 p = (g2 * u2) * rc; o[n * 4 + e] = p[0]; o[n * 4 + e + 1] = p[1]; } }
;                 u32x4 w; w.x = cvt_pk_bf16(o[0], o[1]); w.y = cvt_pk_bf16(o[2], o[3]); w.z = cvt_pk_bf16(o[4], o[5]); w.w = cvt_pk_bf16(o[6], o[7]);
;                 if (CHEAP == 2) { if (w.x == 0x12345678u && w.y == w.z) *(u32x4*)rowp = w; } else *(u32x4*)rowp = w; }
.LBB0_730:
	s_lshl_b32 s9, s58, 10
	s_add_i32 s9, s9, 0
	s_add_i32 s9, s9, 0x20000
	v_lshl_add_u32 v156, v152, 2, s9
	ds_read_b32 v157, v156
	ds_read_b32 v241, v156 offset:64
	ds_read_b32 v242, v156 offset:128
	ds_read_b32 v243, v156 offset:192
	ds_read_b32 v244, v156 offset:512
	ds_read_b32 v245, v156 offset:576
	ds_read_b32 v246, v156 offset:640
	ds_read_b32 v247, v156 offset:704
	v_pk_mul_f32 v[124:125], v[128:129], v[124:125]
	v_pk_mul_f32 v[126:127], v[130:131], v[126:127]
	v_pk_mul_f32 v[116:117], v[120:121], v[116:117]
	v_lshl_or_b32 v146, s57, 7, v153
	s_waitcnt lgkmcnt(0)
	v_mul_f32_e32 v156, 0xbfb8aa3b, v157
	v_pk_mul_f32 v[160:161], v[128:129], v[156:157] op_sel_hi:[1,0]
	v_pk_mul_f32 v[128:129], v[130:131], v[156:157] op_sel_hi:[1,0]
	v_mul_f32_e32 v158, v157, v157
	v_exp_f32_e32 v128, v128
	v_exp_f32_e32 v129, v129
	v_exp_f32_e32 v160, v160
	v_exp_f32_e32 v161, v161
	v_lshl_add_u32 v155, s44, 8, v150
	v_pk_add_f32 v[128:129], v[128:129], 1.0 op_sel_hi:[1,0]
	v_ashrrev_i32_e32 v147, 31, v146
	v_rcp_f32_e32 v128, v128
	v_rcp_f32_e32 v129, v129
	v_pk_add_f32 v[160:161], v[160:161], 1.0 op_sel_hi:[1,0]
	v_mov_b64_e32 v[144:145], s[4:5]
	v_rcp_f32_e32 v160, v160
	v_pk_mul_f32 v[128:129], v[158:159], v[128:129] op_sel_hi:[0,1]
	v_pk_mul_f32 v[126:127], v[126:127], v[128:129]
	v_pk_mul_f32 v[128:129], v[120:121], v[156:157] op_sel_hi:[1,0]
	v_rcp_f32_e32 v161, v161
	v_exp_f32_e32 v128, v128
	v_exp_f32_e32 v129, v129
	s_movk_i32 s16, 0x1600
	v_pk_mul_f32 v[118:119], v[122:123], v[118:119]
	v_mad_i64_i32 v[148:149], s[36:37], v155, s16, v[144:145]
	v_pk_add_f32 v[128:129], v[128:129], 1.0 op_sel_hi:[1,0]
	v_pk_mul_f32 v[160:161], v[158:159], v[160:161] op_sel_hi:[0,1]
	v_rcp_f32_e32 v128, v128
	v_rcp_f32_e32 v129, v129
	v_pk_mul_f32 v[124:125], v[124:125], v[160:161]
	v_pk_mul_f32 v[108:109], v[112:113], v[108:109]
	v_pk_mul_f32 v[110:111], v[114:115], v[110:111]
	v_pk_mul_f32 v[128:129], v[158:159], v[128:129] op_sel_hi:[0,1]
	v_pk_mul_f32 v[120:121], v[116:117], v[128:129]
	v_pk_mul_f32 v[116:117], v[122:123], v[156:157] op_sel_hi:[1,0]
	v_pk_mul_f32 v[100:101], v[104:105], v[100:101]
	v_exp_f32_e32 v116, v116
	v_exp_f32_e32 v117, v117
	v_pk_mul_f32 v[102:103], v[106:107], v[102:103]
	s_movk_i32 s11, 0xef
	v_pk_mul_f32 v[92:93], v[96:97], v[92:93]
	v_pk_add_f32 v[116:117], v[116:117], 1.0 op_sel_hi:[1,0]
	v_pk_mul_f32 v[94:95], v[98:99], v[94:95]
	v_rcp_f32_e32 v116, v116
	v_rcp_f32_e32 v117, v117
	v_pk_mul_f32 v[84:85], v[88:89], v[84:85]
	v_pk_mul_f32 v[86:87], v[90:91], v[86:87]
	v_pk_mul_f32 v[76:77], v[80:81], v[76:77]
	v_pk_mul_f32 v[116:117], v[158:159], v[116:117] op_sel_hi:[0,1]
	v_pk_mul_f32 v[122:123], v[118:119], v[116:117]
	v_lshlrev_b64 v[116:117], 1, v[146:147]
	v_lshl_add_u64 v[128:129], v[148:149], 0, v[116:117]
	v_cvt_pk_bf16_f32 v118, v124, v125
	v_cvt_pk_bf16_f32 v119, v126, v127
	v_cvt_pk_bf16_f32 v120, v120, v121
	v_cvt_pk_bf16_f32 v121, v122, v123
	global_store_dwordx4 v[128:129], v[118:121], off
	v_pk_mul_f32 v[78:79], v[82:83], v[78:79]
	v_pk_mul_f32 v[68:69], v[72:73], v[68:69]
	v_bitop3_b32 v120, v155, s71, 16 bitop3:0xc8
	v_lshl_add_u32 v120, v120, 2, s9
	v_mov_b32_e32 v121, v241
	v_or_b32_e32 v118, 16, v155
	v_mad_i64_i32 v[118:119], s[36:37], v118, s16, v[144:145]
	v_pk_mul_f32 v[70:71], v[74:75], v[70:71]
	s_waitcnt lgkmcnt(0)
	v_mul_f32_e32 v120, 0xbfb8aa3b, v121
	v_pk_mul_f32 v[124:125], v[112:113], v[120:121] op_sel_hi:[1,0]
	v_pk_mul_f32 v[112:113], v[114:115], v[120:121] op_sel_hi:[1,0]
	v_mul_f32_e32 v122, v121, v121
	v_exp_f32_e32 v112, v112
	v_exp_f32_e32 v113, v113
	v_exp_f32_e32 v124, v124
	v_exp_f32_e32 v125, v125
	v_pk_mul_f32 v[60:61], v[64:65], v[60:61]
	v_pk_add_f32 v[112:113], v[112:113], 1.0 op_sel_hi:[1,0]
	v_pk_mul_f32 v[62:63], v[66:67], v[62:63]
	v_rcp_f32_e32 v112, v112
	v_rcp_f32_e32 v113, v113
	v_pk_add_f32 v[124:125], v[124:125], 1.0 op_sel_hi:[1,0]
	v_pk_mul_f32 v[52:53], v[56:57], v[52:53]
	v_rcp_f32_e32 v124, v124
	v_pk_mul_f32 v[112:113], v[122:123], v[112:113] op_sel_hi:[0,1]
	v_pk_mul_f32 v[110:111], v[110:111], v[112:113]
	v_pk_mul_f32 v[112:113], v[104:105], v[120:121] op_sel_hi:[1,0]
	v_rcp_f32_e32 v125, v125
	v_exp_f32_e32 v112, v112
	v_exp_f32_e32 v113, v113
	v_pk_mul_f32 v[54:55], v[58:59], v[54:55]
	v_pk_mul_f32 v[124:125], v[122:123], v[124:125] op_sel_hi:[0,1]
	v_pk_mul_f32 v[108:109], v[108:109], v[124:125]
	v_pk_add_f32 v[112:113], v[112:113], 1.0 op_sel_hi:[1,0]
	v_pk_mul_f32 v[44:45], v[48:49], v[44:45]
	v_rcp_f32_e32 v112, v112
	v_rcp_f32_e32 v113, v113
	v_pk_mul_f32 v[46:47], v[50:51], v[46:47]
	v_pk_mul_f32 v[36:37], v[40:41], v[36:37]
	v_pk_mul_f32 v[38:39], v[42:43], v[38:39]
	v_pk_mul_f32 v[112:113], v[122:123], v[112:113] op_sel_hi:[0,1]
	v_pk_mul_f32 v[104:105], v[100:101], v[112:113]
	v_pk_mul_f32 v[100:101], v[106:107], v[120:121] op_sel_hi:[1,0]
	v_lshl_add_u64 v[112:113], v[118:119], 0, v[116:117]
	v_exp_f32_e32 v100, v100
	v_exp_f32_e32 v101, v101
	v_pk_mul_f32 v[28:29], v[32:33], v[28:29]
	v_pk_mul_f32 v[30:31], v[34:35], v[30:31]
	v_pk_mul_f32 v[20:21], v[24:25], v[20:21]
	v_pk_add_f32 v[100:101], v[100:101], 1.0 op_sel_hi:[1,0]
	v_pk_mul_f32 v[22:23], v[26:27], v[22:23]
	v_rcp_f32_e32 v100, v100
	v_rcp_f32_e32 v101, v101
	v_pk_mul_f32 v[12:13], v[16:17], v[12:13]
	v_pk_mul_f32 v[14:15], v[18:19], v[14:15]
	v_pk_mul_f32 v[4:5], v[8:9], v[4:5]
	v_pk_mul_f32 v[100:101], v[122:123], v[100:101] op_sel_hi:[0,1]
	v_pk_mul_f32 v[106:107], v[102:103], v[100:101]
	v_cvt_pk_bf16_f32 v100, v108, v109
	v_cvt_pk_bf16_f32 v101, v110, v111
	v_cvt_pk_bf16_f32 v102, v104, v105
	v_pk_mul_f32 v[6:7], v[10:11], v[6:7]
	v_cvt_pk_bf16_f32 v103, v106, v107
	global_store_dwordx4 v[112:113], v[100:103], off
	s_andn2_b64 vcc, exec, s[2:3]
	s_nop 0
	v_bitop3_b32 v102, v155, s11, 32 bitop3:0xc8
	v_lshl_add_u32 v102, v102, 2, s9
	v_mov_b32_e32 v103, v242
	v_or_b32_e32 v100, 32, v155
	v_mad_i64_i32 v[100:101], s[36:37], v100, s16, v[144:145]
	s_waitcnt lgkmcnt(0)
; __device__ __forceinline__ unsigned cvt_pk_bf16(float lo, float hi) { unsigned r; asm volatile("v_cvt_pk_bf16_f32 %0, %1, %2" : "=v"(r) : "v"(lo), "v"(hi)); return r; }
;     __device__ __forceinline__ void operator()(const f32x4 (&acc)[2][2][4][2], const Unit& u, int wr, int wc, int fr, int fq) const {
;     ...
;             for (int m = 0; m < 4; ++m) { const int row = row0 + ai * HALF + m * 16; bf16_t* rowp = O + (size_t)row * ldc + col0; const float r = tab[u.idx * 256 + (row & 255)];
;                 float o[8];
;                 const float kr = -1.4426950409f * r, r2 = r * r;
; #pragma unroll
;                 for (int n = 0; n < 2; ++n)
; #pragma unroll
;                     for (int e = 0; e < 4; e += 2) { const f32x2 g2 = {acc[ai][0][m][n][e], acc[ai][0][m][n][e + 1]}, u2 = {acc[ai][1][m][n][e], acc[ai][1][m][n][e + 1]};
;                         if (CHEAP) { const f32x2 p = g2 * u2 * r2; o[n * 4 + e] = p[0]; o[n * 4 + e + 1] = p[1]; }
;                         else { const f32x2 x = g2 * kr; const f32x2 d = (f32x2){__builtin_amdgcn_exp2f(x[0]), __builtin_amdgcn_exp2f(x[1])} + 1.0f;
;                             const f32x2 rc = (f32x2){__builtin_amdgcn_rcpf(d[0]), __builtin_amdgcn_rcpf(d[1])} * r2; const f32x2 p = (g2 * u2) * rc; o[n * 4 + e] = p[0]; o[n * 4 + e + 1] = p[1]; } }
;                 u32x4 w; w.x = cvt_pk_bf16(o[0], o[1]); w.y = cvt_pk_bf16(o[2], o[3]); w.z = cvt_pk_bf16(o[4], o[5]); w.w = cvt_pk_bf16(o[6], o[7]);
;                 if (CHEAP == 2) { if (w.x == 0x12345678u && w.y == w.z) *(u32x4*)rowp = w; } else *(u32x4*)rowp = w; }
	v_mul_f32_e32 v102, 0xbfb8aa3b, v103
	v_pk_mul_f32 v[106:107], v[96:97], v[102:103] op_sel_hi:[1,0]
	v_pk_mul_f32 v[96:97], v[98:99], v[102:103] op_sel_hi:[1,0]
	v_mul_f32_e32 v104, v103, v103
	v_exp_f32_e32 v96, v96
	v_exp_f32_e32 v97, v97
	v_exp_f32_e32 v106, v106
	v_exp_f32_e32 v107, v107
	v_pk_add_f32 v[96:97], v[96:97], 1.0 op_sel_hi:[1,0]
	s_nop 0
	v_rcp_f32_e32 v96, v96
	v_rcp_f32_e32 v97, v97
	v_pk_add_f32 v[106:107], v[106:107], 1.0 op_sel_hi:[1,0]
	v_pk_mul_f32 v[96:97], v[104:105], v[96:97] op_sel_hi:[0,1]
	v_pk_mul_f32 v[94:95], v[94:95], v[96:97]
	v_pk_mul_f32 v[96:97], v[88:89], v[102:103] op_sel_hi:[1,0]
	v_rcp_f32_e32 v106, v106
	v_exp_f32_e32 v96, v96
	v_exp_f32_e32 v97, v97
	v_rcp_f32_e32 v107, v107
	v_pk_add_f32 v[96:97], v[96:97], 1.0 op_sel_hi:[1,0]
	s_nop 0
	v_rcp_f32_e32 v96, v96
	v_rcp_f32_e32 v97, v97
	v_pk_mul_f32 v[106:107], v[104:105], v[106:107] op_sel_hi:[0,1]
	v_pk_mul_f32 v[92:93], v[92:93], v[106:107]
	v_pk_mul_f32 v[96:97], v[104:105], v[96:97] op_sel_hi:[0,1]
	v_pk_mul_f32 v[88:89], v[84:85], v[96:97]
	v_pk_mul_f32 v[84:85], v[90:91], v[102:103] op_sel_hi:[1,0]
	v_lshl_add_u64 v[96:97], v[100:101], 0, v[116:117]
	v_exp_f32_e32 v84, v84
	v_exp_f32_e32 v85, v85
	s_nop 0
	v_pk_add_f32 v[84:85], v[84:85], 1.0 op_sel_hi:[1,0]
	s_nop 0
	v_rcp_f32_e32 v84, v84
	v_rcp_f32_e32 v85, v85
	s_nop 0
	v_pk_mul_f32 v[84:85], v[104:105], v[84:85] op_sel_hi:[0,1]
	v_pk_mul_f32 v[90:91], v[86:87], v[84:85]
	v_cvt_pk_bf16_f32 v84, v92, v93
	v_cvt_pk_bf16_f32 v85, v94, v95
	v_cvt_pk_bf16_f32 v86, v88, v89
	s_nop 0
	v_cvt_pk_bf16_f32 v87, v90, v91
	global_store_dwordx4 v[96:97], v[84:87], off
	s_nop 1
	v_bitop3_b32 v86, v155, s70, 48 bitop3:0xc8
	v_lshl_add_u32 v86, v86, 2, s9
	v_mov_b32_e32 v87, v243
	v_or_b32_e32 v84, 48, v155
	v_mad_i64_i32 v[84:85], s[36:37], v84, s16, v[144:145]
	s_waitcnt lgkmcnt(0)
	v_mul_f32_e32 v86, 0xbfb8aa3b, v87
	v_pk_mul_f32 v[90:91], v[80:81], v[86:87] op_sel_hi:[1,0]
	v_pk_mul_f32 v[80:81], v[82:83], v[86:87] op_sel_hi:[1,0]
	v_mul_f32_e32 v88, v87, v87
	v_exp_f32_e32 v80, v80
	v_exp_f32_e32 v81, v81
	v_exp_f32_e32 v90, v90
	v_exp_f32_e32 v91, v91
	v_pk_add_f32 v[80:81], v[80:81], 1.0 op_sel_hi:[1,0]
	s_nop 0
	v_rcp_f32_e32 v80, v80
	v_rcp_f32_e32 v81, v81
	v_pk_add_f32 v[90:91], v[90:91], 1.0 op_sel_hi:[1,0]
	v_pk_mul_f32 v[80:81], v[88:89], v[80:81] op_sel_hi:[0,1]
	v_pk_mul_f32 v[78:79], v[78:79], v[80:81]
	v_pk_mul_f32 v[80:81], v[72:73], v[86:87] op_sel_hi:[1,0]
	v_rcp_f32_e32 v90, v90
	v_exp_f32_e32 v80, v80
	v_exp_f32_e32 v81, v81
	v_rcp_f32_e32 v91, v91
	v_pk_add_f32 v[80:81], v[80:81], 1.0 op_sel_hi:[1,0]
	s_nop 0
	v_rcp_f32_e32 v80, v80
	v_rcp_f32_e32 v81, v81
	v_pk_mul_f32 v[90:91], v[88:89], v[90:91] op_sel_hi:[0,1]
	v_pk_mul_f32 v[76:77], v[76:77], v[90:91]
	v_pk_mul_f32 v[80:81], v[88:89], v[80:81] op_sel_hi:[0,1]
	v_pk_mul_f32 v[72:73], v[68:69], v[80:81]
	v_pk_mul_f32 v[68:69], v[74:75], v[86:87] op_sel_hi:[1,0]
	v_lshl_add_u64 v[80:81], v[84:85], 0, v[116:117]
	v_exp_f32_e32 v68, v68
	v_exp_f32_e32 v69, v69
	s_nop 0
	v_pk_add_f32 v[68:69], v[68:69], 1.0 op_sel_hi:[1,0]
	s_nop 0
	v_rcp_f32_e32 v68, v68
	v_rcp_f32_e32 v69, v69
	s_nop 0
	v_pk_mul_f32 v[68:69], v[88:89], v[68:69] op_sel_hi:[0,1]
	v_pk_mul_f32 v[74:75], v[70:71], v[68:69]
	v_cvt_pk_bf16_f32 v68, v76, v77
	v_cvt_pk_bf16_f32 v69, v78, v79
	v_cvt_pk_bf16_f32 v70, v72, v73
	s_nop 0
	v_cvt_pk_bf16_f32 v71, v74, v75
	global_store_dwordx4 v[80:81], v[68:71], off
	s_nop 1
	v_add_u32_e32 v70, 0x80, v155
	v_mad_i64_i32 v[68:69], s[36:37], v70, s16, v[144:145]
	v_and_b32_e32 v70, 0xcf, v70
	v_lshl_add_u32 v70, v70, 2, s9
	v_mov_b32_e32 v71, v244
	s_waitcnt lgkmcnt(0)
	v_mul_f32_e32 v70, 0xbfb8aa3b, v71
	v_pk_mul_f32 v[74:75], v[64:65], v[70:71] op_sel_hi:[1,0]
	v_pk_mul_f32 v[64:65], v[66:67], v[70:71] op_sel_hi:[1,0]
	v_mul_f32_e32 v72, v71, v71
	v_exp_f32_e32 v64, v64
	v_exp_f32_e32 v65, v65
	v_exp_f32_e32 v74, v74
	v_exp_f32_e32 v75, v75
	v_pk_add_f32 v[64:65], v[64:65], 1.0 op_sel_hi:[1,0]
	s_nop 0
	v_rcp_f32_e32 v64, v64
	v_rcp_f32_e32 v65, v65
	v_pk_add_f32 v[74:75], v[74:75], 1.0 op_sel_hi:[1,0]
	v_pk_mul_f32 v[64:65], v[72:73], v[64:65] op_sel_hi:[0,1]
	v_pk_mul_f32 v[62:63], v[62:63], v[64:65]
	v_pk_mul_f32 v[64:65], v[56:57], v[70:71] op_sel_hi:[1,0]
	v_rcp_f32_e32 v74, v74
	v_exp_f32_e32 v64, v64
	v_exp_f32_e32 v65, v65
	v_rcp_f32_e32 v75, v75
	v_pk_add_f32 v[64:65], v[64:65], 1.0 op_sel_hi:[1,0]
	s_nop 0
	v_rcp_f32_e32 v64, v64
	v_rcp_f32_e32 v65, v65
	v_pk_mul_f32 v[74:75], v[72:73], v[74:75] op_sel_hi:[0,1]
	v_pk_mul_f32 v[60:61], v[60:61], v[74:75]
	v_pk_mul_f32 v[64:65], v[72:73], v[64:65] op_sel_hi:[0,1]
	v_pk_mul_f32 v[56:57], v[52:53], v[64:65]
	v_pk_mul_f32 v[52:53], v[58:59], v[70:71] op_sel_hi:[1,0]
	v_lshl_add_u64 v[64:65], v[68:69], 0, v[116:117]
	v_exp_f32_e32 v52, v52
	v_exp_f32_e32 v53, v53
	s_nop 0
	v_pk_add_f32 v[52:53], v[52:53], 1.0 op_sel_hi:[1,0]
	s_nop 0
	v_rcp_f32_e32 v52, v52
	v_rcp_f32_e32 v53, v53
	s_nop 0
	v_pk_mul_f32 v[52:53], v[72:73], v[52:53] op_sel_hi:[0,1]
	v_pk_mul_f32 v[58:59], v[54:55], v[52:53]
	v_cvt_pk_bf16_f32 v52, v60, v61
	v_cvt_pk_bf16_f32 v53, v62, v63
	v_cvt_pk_bf16_f32 v54, v56, v57
	s_nop 0
	v_cvt_pk_bf16_f32 v55, v58, v59
	global_store_dwordx4 v[64:65], v[52:55], off
	s_nop 1
	v_add_u32_e32 v54, 0x90, v155
	v_mad_i64_i32 v[52:53], s[36:37], v54, s16, v[144:145]
	v_and_b32_e32 v54, 0xdf, v54
	v_lshl_add_u32 v54, v54, 2, s9
	v_mov_b32_e32 v55, v245
	s_waitcnt lgkmcnt(0)
; __device__ __forceinline__ unsigned cvt_pk_bf16(float lo, float hi) { unsigned r; asm volatile("v_cvt_pk_bf16_f32 %0, %1, %2" : "=v"(r) : "v"(lo), "v"(hi)); return r; }
;     __device__ __forceinline__ void operator()(const f32x4 (&acc)[2][2][4][2], const Unit& u, int wr, int wc, int fr, int fq) const {
;     ...
;             for (int m = 0; m < 4; ++m) { const int row = row0 + ai * HALF + m * 16; bf16_t* rowp = O + (size_t)row * ldc + col0; const float r = tab[u.idx * 256 + (row & 255)];
;                 float o[8];
;                 const float kr = -1.4426950409f * r, r2 = r * r;
; #pragma unroll
;                 for (int n = 0; n < 2; ++n)
; #pragma unroll
;                     for (int e = 0; e < 4; e += 2) { const f32x2 g2 = {acc[ai][0][m][n][e], acc[ai][0][m][n][e + 1]}, u2 = {acc[ai][1][m][n][e], acc[ai][1][m][n][e + 1]};
;                         if (CHEAP) { const f32x2 p = g2 * u2 * r2; o[n * 4 + e] = p[0]; o[n * 4 + e + 1] = p[1]; }
;                         else { const f32x2 x = g2 * kr; const f32x2 d = (f32x2){__builtin_amdgcn_exp2f(x[0]), __builtin_amdgcn_exp2f(x[1])} + 1.0f;
;                             const f32x2 rc = (f32x2){__builtin_amdgcn_rcpf(d[0]), __builtin_amdgcn_rcpf(d[1])} * r2; const f32x2 p = (g2 * u2) * rc; o[n * 4 + e] = p[0]; o[n * 4 + e + 1] = p[1]; } }
;                 u32x4 w; w.x = cvt_pk_bf16(o[0], o[1]); w.y = cvt_pk_bf16(o[2], o[3]); w.z = cvt_pk_bf16(o[4], o[5]); w.w = cvt_pk_bf16(o[6], o[7]);
;                 if (CHEAP == 2) { if (w.x == 0x12345678u && w.y == w.z) *(u32x4*)rowp = w; } else *(u32x4*)rowp = w; }
	v_mul_f32_e32 v54, 0xbfb8aa3b, v55
	v_pk_mul_f32 v[58:59], v[48:49], v[54:55] op_sel_hi:[1,0]
	v_pk_mul_f32 v[48:49], v[50:51], v[54:55] op_sel_hi:[1,0]
	v_mul_f32_e32 v56, v55, v55
	v_exp_f32_e32 v48, v48
	v_exp_f32_e32 v49, v49
	v_exp_f32_e32 v58, v58
	v_exp_f32_e32 v59, v59
	v_pk_add_f32 v[48:49], v[48:49], 1.0 op_sel_hi:[1,0]
	s_nop 0
	v_rcp_f32_e32 v48, v48
	v_rcp_f32_e32 v49, v49
	v_pk_add_f32 v[58:59], v[58:59], 1.0 op_sel_hi:[1,0]
	v_pk_mul_f32 v[48:49], v[56:57], v[48:49] op_sel_hi:[0,1]
	v_pk_mul_f32 v[46:47], v[46:47], v[48:49]
	v_pk_mul_f32 v[48:49], v[40:41], v[54:55] op_sel_hi:[1,0]
	v_rcp_f32_e32 v58, v58
	v_exp_f32_e32 v48, v48
	v_exp_f32_e32 v49, v49
	v_rcp_f32_e32 v59, v59
	v_pk_add_f32 v[48:49], v[48:49], 1.0 op_sel_hi:[1,0]
	s_nop 0
	v_rcp_f32_e32 v48, v48
	v_rcp_f32_e32 v49, v49
	v_pk_mul_f32 v[58:59], v[56:57], v[58:59] op_sel_hi:[0,1]
	v_pk_mul_f32 v[44:45], v[44:45], v[58:59]
	v_pk_mul_f32 v[48:49], v[56:57], v[48:49] op_sel_hi:[0,1]
	v_pk_mul_f32 v[40:41], v[36:37], v[48:49]
	v_pk_mul_f32 v[36:37], v[42:43], v[54:55] op_sel_hi:[1,0]
	v_lshl_add_u64 v[48:49], v[52:53], 0, v[116:117]
	v_exp_f32_e32 v36, v36
	v_exp_f32_e32 v37, v37
	s_nop 0
	v_pk_add_f32 v[36:37], v[36:37], 1.0 op_sel_hi:[1,0]
	s_nop 0
	v_rcp_f32_e32 v36, v36
	v_rcp_f32_e32 v37, v37
	s_nop 0
	v_pk_mul_f32 v[36:37], v[56:57], v[36:37] op_sel_hi:[0,1]
	v_pk_mul_f32 v[42:43], v[38:39], v[36:37]
	v_cvt_pk_bf16_f32 v36, v44, v45
	v_cvt_pk_bf16_f32 v37, v46, v47
	v_cvt_pk_bf16_f32 v38, v40, v41
	s_nop 0
	v_cvt_pk_bf16_f32 v39, v42, v43
	global_store_dwordx4 v[48:49], v[36:39], off
	s_nop 1
	v_add_u32_e32 v38, 0xa0, v155
	v_mad_i64_i32 v[36:37], s[36:37], v38, s16, v[144:145]
	v_and_b32_e32 v38, 0xef, v38
	v_lshl_add_u32 v38, v38, 2, s9
	v_mov_b32_e32 v39, v246
	s_waitcnt lgkmcnt(0)
	v_mul_f32_e32 v38, 0xbfb8aa3b, v39
	v_pk_mul_f32 v[42:43], v[32:33], v[38:39] op_sel_hi:[1,0]
	v_pk_mul_f32 v[32:33], v[34:35], v[38:39] op_sel_hi:[1,0]
	v_mul_f32_e32 v40, v39, v39
	v_exp_f32_e32 v32, v32
	v_exp_f32_e32 v33, v33
	v_exp_f32_e32 v42, v42
	v_exp_f32_e32 v43, v43
	v_pk_add_f32 v[32:33], v[32:33], 1.0 op_sel_hi:[1,0]
	s_nop 0
	v_rcp_f32_e32 v32, v32
	v_rcp_f32_e32 v33, v33
	v_pk_add_f32 v[42:43], v[42:43], 1.0 op_sel_hi:[1,0]
	v_pk_mul_f32 v[32:33], v[40:41], v[32:33] op_sel_hi:[0,1]
	v_pk_mul_f32 v[30:31], v[30:31], v[32:33]
	v_pk_mul_f32 v[32:33], v[24:25], v[38:39] op_sel_hi:[1,0]
	v_rcp_f32_e32 v42, v42
	v_exp_f32_e32 v32, v32
	v_exp_f32_e32 v33, v33
	v_rcp_f32_e32 v43, v43
	v_pk_add_f32 v[32:33], v[32:33], 1.0 op_sel_hi:[1,0]
	s_nop 0
	v_rcp_f32_e32 v32, v32
	v_rcp_f32_e32 v33, v33
	v_pk_mul_f32 v[42:43], v[40:41], v[42:43] op_sel_hi:[0,1]
	v_pk_mul_f32 v[28:29], v[28:29], v[42:43]
	v_pk_mul_f32 v[32:33], v[40:41], v[32:33] op_sel_hi:[0,1]
	v_pk_mul_f32 v[24:25], v[20:21], v[32:33]
	v_pk_mul_f32 v[20:21], v[26:27], v[38:39] op_sel_hi:[1,0]
	v_lshl_add_u64 v[32:33], v[36:37], 0, v[116:117]
	v_exp_f32_e32 v20, v20
	v_exp_f32_e32 v21, v21
	s_nop 0
	v_pk_add_f32 v[20:21], v[20:21], 1.0 op_sel_hi:[1,0]
	s_nop 0
	v_rcp_f32_e32 v20, v20
	v_rcp_f32_e32 v21, v21
	s_nop 0
	v_pk_mul_f32 v[20:21], v[40:41], v[20:21] op_sel_hi:[0,1]
	v_pk_mul_f32 v[26:27], v[22:23], v[20:21]
	v_cvt_pk_bf16_f32 v20, v28, v29
	v_cvt_pk_bf16_f32 v21, v30, v31
	v_cvt_pk_bf16_f32 v22, v24, v25
	s_nop 0
	v_cvt_pk_bf16_f32 v23, v26, v27
	global_store_dwordx4 v[32:33], v[20:23], off
	s_nop 1
	v_add_u32_e32 v22, 0xb0, v155
	v_mad_i64_i32 v[20:21], s[36:37], v22, s16, v[144:145]
	v_and_b32_e32 v22, 0xff, v22
	v_lshl_add_u32 v22, v22, 2, s9
	v_mov_b32_e32 v23, v247
	s_mov_b64 s[36:37], -1
	s_waitcnt lgkmcnt(0)
	v_mul_f32_e32 v22, 0xbfb8aa3b, v23
	v_pk_mul_f32 v[26:27], v[16:17], v[22:23] op_sel_hi:[1,0]
	v_pk_mul_f32 v[16:17], v[18:19], v[22:23] op_sel_hi:[1,0]
	v_mul_f32_e32 v24, v23, v23
	v_exp_f32_e32 v16, v16
	v_exp_f32_e32 v17, v17
	v_exp_f32_e32 v26, v26
	v_exp_f32_e32 v27, v27
	v_pk_add_f32 v[16:17], v[16:17], 1.0 op_sel_hi:[1,0]
	s_nop 0
	v_rcp_f32_e32 v16, v16
	v_rcp_f32_e32 v17, v17
	v_pk_add_f32 v[26:27], v[26:27], 1.0 op_sel_hi:[1,0]
	v_pk_mul_f32 v[16:17], v[24:25], v[16:17] op_sel_hi:[0,1]
	v_pk_mul_f32 v[14:15], v[14:15], v[16:17]
	v_pk_mul_f32 v[16:17], v[8:9], v[22:23] op_sel_hi:[1,0]
	v_rcp_f32_e32 v26, v26
	v_exp_f32_e32 v16, v16
	v_exp_f32_e32 v17, v17
	v_rcp_f32_e32 v27, v27
	v_pk_add_f32 v[16:17], v[16:17], 1.0 op_sel_hi:[1,0]
	s_nop 0
	v_rcp_f32_e32 v16, v16
	v_rcp_f32_e32 v17, v17
	v_pk_mul_f32 v[26:27], v[24:25], v[26:27] op_sel_hi:[0,1]
	v_pk_mul_f32 v[12:13], v[12:13], v[26:27]
	v_pk_mul_f32 v[16:17], v[24:25], v[16:17] op_sel_hi:[0,1]
	v_pk_mul_f32 v[8:9], v[4:5], v[16:17]
	v_pk_mul_f32 v[4:5], v[10:11], v[22:23] op_sel_hi:[1,0]
	v_lshl_add_u64 v[16:17], v[20:21], 0, v[116:117]
	v_exp_f32_e32 v4, v4
	v_exp_f32_e32 v5, v5
	s_nop 0
	v_pk_add_f32 v[4:5], v[4:5], 1.0 op_sel_hi:[1,0]
	s_nop 0
	v_rcp_f32_e32 v4, v4
	v_rcp_f32_e32 v5, v5
	s_nop 0
	v_pk_mul_f32 v[4:5], v[24:25], v[4:5] op_sel_hi:[0,1]
	v_pk_mul_f32 v[10:11], v[6:7], v[4:5]
	v_cvt_pk_bf16_f32 v4, v12, v13
	v_cvt_pk_bf16_f32 v5, v14, v15
	v_cvt_pk_bf16_f32 v6, v8, v9
	s_nop 0
	v_cvt_pk_bf16_f32 v7, v10, v11
	global_store_dwordx4 v[16:17], v[4:7], off
	s_cbranch_vccnz .LBB0_723
	s_andn2_b64 vcc, exec, s[0:1]
	s_cbranch_vccnz .LBB0_722
	s_barrier
	s_branch .LBB0_722
